# MLA + dilated attention: no wait between the alpha ds_write and the wave's own ds_reads (in-order LDS), counted waits in front of the rescale multiplies
# speedup vs baseline: 1.0132x; 1.0007x over previous
.LBB0_718:
	s_lshl_b32 s0, s3, 12
	s_sub_i32 s0, s89, s0
	v_add_u32_e32 v1, s0, v189
	v_add_u32_e32 v2, s0, v191
	ds_read_b128 v[172:175], v1 offset:36864
	ds_read_b128 v[164:167], v1 offset:38912
	ds_read_b128 v[176:179], v2 offset:36864
	ds_read_b128 v[168:171], v2 offset:38912
	ds_read_b128 v[156:159], v1 offset:40960
	ds_read_b128 v[4:7], v1 offset:43008
	ds_read_b128 v[160:163], v2 offset:40960
	ds_read_b128 v[8:11], v2 offset:43008
	s_nop 15
	s_nop 3
	s_nop 0
	v_mov_b32_e32 v1, v100
	v_mov_b32_e32 v2, v108
	v_max3_f32 v1, v1, v100, v116
	v_max3_f32 v1, v1, v101, v117
	v_max3_f32 v1, v1, v102, v118
	v_max3_f32 v1, v1, v103, v119
	v_max3_f32 v1, v1, v104, v120
	v_max3_f32 v1, v1, v105, v121
	v_max3_f32 v1, v1, v106, v122
	v_max3_f32 v1, v1, v107, v123
	v_max3_f32 v2, v2, v108, v124
	v_max3_f32 v2, v2, v109, v125
	v_max3_f32 v2, v2, v110, v126
	v_max3_f32 v2, v2, v111, v127
	v_max3_f32 v2, v2, v112, v128
	v_max3_f32 v2, v2, v113, v129
	v_max3_f32 v2, v2, v114, v130
	v_max3_f32 v2, v2, v115, v131
	s_nop 0
	v_max_f32_e32 v2, v2, v2
	v_max_f32_e32 v1, v1, v1
	v_max_f32_e32 v1, v1, v2
	v_mov_b32_e32 v2, v1
	s_nop 1
	v_permlane32_swap_b32_e32 v1, v2
	v_max3_f32 v2, v195, v1, v2
	v_sub_f32_e32 v1, v195, v2
	v_mul_f32_e32 v1, 0x3e000000, v1
	v_exp_f32_e32 v12, v1
	s_nop 0
	v_cmp_gt_f32_e32 vcc, 1.0, v12
	s_cbranch_vccz .LBB0_722
	s_and_saveexec_b64 s[0:1], s[8:9]
	ds_write_b32 v192, v12 offset:61440
	s_or_b64 exec, exec, s[0:1]
	ds_read_b128 v[12:15], v194 offset:61536
	ds_read_b128 v[196:199], v194 offset:61504
	ds_read_b128 v[200:203], v194 offset:61472
	ds_read_b128 v[204:207], v194 offset:61440
	s_waitcnt lgkmcnt(1)
	v_pk_mul_f32 v[80:81], v[80:81], v[12:13]
	v_pk_mul_f32 v[76:77], v[76:77], v[196:197]
	v_pk_mul_f32 v[72:73], v[72:73], v[200:201]
	v_pk_mul_f32 v[82:83], v[82:83], v[14:15]
	v_pk_mul_f32 v[78:79], v[78:79], v[198:199]
	v_pk_mul_f32 v[74:75], v[74:75], v[202:203]
	s_waitcnt lgkmcnt(0)
	v_pk_mul_f32 v[70:71], v[70:71], v[206:207]
	v_pk_mul_f32 v[68:69], v[68:69], v[204:205]
	v_pk_mul_f32 v[64:65], v[64:65], v[12:13]
	v_pk_mul_f32 v[60:61], v[60:61], v[196:197]
	v_pk_mul_f32 v[56:57], v[56:57], v[200:201]
	v_pk_mul_f32 v[66:67], v[66:67], v[14:15]
	v_pk_mul_f32 v[62:63], v[62:63], v[198:199]
	v_pk_mul_f32 v[58:59], v[58:59], v[202:203]
	v_pk_mul_f32 v[54:55], v[54:55], v[206:207]
	v_pk_mul_f32 v[52:53], v[52:53], v[204:205]
	v_pk_mul_f32 v[48:49], v[48:49], v[12:13]
	v_pk_mul_f32 v[44:45], v[44:45], v[196:197]
	v_pk_mul_f32 v[40:41], v[40:41], v[200:201]
	v_pk_mul_f32 v[50:51], v[50:51], v[14:15]
	v_pk_mul_f32 v[46:47], v[46:47], v[198:199]
	v_pk_mul_f32 v[42:43], v[42:43], v[202:203]
	v_pk_mul_f32 v[38:39], v[38:39], v[206:207]
	v_pk_mul_f32 v[36:37], v[36:37], v[204:205]
	v_pk_mul_f32 v[32:33], v[32:33], v[12:13]
	v_pk_mul_f32 v[28:29], v[28:29], v[196:197]
	v_pk_mul_f32 v[24:25], v[24:25], v[200:201]
	v_pk_mul_f32 v[34:35], v[34:35], v[14:15]
	v_pk_mul_f32 v[30:31], v[30:31], v[198:199]
	v_pk_mul_f32 v[26:27], v[26:27], v[202:203]
	v_pk_mul_f32 v[22:23], v[22:23], v[206:207]
	v_pk_mul_f32 v[20:21], v[20:21], v[204:205]
	v_pk_mul_f32 v[96:97], v[96:97], v[12:13]
	v_pk_mul_f32 v[92:93], v[92:93], v[196:197]
	v_pk_mul_f32 v[88:89], v[88:89], v[200:201]
	v_pk_mul_f32 v[98:99], v[98:99], v[14:15]
	v_pk_mul_f32 v[94:95], v[94:95], v[198:199]
	v_pk_mul_f32 v[90:91], v[90:91], v[202:203]
	v_pk_mul_f32 v[86:87], v[86:87], v[206:207]
	v_pk_mul_f32 v[84:85], v[84:85], v[204:205]

.LBB0_1227:
	s_ashr_i32 s2, s24, 7
	s_ashr_i32 s3, s2, 31
	s_mul_hi_i32 s0, s2, 0x2800000
	v_writelane_b32 v255, s2, 19
	s_mul_i32 s1, s2, 0x2800000
	s_add_u32 s1, s28, s1
	v_writelane_b32 v255, s3, 20
	s_addc_u32 s0, s29, s0
	s_and_b32 s2, s72, 0x1c0
	s_lshl_b32 s2, s2, 1
	s_add_u32 s22, s1, s2
	v_mov_b32_e32 v180, v0
	s_addc_u32 s23, s0, 0
	s_add_u32 s20, s22, 0x1000
	v_lshrrev_b32_e32 v2, 1, v180
	v_readfirstlane_b32 s39, v180
	v_and_b32_e32 v2, 8, v2
	s_addc_u32 s21, s23, 0
	s_and_b32 s40, s39, 0xffffffc0
	v_bfe_u32 v5, v180, 2, 2
	v_or_b32_e32 v6, 4, v2
	s_ashr_i32 s37, s39, 6
	s_lshl_b32 s0, s40, 2
	v_or_b32_e32 v209, v2, v5
	v_or_b32_e32 v208, v6, v5
	v_or_b32_e32 v5, 16, v5
	v_and_b32_e32 v172, 63, v180
	s_add_i32 s41, s0, 0
	s_lshl_b32 s0, s37, 13
	v_or_b32_e32 v207, v2, v5
	v_lshlrev_b32_e32 v2, 1, v180
	v_writelane_b32 v255, s2, 21
	v_lshlrev_b32_e32 v1, 3, v172
	v_and_b32_e32 v210, 31, v180
	s_add_i32 s2, s0, 0
	v_lshlrev_b32_e32 v205, 4, v172
	v_and_b32_e32 v2, 32, v2
	s_movk_i32 s0, 0xc0
	s_and_b32 s26, s25, 0x1e00
	v_and_b32_e32 v4, 24, v1
	v_and_or_b32 v2, v205, s0, v2
	v_and_b32_e32 v1, 0x100, v1
	v_or_b32_e32 v174, s40, v210
	v_bfe_u32 v184, v180, 5, 1
	v_and_or_b32 v28, v180, 32, v4
	v_or_b32_e32 v206, v6, v5
	v_or3_b32 v1, v2, v1, v4
	s_or_b32 s38, s40, 32
	v_add_u32_e32 v2, s26, v174
	v_mov_b64_e32 v[4:5], s[22:23]
	v_or_b32_e32 v19, s38, v210
	v_mad_i64_i32 v[6:7], s[0:1], v2, s96, v[4:5]
	v_lshlrev_b32_e32 v2, 4, v184
	v_lshl_add_u64 v[8:9], v[6:7], 0, v[2:3]
	v_add_u32_e32 v6, s26, v19
	s_add_i32 s8, s40, 0xffffff80
	v_mad_i64_i32 v[4:5], s[0:1], v6, s96, v[4:5]
	s_add_i32 s18, s8, s26
	v_lshl_add_u64 v[12:13], v[4:5], 0, v[2:3]
	v_or_b32_e32 v4, s18, v210
	v_med3_i32 v4, v4, 0, v227
	v_mul_u32_u24_e32 v4, 0xa00, v4
	v_mov_b32_e32 v5, v3
	v_lshl_add_u64 v[4:5], v[4:5], 1, s[22:23]
	v_lshl_add_u64 v[24:25], v[4:5], 0, v[2:3]
	global_load_dwordx4 v[20:23], v[24:25], off offset:3072
	v_or_b32_e32 v211, 32, v172
	v_or_b32_e32 v6, s18, v211
	v_med3_i32 v6, v6, 0, v227
	v_mul_u32_u24_e32 v16, 0xa00, v6
	global_load_dwordx4 v[116:119], v[8:9], off offset:2048
	global_load_dwordx4 v[112:115], v[8:9], off offset:2080
	global_load_dwordx4 v[100:103], v[12:13], off offset:2048
	global_load_dwordx4 v[4:7], v[12:13], off offset:2080
	global_load_dwordx4 v[36:39], v[24:25], off offset:3104
	global_load_dwordx4 v[108:111], v[8:9], off offset:2112
	global_load_dwordx4 v[104:107], v[8:9], off offset:2144
	s_nop 0
	global_load_dwordx4 v[8:11], v[12:13], off offset:2112
	s_nop 0
	global_load_dwordx4 v[12:15], v[12:13], off offset:2144
	s_nop 0
	global_load_dwordx4 v[40:43], v[24:25], off offset:3136
	global_load_dwordx4 v[44:47], v[24:25], off offset:3168
	s_add_i32 s27, s2, 0x10000
	v_mov_b32_e32 v17, v3
	v_add_u32_e32 v181, s27, v1
	v_or_b32_e32 v1, s18, v209
	v_lshl_add_u64 v[16:17], v[16:17], 1, s[22:23]
	v_med3_i32 v1, v1, 0, v227
	v_lshl_add_u64 v[26:27], v[16:17], 0, v[2:3]
	v_mul_u32_u24_e32 v16, 0xa00, v1
	v_mov_b32_e32 v17, v3
	v_lshl_add_u64 v[24:25], v[16:17], 1, s[20:21]
	v_lshlrev_b32_e32 v16, 1, v28
	v_or_b32_e32 v1, s18, v208
	v_lshl_add_u64 v[24:25], v[24:25], 0, v[16:17]
	s_mov_b32 m0, s27
	v_med3_i32 v1, v1, 0, v227
	global_load_lds_dwordx4 v[24:25], off
	v_mul_u32_u24_e32 v24, 0xa00, v1
	v_mov_b32_e32 v25, v3
	v_lshl_add_u64 v[24:25], v[24:25], 1, s[20:21]
	v_or_b32_e32 v1, s18, v207
	v_lshl_add_u64 v[24:25], v[24:25], 0, v[16:17]
	s_add_i32 m0, s2, 0x10400
	v_med3_i32 v1, v1, 0, v227
	global_load_lds_dwordx4 v[24:25], off
	v_mul_u32_u24_e32 v24, 0xa00, v1
	v_mov_b32_e32 v25, v3
	v_lshl_add_u64 v[24:25], v[24:25], 1, s[20:21]
	v_or_b32_e32 v1, s18, v206
	v_lshl_add_u64 v[24:25], v[24:25], 0, v[16:17]
	s_add_i32 m0, s2, 0x10800
	v_med3_i32 v1, v1, 0, v227
	s_or_b32 s0, s18, 32
	global_load_lds_dwordx4 v[24:25], off
	v_mul_u32_u24_e32 v24, 0xa00, v1
	v_mov_b32_e32 v25, v3
	v_lshl_add_u64 v[24:25], v[24:25], 1, s[20:21]
	v_or_b32_e32 v1, s0, v209
	v_lshl_add_u64 v[24:25], v[24:25], 0, v[16:17]
	s_add_i32 m0, s2, 0x10c00
	v_med3_i32 v1, v1, 0, v227
	global_load_lds_dwordx4 v[24:25], off
	v_mul_u32_u24_e32 v24, 0xa00, v1
	v_mov_b32_e32 v25, v3
	s_add_i32 s1, s2, 0x11000
	v_lshl_add_u64 v[24:25], v[24:25], 1, s[20:21]
	v_or_b32_e32 v1, s0, v208
	v_lshl_add_u64 v[24:25], v[24:25], 0, v[16:17]
	s_mov_b32 m0, s1
	v_med3_i32 v1, v1, 0, v227
	global_load_dwordx4 v[68:71], v[26:27], off offset:3072
	global_load_dwordx4 v[72:75], v[26:27], off offset:3104
	global_load_dwordx4 v[76:79], v[26:27], off offset:3136
	global_load_dwordx4 v[80:83], v[26:27], off offset:3168
	v_or_b32_e32 v168, 0x80, v210
	global_load_lds_dwordx4 v[24:25], off
	v_mul_u32_u24_e32 v24, 0xa00, v1
	v_mov_b32_e32 v25, v3
	v_lshl_add_u64 v[24:25], v[24:25], 1, s[20:21]
	v_or_b32_e32 v1, s0, v207
	v_lshl_add_u64 v[24:25], v[24:25], 0, v[16:17]
	s_add_i32 m0, s2, 0x11400
	v_med3_i32 v1, v1, 0, v227
	global_load_lds_dwordx4 v[24:25], off
	v_mul_u32_u24_e32 v24, 0xa00, v1
	v_mov_b32_e32 v25, v3
	v_lshl_add_u64 v[24:25], v[24:25], 1, s[20:21]
	v_lshl_add_u64 v[48:49], v[24:25], 0, v[16:17]
	s_waitcnt vmcnt(0)
	v_mfma_f32_32x32x16_bf16 v[20:35], v[20:23], v[116:119], 0
	v_or_b32_e32 v1, s0, v206
	s_add_i32 m0, s2, 0x11800
	v_med3_i32 v1, v1, 0, v227
	global_load_lds_dwordx4 v[48:49], off
	v_mul_u32_u24_e32 v48, 0xa00, v1
	v_mov_b32_e32 v49, v3
	v_mfma_f32_32x32x16_bf16 v[20:35], v[36:39], v[112:115], v[20:35]
	v_lshl_add_u64 v[36:37], v[48:49], 1, s[20:21]
	v_lshl_add_u64 v[36:37], v[36:37], 0, v[16:17]
	s_add_i32 m0, s2, 0x11c00
	v_lshlrev_b32_e32 v212, 2, v184
	global_load_lds_dwordx4 v[36:37], off
	s_add_i32 s41, s41, 0x21400
	v_mfma_f32_32x32x16_bf16 v[20:35], v[40:43], v[108:111], v[20:35]
	v_sub_u32_e32 v1, v168, v212
	v_cmp_gt_u32_e64 s[2:3], s97, v1
	s_cmp_gt_i32 s18, -1
	v_or_b32_e32 v204, 1, v212
	s_cselect_b64 s[0:1], -1, 0
	v_writelane_b32 v255, s2, 22
	v_sub_u32_e32 v17, v168, v204
	v_mfma_f32_32x32x16_bf16 v[20:35], v[44:47], v[104:107], v[20:35]
	v_or_b32_e32 v136, s18, v212
	v_writelane_b32 v255, s3, 23
	s_and_b64 vcc, s[2:3], s[0:1]
	v_cmp_gt_u32_e64 s[2:3], s97, v17
	v_or_b32_e32 v199, 2, v212
	v_or_b32_e32 v198, 3, v212
	v_writelane_b32 v255, s2, 24
	s_nop 4
	v_cndmask_b32_e32 v1, v18, v20, vcc
	v_cmp_lt_i32_e32 vcc, -2, v136
	v_sub_u32_e32 v20, v168, v199
	v_writelane_b32 v255, s3, 25
	s_and_b64 vcc, s[2:3], vcc
	v_cmp_gt_u32_e64 s[2:3], s97, v20
	v_cndmask_b32_e32 v17, v18, v21, vcc
	v_cmp_lt_i32_e32 vcc, -3, v136
	v_writelane_b32 v255, s2, 26
	v_sub_u32_e32 v21, v168, v198
	s_and_b64 vcc, s[2:3], vcc
	v_writelane_b32 v255, s3, 27
	v_cmp_gt_u32_e64 s[2:3], s97, v21
	v_or_b32_e32 v197, 8, v212
	v_cndmask_b32_e32 v20, v18, v22, vcc
	v_cmp_lt_i32_e32 vcc, -4, v136
	v_writelane_b32 v255, s2, 28
	v_sub_u32_e32 v22, v168, v197
	s_and_b64 vcc, s[2:3], vcc
	v_writelane_b32 v255, s3, 29
	v_cmp_gt_u32_e64 s[2:3], s97, v22
	v_or_b32_e32 v196, 9, v212
	v_cndmask_b32_e32 v21, v18, v23, vcc
	v_cmp_lt_i32_e32 vcc, -9, v136
	v_writelane_b32 v255, s2, 30
	v_sub_u32_e32 v23, v168, v196
	s_and_b64 vcc, s[2:3], vcc
	v_writelane_b32 v255, s3, 31
	v_cmp_gt_u32_e64 s[2:3], s97, v23
	v_or_b32_e32 v195, 10, v212
	v_cndmask_b32_e32 v22, v18, v24, vcc
	v_cmp_lt_i32_e32 vcc, -10, v136
	v_writelane_b32 v255, s2, 32
	v_sub_u32_e32 v24, v168, v195
	s_and_b64 vcc, s[2:3], vcc
	v_writelane_b32 v255, s3, 33
	v_cmp_gt_u32_e64 s[2:3], s97, v24
	v_or_b32_e32 v194, 11, v212
	v_cndmask_b32_e32 v23, v18, v25, vcc
	v_cmp_lt_i32_e32 vcc, -11, v136
	v_writelane_b32 v255, s2, 34
	v_sub_u32_e32 v25, v168, v194
	s_and_b64 vcc, s[2:3], vcc
	v_writelane_b32 v255, s3, 35
	v_cmp_gt_u32_e64 s[2:3], s97, v25
	v_or_b32_e32 v193, 16, v212
	v_cndmask_b32_e32 v24, v18, v26, vcc
	v_cmp_lt_i32_e32 vcc, -12, v136
	v_writelane_b32 v255, s2, 36
	v_sub_u32_e32 v26, v168, v193
	s_and_b64 vcc, s[2:3], vcc
	v_writelane_b32 v255, s3, 37
	v_cmp_gt_u32_e64 s[2:3], s97, v26
	v_or_b32_e32 v192, 17, v212
	v_cndmask_b32_e32 v25, v18, v27, vcc
	v_cmp_lt_i32_e32 vcc, s90, v136
	v_writelane_b32 v255, s2, 38
	v_sub_u32_e32 v27, v168, v192
	s_and_b64 vcc, s[2:3], vcc
	v_writelane_b32 v255, s3, 39
	v_cmp_gt_u32_e64 s[2:3], s97, v27
	s_movk_i32 s9, 0xffee
	v_or_b32_e32 v191, 18, v212
	v_cndmask_b32_e32 v26, v18, v28, vcc
	v_cmp_lt_i32_e32 vcc, s9, v136
	v_writelane_b32 v255, s2, 40
	v_sub_u32_e32 v28, v168, v191
	s_and_b64 vcc, s[2:3], vcc
	v_writelane_b32 v255, s3, 41
	v_cmp_gt_u32_e64 s[2:3], s97, v28
	s_movk_i32 s10, 0xffed
	v_cndmask_b32_e32 v27, v18, v29, vcc
	v_cmp_lt_i32_e32 vcc, s10, v136
	v_writelane_b32 v255, s2, 42
	v_or_b32_e32 v190, 19, v212
	s_and_b64 vcc, s[2:3], vcc
	v_writelane_b32 v255, s3, 43
	v_sub_u32_e32 v29, v168, v190
	s_movk_i32 s2, 0xffec
	v_cndmask_b32_e32 v28, v18, v30, vcc
	v_cmp_gt_u32_e64 s[4:5], s97, v29
	v_cmp_lt_i32_e32 vcc, s2, v136
	v_or_b32_e32 v189, 24, v212
	v_writelane_b32 v255, s4, 44
	s_and_b64 vcc, s[4:5], vcc
	v_sub_u32_e32 v30, v168, v189
	s_movk_i32 s2, 0xffe7
	v_writelane_b32 v255, s5, 45
	v_cndmask_b32_e32 v29, v18, v31, vcc
	v_cmp_gt_u32_e64 s[4:5], s97, v30
	v_cmp_lt_i32_e32 vcc, s2, v136
	v_or_b32_e32 v188, 25, v212
	v_writelane_b32 v255, s4, 46
	s_and_b64 vcc, s[4:5], vcc
	v_sub_u32_e32 v31, v168, v188
	s_movk_i32 s2, 0xffe6
	v_writelane_b32 v255, s5, 47
	v_cndmask_b32_e32 v30, v18, v32, vcc
	v_cmp_gt_u32_e64 s[4:5], s97, v31
	v_cmp_lt_i32_e32 vcc, s2, v136
	v_or_b32_e32 v187, 26, v212
	v_writelane_b32 v255, s4, 48
	s_and_b64 vcc, s[4:5], vcc
	v_sub_u32_e32 v32, v168, v187
	s_movk_i32 s2, 0xffe5
	v_writelane_b32 v255, s5, 49
	v_cndmask_b32_e32 v31, v18, v33, vcc
	v_cmp_gt_u32_e64 s[4:5], s97, v32
	v_cmp_lt_i32_e32 vcc, s2, v136
	v_or_b32_e32 v186, 27, v212
	v_writelane_b32 v255, s4, 50
	s_and_b64 vcc, s[4:5], vcc
	v_sub_u32_e32 v33, v168, v186
	s_movk_i32 s2, 0xffe4
	v_writelane_b32 v255, s5, 51
	v_cndmask_b32_e32 v32, v18, v34, vcc
	v_cmp_gt_u32_e64 s[4:5], s97, v33
	v_cmp_lt_i32_e32 vcc, s2, v136
	v_max_f32_e32 v34, v17, v17
	v_writelane_b32 v255, s4, 52
	s_and_b64 vcc, s[4:5], vcc
	v_cndmask_b32_e32 v33, v18, v35, vcc
	v_max_f32_e32 v35, v1, v1
	v_max_f32_e32 v34, v35, v34
	v_max3_f32 v34, v34, v20, v21
	v_max3_f32 v34, v34, v22, v23
	v_max3_f32 v34, v34, v24, v25
	v_max3_f32 v34, v34, v26, v27
	v_max3_f32 v34, v34, v28, v29
	v_max3_f32 v34, v34, v30, v31
	v_max3_f32 v34, v34, v32, v33
	v_mov_b32_e32 v35, v34
	s_nop 1
	v_permlane32_swap_b32_e32 v34, v35
	s_mov_b32 s2, 0xf149f2ca
	v_max3_f32 v137, v34, v35, s2
	v_sub_f32_e32 v1, v1, v137
	v_exp_f32_e32 v1, v1
	v_sub_f32_e32 v17, v17, v137
	v_exp_f32_e32 v17, v17
	v_sub_f32_e32 v20, v20, v137
	v_exp_f32_e32 v20, v20
	v_sub_f32_e32 v21, v21, v137
	v_exp_f32_e32 v21, v21
	v_sub_f32_e32 v22, v22, v137
	v_add_f32_e32 v35, 0, v1
	v_exp_f32_e32 v22, v22
	v_sub_f32_e32 v23, v23, v137
	v_add_f32_e32 v35, v17, v35
	v_exp_f32_e32 v23, v23
	v_sub_f32_e32 v24, v24, v137
	v_add_f32_e32 v35, v20, v35
	v_exp_f32_e32 v24, v24
	v_sub_f32_e32 v25, v25, v137
	v_add_f32_e32 v35, v21, v35
	v_exp_f32_e32 v25, v25
	v_sub_f32_e32 v26, v26, v137
	v_add_f32_e32 v35, v22, v35
	v_exp_f32_e32 v26, v26
	v_sub_f32_e32 v27, v27, v137
	v_add_f32_e32 v35, v23, v35
	v_exp_f32_e32 v27, v27
	v_sub_f32_e32 v28, v28, v137
	v_add_f32_e32 v35, v24, v35
	v_exp_f32_e32 v28, v28
	v_sub_f32_e32 v29, v29, v137
	s_waitcnt vmcnt(8)
	v_add_f32_e32 v35, v25, v35
	v_exp_f32_e32 v29, v29
	v_sub_f32_e32 v30, v30, v137
	ds_read_b64_tr_b16 v[52:53], v181 offset:0
	v_add_f32_e32 v35, v26, v35
	v_exp_f32_e32 v30, v30
	v_sub_f32_e32 v31, v31, v137
	ds_read_b64_tr_b16 v[54:55], v181 offset:0x400
	v_add_f32_e32 v35, v27, v35
	v_exp_f32_e32 v31, v31
	v_sub_f32_e32 v32, v32, v137
	ds_read_b64_tr_b16 v[56:57], v181 offset:0x800
	v_add_f32_e32 v35, v28, v35
	v_exp_f32_e32 v32, v32
	v_sub_f32_e32 v33, v33, v137
	ds_read_b64_tr_b16 v[58:59], v181 offset:0xc00
	v_add_f32_e32 v35, v29, v35
	v_exp_f32_e32 v33, v33
	ds_read_b64_tr_b16 v[60:61], v181 offset:0x200
	v_sub_f32_e32 v34, 0xf149f2ca, v137
	v_add_f32_e32 v35, v30, v35
	ds_read_b64_tr_b16 v[62:63], v181 offset:0x600
	v_add_f32_e32 v35, v31, v35
	v_exp_f32_e32 v175, v34
	ds_read_b64_tr_b16 v[64:65], v181 offset:0xa00
	v_add_f32_e32 v35, v32, v35
	ds_read_b64_tr_b16 v[66:67], v181 offset:0xe00
	v_add_f32_e32 v176, v33, v35
	v_mov_b32_e32 v177, v176
	v_cvt_pk_bf16_f32 v84, v1, v17
	v_cvt_pk_bf16_f32 v85, v20, v21
	v_cvt_pk_bf16_f32 v86, v22, v23
	v_cvt_pk_bf16_f32 v87, v24, v25
	v_cvt_pk_bf16_f32 v88, v26, v27
	v_cvt_pk_bf16_f32 v89, v28, v29
	v_cvt_pk_bf16_f32 v90, v30, v31
	v_cvt_pk_bf16_f32 v91, v32, v33
	v_cmp_gt_u32_e64 s[6:7], 32, v172
	v_lshl_add_u32 v173, v210, 2, s41
	v_writelane_b32 v255, s5, 53
	v_permlane32_swap_b32_e32 v176, v177
	v_permlane32_swap_b32_e32 v84, v86
	v_permlane32_swap_b32_e32 v85, v87
	v_permlane32_swap_b32_e32 v88, v90
	v_permlane32_swap_b32_e32 v89, v91
	v_cmp_gt_f32_e32 vcc, 1.0, v175
	s_cbranch_vccz .LBB0_1231
	s_and_saveexec_b64 s[4:5], s[6:7]
	ds_write_b32 v173, v175
	s_or_b64 exec, exec, s[4:5]
	v_lshl_add_u32 v1, v212, 2, s41
	ds_read_b128 v[20:23], v1 offset:96
	ds_read_b128 v[24:27], v1 offset:64
	ds_read_b128 v[36:39], v1 offset:32
	ds_read_b128 v[40:43], v1
	s_waitcnt lgkmcnt(0)
	v_pk_mul_f32 v[34:35], v[22:23], 0 op_sel_hi:[1,0]
	v_pk_mul_f32 v[30:31], v[26:27], 0 op_sel_hi:[1,0]
	v_pk_mul_f32 v[26:27], v[38:39], 0 op_sel_hi:[1,0]
	v_pk_mul_f32 v[22:23], v[42:43], 0 op_sel_hi:[1,0]
	v_pk_mul_f32 v[32:33], v[20:21], 0 op_sel_hi:[1,0]
	v_pk_mul_f32 v[28:29], v[24:25], 0 op_sel_hi:[1,0]
	v_pk_mul_f32 v[24:25], v[36:37], 0 op_sel_hi:[1,0]
	v_pk_mul_f32 v[20:21], v[40:41], 0 op_sel_hi:[1,0]
	s_branch .LBB0_1232

.LBB0_1232:
	s_add_i32 s2, s18, 64
	v_add_u32_e32 v1, s2, v210
	v_med3_i32 v1, v1, 0, v227
	v_lshlrev_b32_e32 v17, 3, v184
	v_mul_u32_u24_e32 v36, 0xa00, v1
	v_mov_b32_e32 v37, v3
	s_waitcnt lgkmcnt(0)
	v_lshl_add_u64 v[36:37], v[36:37], 1, s[22:23]
	v_lshlrev_b32_e32 v178, 1, v17
	v_mov_b32_e32 v179, v3
	s_cmp_lt_i32 s18, 0
	v_lshl_add_u64 v[92:93], v[36:37], 0, v[178:179]
	s_cselect_b64 s[42:43], -1, 0
	v_add_u32_e32 v182, 0x1000, v181
	v_or_b32_e32 v1, s2, v209
	v_med3_i32 v1, v1, 0, v227
	v_mfma_f32_32x32x16_bf16 v[36:51], v[84:87], v[52:55], v[20:35]
	v_mul_u32_u24_e32 v52, 0xa00, v1
	v_mov_b32_e32 v53, v3
	v_lshl_add_u64 v[52:53], v[52:53], 1, s[20:21]
	v_mov_b32_e32 v17, v3
	v_or_b32_e32 v1, s2, v208
	v_lshl_add_u64 v[52:53], v[52:53], 0, v[16:17]
	s_mov_b32 m0, s27
	v_med3_i32 v1, v1, 0, v227
	global_load_dwordx4 v[132:135], v[92:93], off offset:3072
	global_load_dwordx4 v[128:131], v[92:93], off offset:3104
	global_load_dwordx4 v[124:127], v[92:93], off offset:3136
	global_load_dwordx4 v[120:123], v[92:93], off offset:3168
	s_add_i32 s30, s27, 0x400
	global_load_lds_dwordx4 v[52:53], off
	v_mul_u32_u24_e32 v52, 0xa00, v1
	v_mov_b32_e32 v53, v3
	v_lshl_add_u64 v[52:53], v[52:53], 1, s[20:21]
	v_or_b32_e32 v1, s2, v207
	v_lshl_add_u64 v[52:53], v[52:53], 0, v[16:17]
	s_mov_b32 m0, s30
	v_med3_i32 v1, v1, 0, v227
	global_load_lds_dwordx4 v[52:53], off
	v_mul_u32_u24_e32 v52, 0xa00, v1
	v_mov_b32_e32 v53, v3
	v_lshl_add_u64 v[52:53], v[52:53], 1, s[20:21]
	s_add_i32 s28, s27, 0x800
	v_or_b32_e32 v1, s2, v206
	v_lshl_add_u64 v[52:53], v[52:53], 0, v[16:17]
	s_mov_b32 m0, s28
	v_med3_i32 v1, v1, 0, v227
	global_load_lds_dwordx4 v[52:53], off
	v_mul_u32_u24_e32 v52, 0xa00, v1
	v_mov_b32_e32 v53, v3
	v_lshl_add_u64 v[52:53], v[52:53], 1, s[20:21]
	s_add_i32 s29, s27, 0xc00
	v_lshl_add_u64 v[52:53], v[52:53], 0, v[16:17]
	s_mov_b32 m0, s29
	v_mfma_f32_32x32x16_bf16 v[20:35], v[84:87], v[60:63], v[20:35]
	global_load_lds_dwordx4 v[52:53], off
	s_waitcnt vmcnt(8)
	ds_read_b64_tr_b16 v[96:97], v182 offset:0
	ds_read_b64_tr_b16 v[98:99], v182 offset:0x400
	ds_read_b64_tr_b16 v[92:93], v182 offset:0x800
	ds_read_b64_tr_b16 v[94:95], v182 offset:0xc00
	v_mfma_f32_32x32x16_bf16 v[36:51], v[88:91], v[56:59], v[36:51]
	v_mfma_f32_32x32x16_bf16 v[20:35], v[88:91], v[64:67], v[20:35]
	ds_read_b64_tr_b16 v[88:89], v182 offset:0x200
	ds_read_b64_tr_b16 v[90:91], v182 offset:0x600
	ds_read_b64_tr_b16 v[84:85], v182 offset:0xa00
	ds_read_b64_tr_b16 v[86:87], v182 offset:0xe00
	v_mfma_f32_32x32x16_bf16 v[52:67], v[68:71], v[116:119], 0
	v_mfma_f32_32x32x16_bf16 v[52:67], v[72:75], v[112:115], v[52:67]
	v_mfma_f32_32x32x16_bf16 v[52:67], v[76:79], v[108:111], v[52:67]
	v_mfma_f32_32x32x16_bf16 v[52:67], v[80:83], v[104:107], v[52:67]
	s_nop 11
	v_cndmask_b32_e64 v52, v52, v18, s[42:43]
	v_cndmask_b32_e64 v53, v53, v18, s[42:43]
	v_cndmask_b32_e64 v1, v67, v18, s[42:43]
	v_cndmask_b32_e64 v17, v66, v18, s[42:43]
	v_max_f32_e32 v66, v53, v53
	v_max_f32_e32 v67, v52, v52
	v_cndmask_b32_e64 v55, v55, v18, s[42:43]
	v_cndmask_b32_e64 v54, v54, v18, s[42:43]
	v_max_f32_e32 v66, v67, v66
	v_cndmask_b32_e64 v57, v57, v18, s[42:43]
	v_cndmask_b32_e64 v56, v56, v18, s[42:43]
	v_max3_f32 v66, v66, v54, v55
	v_cndmask_b32_e64 v59, v59, v18, s[42:43]
	v_cndmask_b32_e64 v58, v58, v18, s[42:43]
	v_max3_f32 v66, v66, v56, v57
	v_cndmask_b32_e64 v61, v61, v18, s[42:43]
	v_cndmask_b32_e64 v60, v60, v18, s[42:43]
	v_max3_f32 v66, v66, v58, v59
	v_cndmask_b32_e64 v63, v63, v18, s[42:43]
	v_cndmask_b32_e64 v62, v62, v18, s[42:43]
	v_max3_f32 v66, v66, v60, v61
	v_cndmask_b32_e64 v65, v65, v18, s[42:43]
	v_cndmask_b32_e64 v64, v64, v18, s[42:43]
	v_max3_f32 v66, v66, v62, v63
	v_max3_f32 v66, v66, v64, v65
	v_max3_f32 v66, v66, v17, v1
	v_mov_b32_e32 v67, v66
	s_nop 1
	v_permlane32_swap_b32_e32 v66, v67
	v_max3_f32 v169, v137, v66, v67
	v_sub_f32_e32 v52, v52, v169
	v_exp_f32_e32 v52, v52
	v_sub_f32_e32 v53, v53, v169
	v_exp_f32_e32 v53, v53
	v_sub_f32_e32 v54, v54, v169
	v_exp_f32_e32 v54, v54
	v_sub_f32_e32 v55, v55, v169
	v_exp_f32_e32 v55, v55
	v_sub_f32_e32 v56, v56, v169
	v_add_f32_e32 v67, 0, v52
	v_exp_f32_e32 v56, v56
	v_sub_f32_e32 v57, v57, v169
	v_add_f32_e32 v67, v53, v67
	v_exp_f32_e32 v57, v57
	v_sub_f32_e32 v58, v58, v169
	v_add_f32_e32 v67, v54, v67
	v_exp_f32_e32 v58, v58
	v_sub_f32_e32 v59, v59, v169
	v_add_f32_e32 v67, v55, v67
	v_exp_f32_e32 v59, v59
	v_sub_f32_e32 v60, v60, v169
	v_add_f32_e32 v67, v56, v67
	v_exp_f32_e32 v60, v60
	v_sub_f32_e32 v61, v61, v169
	v_add_f32_e32 v67, v57, v67
	v_exp_f32_e32 v61, v61
	v_sub_f32_e32 v62, v62, v169
	v_add_f32_e32 v67, v58, v67
	v_exp_f32_e32 v62, v62
	v_sub_f32_e32 v63, v63, v169
	v_add_f32_e32 v67, v59, v67
	v_exp_f32_e32 v63, v63
	v_sub_f32_e32 v64, v64, v169
	v_add_f32_e32 v67, v60, v67
	v_exp_f32_e32 v64, v64
	v_sub_f32_e32 v65, v65, v169
	v_add_f32_e32 v67, v61, v67
	v_exp_f32_e32 v65, v65
	v_sub_f32_e32 v17, v17, v169
	v_add_f32_e32 v67, v62, v67
	v_exp_f32_e32 v17, v17
	v_sub_f32_e32 v1, v1, v169
	v_add_f32_e32 v67, v63, v67
	v_exp_f32_e32 v1, v1
	v_sub_f32_e32 v66, v137, v169
	v_add_f32_e32 v67, v64, v67
	v_add_f32_e32 v67, v65, v67
	v_exp_f32_e32 v183, v66
	v_add_f32_e32 v67, v17, v67
	v_add_f32_e32 v185, v1, v67
	v_mov_b32_e32 v213, v185
	v_cvt_pk_bf16_f32 v52, v52, v53
	v_cvt_pk_bf16_f32 v53, v54, v55
	v_cvt_pk_bf16_f32 v54, v56, v57
	v_cvt_pk_bf16_f32 v55, v58, v59
	v_cvt_pk_bf16_f32 v56, v60, v61
	v_cvt_pk_bf16_f32 v57, v62, v63
	v_cvt_pk_bf16_f32 v58, v64, v65
	v_cvt_pk_bf16_f32 v59, v17, v1
	s_nop 1
	v_permlane32_swap_b32_e32 v185, v213
	v_permlane32_swap_b32_e32 v52, v54
	v_permlane32_swap_b32_e32 v53, v55
	v_permlane32_swap_b32_e32 v56, v58
	v_permlane32_swap_b32_e32 v57, v59
	v_cmp_gt_f32_e32 vcc, 1.0, v183
	s_cbranch_vccz .LBB0_1236
	s_and_saveexec_b64 s[4:5], s[6:7]
	ds_write_b32 v173, v183
	s_or_b64 exec, exec, s[4:5]
	v_lshl_add_u32 v1, v212, 2, s41
	ds_read_b128 v[60:63], v1 offset:96
	ds_read_b128 v[64:67], v1 offset:64
	ds_read_b128 v[138:141], v1 offset:32
	ds_read_b128 v[142:145], v1
	s_waitcnt lgkmcnt(0)
	v_pk_mul_f32 v[50:51], v[50:51], v[62:63]
	v_pk_mul_f32 v[46:47], v[46:47], v[66:67]
	v_pk_mul_f32 v[42:43], v[42:43], v[140:141]
	v_pk_mul_f32 v[38:39], v[38:39], v[144:145]
	v_pk_mul_f32 v[48:49], v[48:49], v[60:61]
	v_pk_mul_f32 v[44:45], v[44:45], v[64:65]
	v_pk_mul_f32 v[40:41], v[40:41], v[138:139]
	v_pk_mul_f32 v[36:37], v[36:37], v[142:143]
	v_pk_mul_f32 v[34:35], v[34:35], v[62:63]
	v_pk_mul_f32 v[30:31], v[30:31], v[66:67]
	v_pk_mul_f32 v[26:27], v[26:27], v[140:141]
	v_pk_mul_f32 v[22:23], v[22:23], v[144:145]
	v_pk_mul_f32 v[32:33], v[32:33], v[60:61]
	v_pk_mul_f32 v[28:29], v[28:29], v[64:65]
	v_pk_mul_f32 v[24:25], v[24:25], v[138:139]
	v_pk_mul_f32 v[20:21], v[20:21], v[142:143]
.LBB0_1236:
	s_waitcnt lgkmcnt(0)
	v_subrev_u32_e32 v230, s8, v19
	v_or_b32_e32 v1, 32, v136
	v_mfma_f32_32x32x16_bf16 v[36:51], v[52:55], v[96:99], v[36:51]
	v_subrev_u32_e32 v17, 32, v230
	v_mfma_f32_32x32x16_bf16 v[20:35], v[52:55], v[88:91], v[20:35]
	v_mfma_f32_32x32x16_bf16 v[36:51], v[56:59], v[92:95], v[36:51]
	v_mfma_f32_32x32x16_bf16 v[20:35], v[56:59], v[84:87], v[20:35]
	v_mfma_f32_32x32x16_bf16 v[52:67], v[68:71], v[100:103], 0
	v_sub_u32_e32 v68, v17, v212
	v_cmp_gt_u32_e32 vcc, s97, v68
	s_and_b64 vcc, vcc, s[0:1]
	v_sub_u32_e32 v68, v17, v204
	v_cmp_lt_i32_e64 s[0:1], -2, v1
	v_mfma_f32_32x32x16_bf16 v[52:67], v[72:75], v[4:7], v[52:67]
	v_mfma_f32_32x32x16_bf16 v[52:67], v[76:79], v[8:11], v[52:67]
	v_mfma_f32_32x32x16_bf16 v[52:67], v[80:83], v[12:15], v[52:67]
	s_nop 11
	v_cndmask_b32_e32 v52, v18, v52, vcc
	v_cmp_gt_u32_e32 vcc, s97, v68
	s_and_b64 vcc, vcc, s[0:1]
	v_sub_u32_e32 v68, v17, v199
	v_cndmask_b32_e32 v53, v18, v53, vcc
	v_cmp_gt_u32_e32 vcc, s97, v68
	v_cmp_lt_i32_e64 s[0:1], -3, v1
	s_and_b64 vcc, vcc, s[0:1]
	v_sub_u32_e32 v68, v17, v198
	v_cndmask_b32_e32 v54, v18, v54, vcc
	v_cmp_gt_u32_e32 vcc, s97, v68
	v_cmp_lt_i32_e64 s[0:1], -4, v1
	s_and_b64 vcc, vcc, s[0:1]
	v_sub_u32_e32 v68, v17, v197
	v_cndmask_b32_e32 v55, v18, v55, vcc
	v_cmp_gt_u32_e32 vcc, s97, v68
	v_cmp_lt_i32_e64 s[0:1], -9, v1
	s_and_b64 vcc, vcc, s[0:1]
	v_sub_u32_e32 v68, v17, v196
	v_cndmask_b32_e32 v56, v18, v56, vcc
	v_cmp_gt_u32_e32 vcc, s97, v68
	v_cmp_lt_i32_e64 s[0:1], -10, v1
	s_and_b64 vcc, vcc, s[0:1]
	v_sub_u32_e32 v68, v17, v195
	v_cndmask_b32_e32 v57, v18, v57, vcc
	v_cmp_gt_u32_e32 vcc, s97, v68
	v_cmp_lt_i32_e64 s[0:1], -11, v1
	s_and_b64 vcc, vcc, s[0:1]
	v_sub_u32_e32 v68, v17, v194
	v_cndmask_b32_e32 v58, v18, v58, vcc
	v_cmp_gt_u32_e32 vcc, s97, v68
	v_cmp_lt_i32_e64 s[0:1], -12, v1
	s_and_b64 vcc, vcc, s[0:1]
	v_sub_u32_e32 v68, v17, v193
	v_cndmask_b32_e32 v59, v18, v59, vcc
	v_cmp_gt_u32_e32 vcc, s97, v68
	v_cmp_lt_i32_e64 s[0:1], s90, v1
	s_and_b64 vcc, vcc, s[0:1]
	v_sub_u32_e32 v68, v17, v192
	v_cndmask_b32_e32 v60, v18, v60, vcc
	v_cmp_gt_u32_e32 vcc, s97, v68
	v_cmp_lt_i32_e64 s[0:1], s9, v1
	s_and_b64 vcc, vcc, s[0:1]
	v_sub_u32_e32 v68, v17, v191
	v_cndmask_b32_e32 v61, v18, v61, vcc
	v_cmp_gt_u32_e32 vcc, s97, v68
	v_cmp_lt_i32_e64 s[0:1], s10, v1
	s_and_b64 vcc, vcc, s[0:1]
	v_sub_u32_e32 v68, v17, v190
	s_movk_i32 s0, 0xffec
	v_cndmask_b32_e32 v62, v18, v62, vcc
	v_cmp_gt_u32_e32 vcc, s97, v68
	v_cmp_lt_i32_e64 s[0:1], s0, v1
	s_and_b64 vcc, vcc, s[0:1]
	v_sub_u32_e32 v68, v17, v189
	s_movk_i32 s0, 0xffe7
	v_cndmask_b32_e32 v63, v18, v63, vcc
	v_cmp_gt_u32_e32 vcc, s97, v68
	v_cmp_lt_i32_e64 s[0:1], s0, v1
	s_and_b64 vcc, vcc, s[0:1]
	v_sub_u32_e32 v68, v17, v188
	s_movk_i32 s0, 0xffe6
	v_cndmask_b32_e32 v64, v18, v64, vcc
	v_cmp_gt_u32_e32 vcc, s97, v68
	v_cmp_lt_i32_e64 s[0:1], s0, v1
	s_and_b64 vcc, vcc, s[0:1]
	v_sub_u32_e32 v68, v17, v187
	s_movk_i32 s0, 0xffe5
	v_cndmask_b32_e32 v65, v18, v65, vcc
	v_cmp_gt_u32_e32 vcc, s97, v68
	v_cmp_lt_i32_e64 s[0:1], s0, v1
	s_and_b64 vcc, vcc, s[0:1]
	v_sub_u32_e32 v17, v17, v186
	s_movk_i32 s0, 0xffe4
	v_cndmask_b32_e32 v66, v18, v66, vcc
	v_cmp_gt_u32_e32 vcc, s97, v17
	v_cmp_lt_i32_e64 s[0:1], s0, v1
	s_and_b64 vcc, vcc, s[0:1]
	v_cndmask_b32_e32 v1, v18, v67, vcc
	v_max_f32_e32 v17, v53, v53
	v_max_f32_e32 v67, v52, v52
	v_max_f32_e32 v17, v67, v17
	v_max3_f32 v17, v17, v54, v55
	v_max3_f32 v17, v17, v56, v57
	v_max3_f32 v17, v17, v58, v59
	v_max3_f32 v17, v17, v60, v61
	v_max3_f32 v17, v17, v62, v63
	v_max3_f32 v17, v17, v64, v65
	v_max3_f32 v17, v17, v66, v1
	v_mov_b32_e32 v67, v17
	s_nop 1
	v_permlane32_swap_b32_e32 v17, v67
	s_mov_b32 s0, 0xf149f2ca
	v_max3_f32 v170, v17, v67, s0
	v_sub_f32_e32 v52, v52, v170
	v_exp_f32_e32 v52, v52
	v_sub_f32_e32 v53, v53, v170
	v_exp_f32_e32 v53, v53
	v_sub_f32_e32 v54, v54, v170
	v_exp_f32_e32 v54, v54
	v_sub_f32_e32 v55, v55, v170
	v_exp_f32_e32 v55, v55
	v_sub_f32_e32 v56, v56, v170
	v_add_f32_e32 v67, 0, v52
	v_exp_f32_e32 v56, v56
	v_sub_f32_e32 v57, v57, v170
	v_add_f32_e32 v67, v53, v67
	v_exp_f32_e32 v57, v57
	v_sub_f32_e32 v58, v58, v170
	v_add_f32_e32 v67, v54, v67
	v_exp_f32_e32 v58, v58
	v_sub_f32_e32 v59, v59, v170
	v_add_f32_e32 v67, v55, v67
	v_exp_f32_e32 v59, v59
	v_sub_f32_e32 v60, v60, v170
	v_add_f32_e32 v67, v56, v67
	v_exp_f32_e32 v60, v60
	v_sub_f32_e32 v61, v61, v170
	v_add_f32_e32 v67, v57, v67
	v_exp_f32_e32 v61, v61
	v_sub_f32_e32 v62, v62, v170
	v_add_f32_e32 v67, v58, v67
	v_exp_f32_e32 v62, v62
	v_sub_f32_e32 v63, v63, v170
	v_add_f32_e32 v67, v59, v67
	v_exp_f32_e32 v63, v63
	v_sub_f32_e32 v64, v64, v170
	v_add_f32_e32 v67, v60, v67
	v_exp_f32_e32 v64, v64
	v_sub_f32_e32 v65, v65, v170
	v_add_f32_e32 v67, v61, v67
	v_exp_f32_e32 v65, v65
	v_sub_f32_e32 v66, v66, v170
	v_add_f32_e32 v67, v62, v67
	v_exp_f32_e32 v66, v66
	v_sub_f32_e32 v1, v1, v170
	v_add_f32_e32 v67, v63, v67
	v_exp_f32_e32 v1, v1
	v_sub_f32_e32 v17, 0xf149f2ca, v170
	v_add_f32_e32 v67, v64, v67
	v_add_f32_e32 v67, v65, v67
	v_exp_f32_e32 v214, v17
	v_add_f32_e32 v67, v66, v67
	v_add_f32_e32 v215, v1, v67
	v_mov_b32_e32 v229, v215
	v_cvt_pk_bf16_f32 v152, v52, v53
	v_cvt_pk_bf16_f32 v153, v54, v55
	v_cvt_pk_bf16_f32 v154, v56, v57
	v_cvt_pk_bf16_f32 v155, v58, v59
	v_cvt_pk_bf16_f32 v156, v60, v61
	v_cvt_pk_bf16_f32 v157, v62, v63
	v_cvt_pk_bf16_f32 v158, v64, v65
	v_cvt_pk_bf16_f32 v159, v66, v1
	s_nop 1
	v_permlane32_swap_b32_e32 v215, v229
	v_permlane32_swap_b32_e32 v152, v154
	v_permlane32_swap_b32_e32 v153, v155
	v_permlane32_swap_b32_e32 v156, v158
	v_permlane32_swap_b32_e32 v157, v159
	v_cmp_gt_f32_e32 vcc, 1.0, v214
	s_cbranch_vccz .LBB0_1240
	s_and_saveexec_b64 s[0:1], s[6:7]
	ds_write_b32 v173, v214
	s_or_b64 exec, exec, s[0:1]
	v_lshl_add_u32 v1, v212, 2, s41
	ds_read_b128 v[52:55], v1 offset:96
	ds_read_b128 v[56:59], v1 offset:64
	ds_read_b128 v[68:71], v1 offset:32
	ds_read_b128 v[72:75], v1
	s_waitcnt lgkmcnt(0)
	v_pk_mul_f32 v[66:67], v[54:55], 0 op_sel_hi:[1,0]
	v_pk_mul_f32 v[62:63], v[58:59], 0 op_sel_hi:[1,0]
	v_pk_mul_f32 v[58:59], v[70:71], 0 op_sel_hi:[1,0]
	v_pk_mul_f32 v[54:55], v[74:75], 0 op_sel_hi:[1,0]
	v_pk_mul_f32 v[64:65], v[52:53], 0 op_sel_hi:[1,0]
	v_pk_mul_f32 v[60:61], v[56:57], 0 op_sel_hi:[1,0]
	v_pk_mul_f32 v[56:57], v[68:69], 0 op_sel_hi:[1,0]
	v_pk_mul_f32 v[52:53], v[72:73], 0 op_sel_hi:[1,0]
	s_branch .LBB0_1241

.LBB0_1243:
	s_nop 10
	v_max_f32_e32 v1, v85, v85
	v_max_f32_e32 v17, v84, v84
	v_max_f32_e32 v1, v17, v1
	v_max3_f32 v1, v1, v86, v87
	v_max3_f32 v1, v1, v88, v89
	v_max3_f32 v1, v1, v90, v91
	v_max3_f32 v1, v1, v92, v93
	v_max3_f32 v1, v1, v94, v95
	v_max3_f32 v1, v1, v96, v97
	v_max3_f32 v1, v1, v98, v99
	v_mov_b32_e32 v17, v1
	s_nop 1
	v_permlane32_swap_b32_e32 v1, v17
	v_max3_f32 v171, v169, v1, v17
	v_sub_f32_e32 v17, v84, v171
	v_exp_f32_e32 v17, v17
	v_sub_f32_e32 v84, v85, v171
	v_exp_f32_e32 v84, v84
	v_sub_f32_e32 v85, v86, v171
	v_exp_f32_e32 v85, v85
	v_sub_f32_e32 v86, v87, v171
	v_exp_f32_e32 v86, v86
	v_sub_f32_e32 v88, v88, v171
	v_add_f32_e32 v87, 0, v17
	v_exp_f32_e32 v88, v88
	v_sub_f32_e32 v89, v89, v171
	v_add_f32_e32 v87, v84, v87
	v_exp_f32_e32 v89, v89
	v_sub_f32_e32 v90, v90, v171
	v_add_f32_e32 v87, v85, v87
	v_exp_f32_e32 v90, v90
	v_sub_f32_e32 v91, v91, v171
	v_add_f32_e32 v87, v86, v87
	v_exp_f32_e32 v91, v91
	v_sub_f32_e32 v92, v92, v171
	v_add_f32_e32 v87, v88, v87
	v_exp_f32_e32 v92, v92
	v_sub_f32_e32 v93, v93, v171
	v_add_f32_e32 v87, v89, v87
	v_exp_f32_e32 v93, v93
	v_sub_f32_e32 v94, v94, v171
	v_add_f32_e32 v87, v90, v87
	v_exp_f32_e32 v94, v94
	v_sub_f32_e32 v95, v95, v171
	v_add_f32_e32 v87, v91, v87
	v_exp_f32_e32 v95, v95
	v_sub_f32_e32 v96, v96, v171
	v_add_f32_e32 v87, v92, v87
	v_exp_f32_e32 v96, v96
	v_sub_f32_e32 v97, v97, v171
	v_add_f32_e32 v87, v93, v87
	v_exp_f32_e32 v97, v97
	v_sub_f32_e32 v98, v98, v171
	v_add_f32_e32 v87, v94, v87
	v_exp_f32_e32 v98, v98
	v_sub_f32_e32 v99, v99, v171
	v_add_f32_e32 v87, v95, v87
	v_exp_f32_e32 v99, v99
	v_sub_f32_e32 v1, v169, v171
	v_add_f32_e32 v87, v96, v87
	v_add_f32_e32 v87, v97, v87
	v_exp_f32_e32 v231, v1
	v_add_f32_e32 v87, v98, v87
	v_add_f32_e32 v232, v99, v87
	v_mov_b32_e32 v233, v232
	v_cvt_pk_bf16_f32 v84, v17, v84
	v_cvt_pk_bf16_f32 v85, v85, v86
	v_cvt_pk_bf16_f32 v86, v88, v89
	v_cvt_pk_bf16_f32 v87, v90, v91
	v_cvt_pk_bf16_f32 v88, v92, v93
	v_cvt_pk_bf16_f32 v89, v94, v95
	v_cvt_pk_bf16_f32 v90, v96, v97
	v_cvt_pk_bf16_f32 v91, v98, v99
	s_nop 1
	v_permlane32_swap_b32_e32 v232, v233
	v_permlane32_swap_b32_e32 v84, v86
	v_permlane32_swap_b32_e32 v85, v87
	v_permlane32_swap_b32_e32 v88, v90
	v_permlane32_swap_b32_e32 v89, v91
	v_cmp_gt_f32_e32 vcc, 1.0, v231
	s_cbranch_vccz .LBB0_1247
	s_and_saveexec_b64 s[0:1], s[6:7]
	ds_write_b32 v173, v231
	s_or_b64 exec, exec, s[0:1]
	v_lshl_add_u32 v1, v212, 2, s41
	ds_read_b128 v[92:95], v1 offset:96
	ds_read_b128 v[96:99], v1 offset:64
	ds_read_b128 v[236:239], v1 offset:32
	ds_read_b128 v[240:243], v1
	s_waitcnt lgkmcnt(0)
	v_pk_mul_f32 v[50:51], v[50:51], v[94:95]
	v_pk_mul_f32 v[46:47], v[46:47], v[98:99]
	v_pk_mul_f32 v[42:43], v[42:43], v[238:239]
	v_pk_mul_f32 v[38:39], v[38:39], v[242:243]
	v_pk_mul_f32 v[48:49], v[48:49], v[92:93]
	v_pk_mul_f32 v[44:45], v[44:45], v[96:97]
	v_pk_mul_f32 v[40:41], v[40:41], v[236:237]
	v_pk_mul_f32 v[36:37], v[36:37], v[240:241]
	v_pk_mul_f32 v[34:35], v[34:35], v[94:95]
	v_pk_mul_f32 v[30:31], v[30:31], v[98:99]
	v_pk_mul_f32 v[26:27], v[26:27], v[238:239]
	v_pk_mul_f32 v[22:23], v[22:23], v[242:243]
	v_pk_mul_f32 v[32:33], v[32:33], v[92:93]
	v_pk_mul_f32 v[28:29], v[28:29], v[96:97]
	v_pk_mul_f32 v[24:25], v[24:25], v[236:237]
	v_pk_mul_f32 v[20:21], v[20:21], v[240:241]

.LBB0_1249:
	s_nop 10
	v_max_f32_e32 v1, v85, v85
	v_max_f32_e32 v17, v84, v84
	v_max_f32_e32 v1, v17, v1
	v_max3_f32 v1, v1, v86, v87
	v_max3_f32 v1, v1, v88, v89
	v_max3_f32 v1, v1, v90, v91
	v_max3_f32 v1, v1, v92, v93
	v_max3_f32 v1, v1, v94, v95
	v_max3_f32 v1, v1, v96, v97
	v_max3_f32 v1, v1, v98, v99
	v_mov_b32_e32 v17, v1
	s_nop 1
	v_permlane32_swap_b32_e32 v1, v17
	v_max3_f32 v169, v170, v1, v17
	v_sub_f32_e32 v17, v84, v169
	v_exp_f32_e32 v17, v17
	v_sub_f32_e32 v84, v85, v169
	v_exp_f32_e32 v84, v84
	v_sub_f32_e32 v85, v86, v169
	v_exp_f32_e32 v85, v85
	v_sub_f32_e32 v86, v87, v169
	v_exp_f32_e32 v86, v86
	v_sub_f32_e32 v88, v88, v169
	v_add_f32_e32 v87, 0, v17
	v_exp_f32_e32 v120, v88
	v_sub_f32_e32 v88, v89, v169
	v_add_f32_e32 v87, v84, v87
	v_exp_f32_e32 v121, v88
	v_sub_f32_e32 v88, v90, v169
	v_add_f32_e32 v87, v85, v87
	v_exp_f32_e32 v122, v88
	v_sub_f32_e32 v88, v91, v169
	v_add_f32_e32 v87, v86, v87
	v_exp_f32_e32 v91, v88
	v_sub_f32_e32 v88, v92, v169
	v_add_f32_e32 v87, v120, v87
	v_exp_f32_e32 v92, v88
	v_sub_f32_e32 v88, v93, v169
	v_add_f32_e32 v87, v121, v87
	v_exp_f32_e32 v93, v88
	v_sub_f32_e32 v88, v94, v169
	v_add_f32_e32 v87, v122, v87
	v_exp_f32_e32 v94, v88
	v_sub_f32_e32 v88, v95, v169
	v_add_f32_e32 v87, v91, v87
	v_exp_f32_e32 v95, v88
	v_sub_f32_e32 v88, v96, v169
	v_add_f32_e32 v87, v92, v87
	v_exp_f32_e32 v96, v88
	v_sub_f32_e32 v88, v97, v169
	v_add_f32_e32 v87, v93, v87
	v_exp_f32_e32 v97, v88
	v_sub_f32_e32 v88, v98, v169
	v_add_f32_e32 v87, v94, v87
	v_exp_f32_e32 v98, v88
	v_sub_f32_e32 v88, v99, v169
	v_add_f32_e32 v87, v95, v87
	v_exp_f32_e32 v99, v88
	v_sub_f32_e32 v1, v170, v169
	v_add_f32_e32 v87, v96, v87
	v_add_f32_e32 v87, v97, v87
	v_exp_f32_e32 v234, v1
	v_add_f32_e32 v87, v98, v87
	v_add_f32_e32 v235, v99, v87
	v_mov_b32_e32 v236, v235
	v_cvt_pk_bf16_f32 v88, v17, v84
	v_cvt_pk_bf16_f32 v89, v85, v86
	v_cvt_pk_bf16_f32 v90, v120, v121
	v_cvt_pk_bf16_f32 v91, v122, v91
	v_cvt_pk_bf16_f32 v84, v92, v93
	v_cvt_pk_bf16_f32 v85, v94, v95
	v_cvt_pk_bf16_f32 v86, v96, v97
	v_cvt_pk_bf16_f32 v87, v98, v99
	s_nop 1
	v_permlane32_swap_b32_e32 v235, v236
	v_permlane32_swap_b32_e32 v88, v90
	v_permlane32_swap_b32_e32 v89, v91
	v_permlane32_swap_b32_e32 v84, v86
	v_permlane32_swap_b32_e32 v85, v87
	v_cmp_gt_f32_e32 vcc, 1.0, v234
	s_cbranch_vccz .LBB0_1253
	s_and_saveexec_b64 s[0:1], s[6:7]
	ds_write_b32 v173, v234
	s_or_b64 exec, exec, s[0:1]
	v_lshl_add_u32 v1, v212, 2, s41
	ds_read_b128 v[92:95], v1 offset:96
	ds_read_b128 v[96:99], v1 offset:64
	ds_read_b128 v[120:123], v1 offset:32
	ds_read_b128 v[124:127], v1
	s_waitcnt lgkmcnt(0)
	v_pk_mul_f32 v[82:83], v[82:83], v[94:95]
	v_pk_mul_f32 v[78:79], v[78:79], v[98:99]
	v_pk_mul_f32 v[74:75], v[74:75], v[122:123]
	v_pk_mul_f32 v[70:71], v[70:71], v[126:127]
	v_pk_mul_f32 v[80:81], v[80:81], v[92:93]
	v_pk_mul_f32 v[76:77], v[76:77], v[96:97]
	v_pk_mul_f32 v[72:73], v[72:73], v[120:121]
	v_pk_mul_f32 v[68:69], v[68:69], v[124:125]
	v_pk_mul_f32 v[66:67], v[66:67], v[94:95]
	v_pk_mul_f32 v[62:63], v[62:63], v[98:99]
	v_pk_mul_f32 v[58:59], v[58:59], v[122:123]
	v_pk_mul_f32 v[54:55], v[54:55], v[126:127]
	v_pk_mul_f32 v[64:65], v[64:65], v[92:93]
	v_pk_mul_f32 v[60:61], v[60:61], v[96:97]
	v_pk_mul_f32 v[56:57], v[56:57], v[120:121]
	v_pk_mul_f32 v[52:53], v[52:53], v[124:125]

.LBB0_1255:
	s_nop 10
	v_max_f32_e32 v1, v85, v85
	v_max_f32_e32 v17, v84, v84
	v_max_f32_e32 v1, v17, v1
	v_max3_f32 v1, v1, v86, v87
	v_max3_f32 v1, v1, v88, v89
	v_max3_f32 v1, v1, v90, v91
	v_max3_f32 v1, v1, v92, v93
	v_max3_f32 v1, v1, v94, v95
	v_max3_f32 v1, v1, v96, v97
	v_max3_f32 v1, v1, v98, v99
	v_mov_b32_e32 v17, v1
	s_nop 1
	v_permlane32_swap_b32_e32 v1, v17
	v_max3_f32 v243, v171, v1, v17
	v_sub_f32_e32 v17, v84, v243
	v_exp_f32_e32 v17, v17
	v_sub_f32_e32 v84, v85, v243
	v_exp_f32_e32 v84, v84
	v_sub_f32_e32 v85, v86, v243
	v_exp_f32_e32 v85, v85
	v_sub_f32_e32 v86, v87, v243
	v_exp_f32_e32 v86, v86
	v_sub_f32_e32 v88, v88, v243
	v_add_f32_e32 v87, 0, v17
	v_exp_f32_e32 v88, v88
	v_sub_f32_e32 v89, v89, v243
	v_add_f32_e32 v87, v84, v87
	v_exp_f32_e32 v89, v89
	v_sub_f32_e32 v90, v90, v243
	v_add_f32_e32 v87, v85, v87
	v_exp_f32_e32 v90, v90
	v_sub_f32_e32 v91, v91, v243
	v_add_f32_e32 v87, v86, v87
	v_exp_f32_e32 v91, v91
	v_sub_f32_e32 v92, v92, v243
	v_add_f32_e32 v87, v88, v87
	v_exp_f32_e32 v92, v92
	v_sub_f32_e32 v93, v93, v243
	v_add_f32_e32 v87, v89, v87
	v_exp_f32_e32 v93, v93
	v_sub_f32_e32 v94, v94, v243
	v_add_f32_e32 v87, v90, v87
	v_exp_f32_e32 v94, v94
	v_sub_f32_e32 v95, v95, v243
	v_add_f32_e32 v87, v91, v87
	v_exp_f32_e32 v95, v95
	v_sub_f32_e32 v96, v96, v243
	v_add_f32_e32 v87, v92, v87
	v_exp_f32_e32 v96, v96
	v_sub_f32_e32 v97, v97, v243
	v_add_f32_e32 v87, v93, v87
	v_exp_f32_e32 v97, v97
	v_sub_f32_e32 v98, v98, v243
	v_add_f32_e32 v87, v94, v87
	v_exp_f32_e32 v98, v98
	v_sub_f32_e32 v99, v99, v243
	v_add_f32_e32 v87, v95, v87
	v_exp_f32_e32 v99, v99
	v_sub_f32_e32 v1, v171, v243
	v_add_f32_e32 v87, v96, v87
	v_add_f32_e32 v87, v97, v87
	v_exp_f32_e32 v237, v1
	v_add_f32_e32 v87, v98, v87
	v_add_f32_e32 v238, v99, v87
	v_mov_b32_e32 v239, v238
	v_cvt_pk_bf16_f32 v84, v17, v84
	v_cvt_pk_bf16_f32 v85, v85, v86
	v_cvt_pk_bf16_f32 v86, v88, v89
	v_cvt_pk_bf16_f32 v87, v90, v91
	v_cvt_pk_bf16_f32 v88, v92, v93
	v_cvt_pk_bf16_f32 v89, v94, v95
	v_cvt_pk_bf16_f32 v90, v96, v97
	v_cvt_pk_bf16_f32 v91, v98, v99
	s_nop 1
	v_permlane32_swap_b32_e32 v238, v239
	v_permlane32_swap_b32_e32 v84, v86
	v_permlane32_swap_b32_e32 v85, v87
	v_permlane32_swap_b32_e32 v88, v90
	v_permlane32_swap_b32_e32 v89, v91
	v_cmp_gt_f32_e32 vcc, 1.0, v237
	s_cbranch_vccz .LBB0_1259
	s_and_saveexec_b64 s[0:1], s[6:7]
	ds_write_b32 v173, v237
	s_or_b64 exec, exec, s[0:1]
	v_lshl_add_u32 v1, v212, 2, s41
	ds_read_b128 v[92:95], v1 offset:96
	ds_read_b128 v[96:99], v1 offset:64
	ds_read_b128 v[244:247], v1 offset:32
	ds_read_b128 v[200:203], v1
	s_waitcnt lgkmcnt(0)
	v_pk_mul_f32 v[50:51], v[50:51], v[94:95]
	v_pk_mul_f32 v[46:47], v[46:47], v[98:99]
	v_pk_mul_f32 v[42:43], v[42:43], v[246:247]
	v_pk_mul_f32 v[38:39], v[38:39], v[202:203]
	v_pk_mul_f32 v[48:49], v[48:49], v[92:93]
	v_pk_mul_f32 v[44:45], v[44:45], v[96:97]
	v_pk_mul_f32 v[40:41], v[40:41], v[244:245]
	v_pk_mul_f32 v[36:37], v[36:37], v[200:201]
	v_pk_mul_f32 v[34:35], v[34:35], v[94:95]
	v_pk_mul_f32 v[30:31], v[30:31], v[98:99]
	v_pk_mul_f32 v[26:27], v[26:27], v[246:247]
	v_pk_mul_f32 v[22:23], v[22:23], v[202:203]
	v_pk_mul_f32 v[32:33], v[32:33], v[92:93]
	v_pk_mul_f32 v[28:29], v[28:29], v[96:97]
	v_pk_mul_f32 v[24:25], v[24:25], v[244:245]
	v_pk_mul_f32 v[20:21], v[20:21], v[200:201]

.LBB0_1261:
	s_nop 10
	v_max_f32_e32 v1, v85, v85
	v_max_f32_e32 v17, v84, v84
	v_max_f32_e32 v1, v17, v1
	v_max3_f32 v1, v1, v86, v87
	v_max3_f32 v1, v1, v88, v89
	v_max3_f32 v1, v1, v90, v91
	v_max3_f32 v1, v1, v92, v93
	v_max3_f32 v1, v1, v94, v95
	v_max3_f32 v1, v1, v96, v97
	v_max3_f32 v1, v1, v98, v99
	v_mov_b32_e32 v17, v1
	s_nop 1
	v_permlane32_swap_b32_e32 v1, v17
	v_max3_f32 v244, v169, v1, v17
	v_sub_f32_e32 v17, v84, v244
	v_exp_f32_e32 v17, v17
	v_sub_f32_e32 v84, v85, v244
	v_exp_f32_e32 v84, v84
	v_sub_f32_e32 v85, v86, v244
	v_exp_f32_e32 v85, v85
	v_sub_f32_e32 v86, v87, v244
	v_exp_f32_e32 v86, v86
	v_sub_f32_e32 v88, v88, v244
	v_add_f32_e32 v87, 0, v17
	v_exp_f32_e32 v88, v88
	v_sub_f32_e32 v89, v89, v244
	v_add_f32_e32 v87, v84, v87
	v_exp_f32_e32 v89, v89
	v_sub_f32_e32 v90, v90, v244
	v_add_f32_e32 v87, v85, v87
	v_exp_f32_e32 v90, v90
	v_sub_f32_e32 v91, v91, v244
	v_add_f32_e32 v87, v86, v87
	v_exp_f32_e32 v91, v91
	v_sub_f32_e32 v92, v92, v244
	v_add_f32_e32 v87, v88, v87
	v_exp_f32_e32 v92, v92
	v_sub_f32_e32 v93, v93, v244
	v_add_f32_e32 v87, v89, v87
	v_exp_f32_e32 v93, v93
	v_sub_f32_e32 v94, v94, v244
	v_add_f32_e32 v87, v90, v87
	v_exp_f32_e32 v94, v94
	v_sub_f32_e32 v95, v95, v244
	v_add_f32_e32 v87, v91, v87
	v_exp_f32_e32 v95, v95
	v_sub_f32_e32 v96, v96, v244
	v_add_f32_e32 v87, v92, v87
	v_exp_f32_e32 v96, v96
	v_sub_f32_e32 v97, v97, v244
	v_add_f32_e32 v87, v93, v87
	v_exp_f32_e32 v97, v97
	v_sub_f32_e32 v98, v98, v244
	v_add_f32_e32 v87, v94, v87
	v_exp_f32_e32 v98, v98
	v_sub_f32_e32 v99, v99, v244
	v_add_f32_e32 v87, v95, v87
	v_exp_f32_e32 v99, v99
	v_sub_f32_e32 v1, v169, v244
	v_add_f32_e32 v87, v96, v87
	v_add_f32_e32 v87, v97, v87
	v_exp_f32_e32 v240, v1
	v_add_f32_e32 v87, v98, v87
	v_add_f32_e32 v241, v99, v87
	v_mov_b32_e32 v242, v241
	v_cvt_pk_bf16_f32 v84, v17, v84
	v_cvt_pk_bf16_f32 v85, v85, v86
	v_cvt_pk_bf16_f32 v86, v88, v89
	v_cvt_pk_bf16_f32 v87, v90, v91
	v_cvt_pk_bf16_f32 v168, v92, v93
	v_cvt_pk_bf16_f32 v169, v94, v95
	v_cvt_pk_bf16_f32 v170, v96, v97
	v_cvt_pk_bf16_f32 v171, v98, v99
	s_nop 1
	v_permlane32_swap_b32_e32 v241, v242
	v_permlane32_swap_b32_e32 v84, v86
	v_permlane32_swap_b32_e32 v85, v87
	v_permlane32_swap_b32_e32 v168, v170
	v_permlane32_swap_b32_e32 v169, v171
	v_cmp_gt_f32_e32 vcc, 1.0, v240
	s_cbranch_vccz .LBB0_1265
	s_and_saveexec_b64 s[0:1], s[6:7]
	ds_write_b32 v173, v240
	s_or_b64 exec, exec, s[0:1]
	v_lshl_add_u32 v1, v212, 2, s41
	ds_read_b128 v[88:91], v1 offset:96
	ds_read_b128 v[92:95], v1 offset:64
	ds_read_b128 v[96:99], v1 offset:32
	ds_read_b128 v[136:139], v1
	s_waitcnt lgkmcnt(0)
	v_pk_mul_f32 v[82:83], v[82:83], v[90:91]
	v_pk_mul_f32 v[78:79], v[78:79], v[94:95]
	v_pk_mul_f32 v[74:75], v[74:75], v[98:99]
	v_pk_mul_f32 v[70:71], v[70:71], v[138:139]
	v_pk_mul_f32 v[80:81], v[80:81], v[88:89]
	v_pk_mul_f32 v[76:77], v[76:77], v[92:93]
	v_pk_mul_f32 v[72:73], v[72:73], v[96:97]
	v_pk_mul_f32 v[68:69], v[68:69], v[136:137]
	v_pk_mul_f32 v[66:67], v[66:67], v[90:91]
	v_pk_mul_f32 v[62:63], v[62:63], v[94:95]
	v_pk_mul_f32 v[58:59], v[58:59], v[98:99]
	v_pk_mul_f32 v[54:55], v[54:55], v[138:139]
	v_pk_mul_f32 v[64:65], v[64:65], v[88:89]
	v_pk_mul_f32 v[60:61], v[60:61], v[92:93]
	v_pk_mul_f32 v[56:57], v[56:57], v[96:97]
	v_pk_mul_f32 v[52:53], v[52:53], v[136:137]
.LBB0_1265:
	v_or_b32_e32 v1, 0xa0, v172
	v_add_u32_e32 v1, s18, v1
	v_med3_i32 v1, v1, 0, v227
	v_mul_u32_u24_e32 v88, 0xa00, v1
	v_mov_b32_e32 v89, v3
	s_waitcnt lgkmcnt(0)
	v_lshl_add_u64 v[88:89], v[88:89], 1, s[22:23]
	v_mov_b32_e32 v179, v3
	s_add_i32 s0, s18, 0xa0
	v_or_b32_e32 v1, 0x80, v212
	v_lshl_add_u64 v[88:89], v[88:89], 0, v[178:179]
	v_add_u32_e32 v1, s18, v1
	v_or_b32_e32 v17, s0, v209
	v_med3_i32 v17, v17, 0, v227
	global_load_dwordx4 v[148:151], v[88:89], off offset:3072
	global_load_dwordx4 v[136:139], v[88:89], off offset:3104
	global_load_dwordx4 v[140:143], v[88:89], off offset:3136
	global_load_dwordx4 v[144:147], v[88:89], off offset:3168
	v_mul_u32_u24_e32 v88, 0xa00, v17
	v_mov_b32_e32 v89, v3
	v_lshl_add_u64 v[88:89], v[88:89], 1, s[20:21]
	v_mov_b32_e32 v17, v3
	s_mov_b32 m0, s36
	v_lshl_add_u64 v[88:89], v[88:89], 0, v[16:17]
	global_load_lds_dwordx4 v[88:89], off
	v_or_b32_e32 v88, s0, v208
	v_med3_i32 v88, v88, 0, v227
	v_mul_u32_u24_e32 v88, 0xa00, v88
	v_mov_b32_e32 v89, v3
	v_mfma_f32_32x32x16_bf16 v[68:83], v[84:87], v[164:167], v[68:83]
	v_lshl_add_u64 v[88:89], v[88:89], 1, s[20:21]
	v_lshl_add_u64 v[88:89], v[88:89], 0, v[16:17]
	s_mov_b32 m0, s34
	v_cmp_lt_i32_e64 s[76:77], -1, v1
	global_load_lds_dwordx4 v[88:89], off
	s_mov_b32 m0, s31
	v_mfma_f32_32x32x16_bf16 v[52:67], v[84:87], v[156:159], v[52:67]
	v_or_b32_e32 v84, s0, v207
	v_med3_i32 v84, v84, 0, v227
	v_mul_u32_u24_e32 v156, 0xa00, v84
	v_mov_b32_e32 v157, v3
	v_cmp_lt_i32_e64 s[78:79], -2, v1
	v_cmp_lt_i32_e64 s[80:81], -3, v1
	v_cmp_lt_i32_e64 s[82:83], -4, v1
	s_waitcnt vmcnt(0)
	v_mfma_f32_32x32x16_bf16 v[84:99], v[132:135], v[116:119], 0
	v_lshl_add_u64 v[116:117], v[156:157], 1, s[20:21]
	v_lshl_add_u64 v[116:117], v[116:117], 0, v[16:17]
	global_load_lds_dwordx4 v[116:117], off
	v_or_b32_e32 v116, s0, v206
	v_med3_i32 v116, v116, 0, v227
	s_mov_b32 m0, s35
	v_mfma_f32_32x32x16_bf16 v[84:99], v[128:131], v[112:115], v[84:99]
	v_mul_u32_u24_e32 v112, 0xa00, v116
	v_mov_b32_e32 v113, v3
	v_lshl_add_u64 v[112:113], v[112:113], 1, s[20:21]
	v_lshl_add_u64 v[112:113], v[112:113], 0, v[16:17]
	global_load_lds_dwordx4 v[112:113], off
	v_sub_u32_e32 v17, v210, v212
	v_mfma_f32_32x32x16_bf16 v[84:99], v[124:127], v[108:111], v[84:99]
	v_cmp_gt_u32_e64 s[14:15], s97, v17
	v_sub_u32_e32 v17, v210, v204
	v_cmp_gt_u32_e64 s[70:71], s97, v17
	v_sub_u32_e32 v17, v210, v199
	s_and_b64 vcc, s[14:15], s[76:77]
	v_cmp_gt_u32_e64 s[16:17], s97, v17
	v_sub_u32_e32 v17, v210, v198
	v_mfma_f32_32x32x16_bf16 v[84:99], v[120:123], v[104:107], v[84:99]
	v_cmp_gt_u32_e64 s[66:67], s97, v17
	v_sub_u32_e32 v17, v210, v197
	v_cmp_gt_u32_e64 s[64:65], s97, v17
	v_sub_u32_e32 v17, v210, v196
	v_cmp_lt_i32_e64 s[84:85], -9, v1
	v_cmp_gt_u32_e64 s[62:63], s97, v17
	v_sub_u32_e32 v17, v210, v195
	s_nop 4
	v_cndmask_b32_e32 v84, v18, v84, vcc
	s_and_b64 vcc, s[70:71], s[78:79]
	v_cndmask_b32_e32 v85, v18, v85, vcc
	s_and_b64 vcc, s[16:17], s[80:81]
	v_cndmask_b32_e32 v86, v18, v86, vcc
	s_and_b64 vcc, s[66:67], s[82:83]
	v_cndmask_b32_e32 v87, v18, v87, vcc
	s_and_b64 vcc, s[64:65], s[84:85]
	v_cmp_lt_i32_e64 s[86:87], -10, v1
	v_cmp_gt_u32_e64 s[44:45], s97, v17
	v_sub_u32_e32 v17, v210, v194
	v_cndmask_b32_e32 v88, v18, v88, vcc
	s_and_b64 vcc, s[62:63], s[86:87]
	v_cmp_lt_i32_e64 s[88:89], -11, v1
	v_cmp_gt_u32_e64 s[0:1], s97, v17
	v_cndmask_b32_e32 v89, v18, v89, vcc
	s_and_b64 vcc, s[44:45], s[88:89]
	v_cmp_lt_i32_e64 s[90:91], -12, v1
	v_writelane_b32 v255, s0, 54
	v_sub_u32_e32 v17, v210, v193
	v_cndmask_b32_e32 v90, v18, v90, vcc
	v_writelane_b32 v255, s1, 55
	s_and_b64 vcc, s[0:1], s[90:91]
	v_cmp_gt_u32_e64 s[46:47], s97, v17
	s_movk_i32 s0, 0xffef
	v_sub_u32_e32 v17, v210, v192
	v_cmp_lt_i32_e64 s[92:93], s0, v1
	v_cmp_gt_u32_e64 s[52:53], s97, v17
	v_sub_u32_e32 v17, v210, v191
	v_cndmask_b32_e32 v91, v18, v91, vcc
	s_and_b64 vcc, s[46:47], s[92:93]
	v_cmp_lt_i32_e64 s[94:95], s9, v1
	v_cmp_gt_u32_e64 s[48:49], s97, v17
	s_movk_i32 s2, 0x81
	s_movk_i32 s0, 0xffed
	v_sub_u32_e32 v17, v210, v190
	v_cndmask_b32_e32 v92, v18, v92, vcc
	s_and_b64 vcc, s[52:53], s[94:95]
	v_cmp_lt_i32_e64 s[96:97], s0, v1
	v_cmp_gt_u32_e64 s[54:55], s2, v17
	s_movk_i32 s0, 0xffec
	v_sub_u32_e32 v17, v210, v189
	v_cndmask_b32_e32 v93, v18, v93, vcc
	s_and_b64 vcc, s[48:49], s[96:97]
	v_cmp_lt_i32_e64 s[12:13], s0, v1
	v_cmp_gt_u32_e64 s[50:51], s2, v17
	s_movk_i32 s0, 0xffe7
	v_sub_u32_e32 v17, v210, v188
	v_cndmask_b32_e32 v94, v18, v94, vcc
	s_and_b64 vcc, s[54:55], s[12:13]
	v_cmp_lt_i32_e64 s[4:5], s0, v1
	v_cmp_gt_u32_e64 s[56:57], s2, v17
	s_movk_i32 s0, 0xffe6
	v_sub_u32_e32 v17, v210, v187
	v_cndmask_b32_e32 v95, v18, v95, vcc
	s_and_b64 vcc, s[50:51], s[4:5]
	v_cmp_lt_i32_e64 s[0:1], s0, v1
	v_cmp_gt_u32_e64 s[60:61], s2, v17
	s_movk_i32 s3, 0xffe5
	v_sub_u32_e32 v17, v210, v186
	v_cndmask_b32_e32 v96, v18, v96, vcc
	s_and_b64 vcc, s[56:57], s[0:1]
	v_cmp_lt_i32_e64 s[8:9], s3, v1
	v_cmp_gt_u32_e64 s[58:59], s2, v17
	s_movk_i32 s2, 0xffe4
	v_cndmask_b32_e32 v97, v18, v97, vcc
	s_and_b64 vcc, s[60:61], s[8:9]
	v_cmp_lt_i32_e64 s[10:11], s2, v1
	v_cndmask_b32_e32 v98, v18, v98, vcc
	s_and_b64 vcc, s[58:59], s[10:11]
	v_cndmask_b32_e32 v1, v18, v99, vcc
	v_max_f32_e32 v17, v85, v85
	v_max_f32_e32 v99, v84, v84
	v_max_f32_e32 v17, v99, v17
	v_max3_f32 v17, v17, v86, v87
	v_max3_f32 v17, v17, v88, v89
	v_max3_f32 v17, v17, v90, v91
	v_max3_f32 v17, v17, v92, v93
	v_max3_f32 v17, v17, v94, v95
	v_max3_f32 v17, v17, v96, v97
	v_max3_f32 v17, v17, v98, v1
	v_mov_b32_e32 v99, v17
	s_nop 1
	v_permlane32_swap_b32_e32 v17, v99
	v_max3_f32 v17, v243, v17, v99
	v_sub_f32_e32 v84, v84, v17
	v_exp_f32_e32 v84, v84
	v_sub_f32_e32 v85, v85, v17
	v_exp_f32_e32 v85, v85
	v_sub_f32_e32 v86, v86, v17
	v_exp_f32_e32 v86, v86
	v_sub_f32_e32 v87, v87, v17
	v_exp_f32_e32 v87, v87
	v_sub_f32_e32 v88, v88, v17
	v_mfma_f32_32x32x16_bf16 v[52:67], v[168:171], v[152:155], v[52:67]
	v_add_f32_e32 v152, 0, v84
	v_exp_f32_e32 v88, v88
	v_sub_f32_e32 v89, v89, v17
	v_add_f32_e32 v152, v85, v152
	v_exp_f32_e32 v89, v89
	v_sub_f32_e32 v90, v90, v17
	v_add_f32_e32 v152, v86, v152
	v_exp_f32_e32 v90, v90
	v_sub_f32_e32 v91, v91, v17
	v_add_f32_e32 v152, v87, v152
	v_exp_f32_e32 v91, v91
	v_sub_f32_e32 v92, v92, v17
	v_add_f32_e32 v152, v88, v152
	v_exp_f32_e32 v92, v92
	v_sub_f32_e32 v93, v93, v17
	v_add_f32_e32 v152, v89, v152
	v_exp_f32_e32 v93, v93
	v_sub_f32_e32 v94, v94, v17
	v_add_f32_e32 v152, v90, v152
	v_exp_f32_e32 v94, v94
	v_sub_f32_e32 v95, v95, v17
	v_add_f32_e32 v152, v91, v152
	v_exp_f32_e32 v95, v95
	v_sub_f32_e32 v96, v96, v17
	v_add_f32_e32 v152, v92, v152
	v_exp_f32_e32 v96, v96
	v_sub_f32_e32 v97, v97, v17
	s_waitcnt vmcnt(8)
	v_add_f32_e32 v152, v93, v152
	v_exp_f32_e32 v97, v97
	v_sub_f32_e32 v98, v98, v17
	ds_read_b64_tr_b16 v[108:109], v181 offset:0
	v_add_f32_e32 v152, v94, v152
	v_exp_f32_e32 v98, v98
	v_sub_f32_e32 v1, v1, v17
	ds_read_b64_tr_b16 v[110:111], v181 offset:0x400
	v_add_f32_e32 v152, v95, v152
	v_exp_f32_e32 v1, v1
	v_mfma_f32_32x32x16_bf16 v[68:83], v[168:171], v[160:163], v[68:83]
	ds_read_b64_tr_b16 v[112:113], v181 offset:0x800
	v_add_f32_e32 v152, v96, v152
	ds_read_b64_tr_b16 v[114:115], v181 offset:0xc00
	v_add_f32_e32 v152, v97, v152
	ds_read_b64_tr_b16 v[116:117], v181 offset:0x200
	v_sub_f32_e32 v99, v243, v17
	v_add_f32_e32 v152, v98, v152
	ds_read_b64_tr_b16 v[118:119], v181 offset:0x600
	v_add_f32_e32 v153, v1, v152
	v_exp_f32_e32 v152, v99
	ds_read_b64_tr_b16 v[104:105], v181 offset:0xa00
	ds_read_b64_tr_b16 v[106:107], v181 offset:0xe00
	v_mov_b32_e32 v154, v153
	v_cvt_pk_bf16_f32 v84, v84, v85
	v_cvt_pk_bf16_f32 v85, v86, v87
	v_cvt_pk_bf16_f32 v86, v88, v89
	v_cvt_pk_bf16_f32 v87, v90, v91
	v_cvt_pk_bf16_f32 v88, v92, v93
	v_cvt_pk_bf16_f32 v89, v94, v95
	v_cvt_pk_bf16_f32 v90, v96, v97
	v_cvt_pk_bf16_f32 v91, v98, v1
	s_nop 1
	v_permlane32_swap_b32_e32 v153, v154
	v_permlane32_swap_b32_e32 v84, v86
	v_permlane32_swap_b32_e32 v85, v87
	v_permlane32_swap_b32_e32 v88, v90
	v_permlane32_swap_b32_e32 v89, v91
	v_cmp_gt_f32_e32 vcc, 1.0, v152
	s_cbranch_vccz .LBB0_1269
	s_and_saveexec_b64 vcc, s[6:7]
	ds_write_b32 v173, v152
	s_or_b64 exec, exec, vcc
	v_lshl_add_u32 v1, v212, 2, s41
	ds_read_b128 v[92:95], v1 offset:96
	ds_read_b128 v[96:99], v1 offset:64
	ds_read_b128 v[156:159], v1 offset:32
	ds_read_b128 v[160:163], v1
	s_waitcnt lgkmcnt(0)
	v_pk_mul_f32 v[50:51], v[50:51], v[94:95]
	v_pk_mul_f32 v[46:47], v[46:47], v[98:99]
	v_pk_mul_f32 v[42:43], v[42:43], v[158:159]
	v_pk_mul_f32 v[38:39], v[38:39], v[162:163]
	v_pk_mul_f32 v[48:49], v[48:49], v[92:93]
	v_pk_mul_f32 v[44:45], v[44:45], v[96:97]
	v_pk_mul_f32 v[40:41], v[40:41], v[156:157]
	v_pk_mul_f32 v[36:37], v[36:37], v[160:161]
	v_pk_mul_f32 v[34:35], v[34:35], v[94:95]
	v_pk_mul_f32 v[30:31], v[30:31], v[98:99]
	v_pk_mul_f32 v[26:27], v[26:27], v[158:159]
	v_pk_mul_f32 v[22:23], v[22:23], v[162:163]
	v_pk_mul_f32 v[32:33], v[32:33], v[92:93]
	v_pk_mul_f32 v[28:29], v[28:29], v[96:97]
	v_pk_mul_f32 v[24:25], v[24:25], v[156:157]
	v_pk_mul_f32 v[20:21], v[20:21], v[160:161]

.LBB0_1272:
	s_nop 7
	v_max_f32_e32 v1, v85, v85
	v_max_f32_e32 v120, v84, v84
	v_max_f32_e32 v1, v120, v1
	v_max3_f32 v1, v1, v86, v87
	v_max3_f32 v1, v1, v88, v89
	v_max3_f32 v1, v1, v90, v91
	v_max3_f32 v1, v1, v92, v93
	v_max3_f32 v1, v1, v94, v95
	v_max3_f32 v1, v1, v96, v97
	v_max3_f32 v1, v1, v98, v99
	v_mov_b32_e32 v120, v1
	s_nop 1
	v_permlane32_swap_b32_e32 v1, v120
	v_max3_f32 v123, v244, v1, v120
	v_sub_f32_e32 v84, v84, v123
	v_exp_f32_e32 v84, v84
	v_sub_f32_e32 v85, v85, v123
	v_exp_f32_e32 v85, v85
	v_sub_f32_e32 v86, v86, v123
	v_exp_f32_e32 v86, v86
	v_sub_f32_e32 v87, v87, v123
	v_exp_f32_e32 v87, v87
	v_sub_f32_e32 v88, v88, v123
	v_add_f32_e32 v120, 0, v84
	v_exp_f32_e32 v88, v88
	v_sub_f32_e32 v89, v89, v123
	v_add_f32_e32 v120, v85, v120
	v_exp_f32_e32 v89, v89
	v_sub_f32_e32 v90, v90, v123
	v_add_f32_e32 v120, v86, v120
	v_exp_f32_e32 v90, v90
	v_sub_f32_e32 v91, v91, v123
	v_add_f32_e32 v120, v87, v120
	v_exp_f32_e32 v91, v91
	v_sub_f32_e32 v92, v92, v123
	v_add_f32_e32 v120, v88, v120
	v_exp_f32_e32 v92, v92
	v_sub_f32_e32 v93, v93, v123
	v_add_f32_e32 v120, v89, v120
	v_exp_f32_e32 v93, v93
	v_sub_f32_e32 v94, v94, v123
	v_add_f32_e32 v120, v90, v120
	v_exp_f32_e32 v94, v94
	v_sub_f32_e32 v95, v95, v123
	v_add_f32_e32 v120, v91, v120
	v_exp_f32_e32 v95, v95
	v_sub_f32_e32 v96, v96, v123
	v_add_f32_e32 v120, v92, v120
	v_exp_f32_e32 v96, v96
	v_sub_f32_e32 v97, v97, v123
	v_add_f32_e32 v120, v93, v120
	v_exp_f32_e32 v97, v97
	v_sub_f32_e32 v98, v98, v123
	v_add_f32_e32 v120, v94, v120
	v_exp_f32_e32 v98, v98
	v_sub_f32_e32 v99, v99, v123
	v_add_f32_e32 v120, v95, v120
	v_exp_f32_e32 v99, v99
	v_add_f32_e32 v120, v96, v120
	v_add_f32_e32 v120, v97, v120
	v_sub_f32_e32 v1, v244, v123
	v_add_f32_e32 v120, v98, v120
	v_add_f32_e32 v121, v99, v120
	v_exp_f32_e32 v120, v1
	v_mov_b32_e32 v122, v121
	v_cvt_pk_bf16_f32 v84, v84, v85
	v_cvt_pk_bf16_f32 v85, v86, v87
	v_cvt_pk_bf16_f32 v86, v88, v89
	v_cvt_pk_bf16_f32 v87, v90, v91
	v_cvt_pk_bf16_f32 v88, v92, v93
	v_cvt_pk_bf16_f32 v89, v94, v95
	v_cvt_pk_bf16_f32 v90, v96, v97
	v_cvt_pk_bf16_f32 v91, v98, v99
	s_movk_i32 s5, 0xffef
	s_movk_i32 s8, 0xffee
	s_movk_i32 s9, 0xffed
	s_movk_i32 s10, 0xffdf
	s_movk_i32 s33, 0xffdb
	s_movk_i32 s96, 0xffd7
	s_movk_i32 s97, 0xffd3
	v_permlane32_swap_b32_e32 v121, v122
	v_permlane32_swap_b32_e32 v84, v86
	v_permlane32_swap_b32_e32 v85, v87
	v_permlane32_swap_b32_e32 v88, v90
	v_permlane32_swap_b32_e32 v89, v91
	v_cmp_gt_f32_e32 vcc, 1.0, v120
	s_cbranch_vccz .LBB0_1276
	s_and_saveexec_b64 s[0:1], s[6:7]
	ds_write_b32 v173, v120
	s_or_b64 exec, exec, s[0:1]
	v_lshl_add_u32 v1, v212, 2, s41
	ds_read_b128 v[92:95], v1 offset:96
	ds_read_b128 v[96:99], v1 offset:64
	ds_read_b128 v[124:127], v1 offset:32
	ds_read_b128 v[128:131], v1
	s_waitcnt lgkmcnt(0)
	v_pk_mul_f32 v[82:83], v[82:83], v[94:95]
	v_pk_mul_f32 v[78:79], v[78:79], v[98:99]
	v_pk_mul_f32 v[74:75], v[74:75], v[126:127]
	v_pk_mul_f32 v[70:71], v[70:71], v[130:131]
	v_pk_mul_f32 v[80:81], v[80:81], v[92:93]
	v_pk_mul_f32 v[76:77], v[76:77], v[96:97]
	v_pk_mul_f32 v[72:73], v[72:73], v[124:125]
	v_pk_mul_f32 v[68:69], v[68:69], v[128:129]
	v_pk_mul_f32 v[66:67], v[66:67], v[94:95]
	v_pk_mul_f32 v[62:63], v[62:63], v[98:99]
	v_pk_mul_f32 v[58:59], v[58:59], v[126:127]
	v_pk_mul_f32 v[54:55], v[54:55], v[130:131]
	v_pk_mul_f32 v[64:65], v[64:65], v[92:93]
	v_pk_mul_f32 v[60:61], v[60:61], v[96:97]
	v_pk_mul_f32 v[56:57], v[56:57], v[124:125]
	v_pk_mul_f32 v[52:53], v[52:53], v[128:129]
.LBB0_1276:
	s_waitcnt lgkmcnt(0)
	v_or_b32_e32 v1, 0xa0, v212
	v_add_u32_e32 v1, s18, v1
	v_mfma_f32_32x32x16_bf16 v[68:83], v[84:87], v[108:111], v[68:83]
	v_cmp_lt_i32_e64 s[0:1], -1, v1
	s_waitcnt vmcnt(0)
	v_mfma_f32_32x32x16_bf16 v[52:67], v[84:87], v[116:119], v[52:67]
	ds_read_b64_tr_b16 v[116:117], v182 offset:0
	ds_read_b64_tr_b16 v[118:119], v182 offset:0x400
	v_mfma_f32_32x32x16_bf16 v[68:83], v[88:91], v[112:115], v[68:83]
	ds_read_b64_tr_b16 v[112:113], v182 offset:0x800
	ds_read_b64_tr_b16 v[114:115], v182 offset:0xc00
	ds_read_b64_tr_b16 v[108:109], v182 offset:0x200
	ds_read_b64_tr_b16 v[110:111], v182 offset:0x600
	v_mfma_f32_32x32x16_bf16 v[52:67], v[88:91], v[104:107], v[52:67]
	ds_read_b64_tr_b16 v[104:105], v182 offset:0xa00
	ds_read_b64_tr_b16 v[106:107], v182 offset:0xe00
	v_mfma_f32_32x32x16_bf16 v[84:99], v[148:151], v[100:103], 0
	v_mfma_f32_32x32x16_bf16 v[84:99], v[136:139], v[4:7], v[84:99]
	v_add_u32_e32 v4, 0xffffff60, v230
	v_sub_u32_e32 v5, v4, v212
	v_cmp_gt_u32_e32 vcc, s19, v5
	s_and_b64 vcc, vcc, s[0:1]
	v_sub_u32_e32 v6, v4, v204
	v_cmp_lt_i32_e64 s[0:1], -2, v1
	v_sub_u32_e32 v7, v4, v199
	v_mfma_f32_32x32x16_bf16 v[84:99], v[140:143], v[8:11], v[84:99]
	v_sub_u32_e32 v8, v4, v198
	v_sub_u32_e32 v9, v4, v197
	v_sub_u32_e32 v10, v4, v196
	v_sub_u32_e32 v11, v4, v195
	v_mfma_f32_32x32x16_bf16 v[84:99], v[144:147], v[12:15], v[84:99]
	v_sub_u32_e32 v12, v4, v194
	s_nop 10
	v_cndmask_b32_e32 v5, v18, v84, vcc
	v_cmp_gt_u32_e32 vcc, s19, v6
	s_and_b64 vcc, vcc, s[0:1]
	v_cmp_lt_i32_e64 s[0:1], -3, v1
	v_cndmask_b32_e32 v6, v18, v85, vcc
	v_cmp_gt_u32_e32 vcc, s19, v7
	s_and_b64 vcc, vcc, s[0:1]
	v_cmp_lt_i32_e64 s[0:1], -4, v1
	v_cndmask_b32_e32 v7, v18, v86, vcc
	v_cmp_gt_u32_e32 vcc, s19, v8
	s_and_b64 vcc, vcc, s[0:1]
	v_cmp_lt_i32_e64 s[0:1], -9, v1
	v_cndmask_b32_e32 v8, v18, v87, vcc
	v_cmp_gt_u32_e32 vcc, s19, v9
	s_and_b64 vcc, vcc, s[0:1]
	v_cmp_lt_i32_e64 s[0:1], -10, v1
	v_cndmask_b32_e32 v9, v18, v88, vcc
	v_cmp_gt_u32_e32 vcc, s19, v10
	s_and_b64 vcc, vcc, s[0:1]
	v_cmp_lt_i32_e64 s[0:1], -11, v1
	v_cndmask_b32_e32 v10, v18, v89, vcc
	v_cmp_gt_u32_e32 vcc, s19, v11
	s_and_b64 vcc, vcc, s[0:1]
	v_cmp_lt_i32_e64 s[0:1], -12, v1
	v_cndmask_b32_e32 v11, v18, v90, vcc
	v_cmp_gt_u32_e32 vcc, s19, v12
	s_and_b64 vcc, vcc, s[0:1]
	v_sub_u32_e32 v12, v4, v193
	v_cndmask_b32_e32 v13, v18, v91, vcc
	v_cmp_gt_u32_e32 vcc, s19, v12
	v_cmp_lt_i32_e64 s[0:1], s5, v1
	s_and_b64 vcc, vcc, s[0:1]
	v_sub_u32_e32 v12, v4, v192
	v_cndmask_b32_e32 v14, v18, v92, vcc
	v_cmp_gt_u32_e32 vcc, s19, v12
	v_cmp_lt_i32_e64 s[0:1], s8, v1
	s_and_b64 vcc, vcc, s[0:1]
	v_sub_u32_e32 v12, v4, v191
	v_cndmask_b32_e32 v15, v18, v93, vcc
	v_cmp_gt_u32_e32 vcc, s19, v12
	v_cmp_lt_i32_e64 s[0:1], s9, v1
	s_and_b64 vcc, vcc, s[0:1]
	v_sub_u32_e32 v12, v4, v190
	s_movk_i32 s0, 0xffec
	v_cndmask_b32_e32 v84, v18, v94, vcc
	v_cmp_gt_u32_e32 vcc, s19, v12
	v_cmp_lt_i32_e64 s[0:1], s0, v1
	s_and_b64 vcc, vcc, s[0:1]
	v_sub_u32_e32 v12, v4, v189
	s_movk_i32 s0, 0xffe7
	v_cndmask_b32_e32 v85, v18, v95, vcc
	v_cmp_gt_u32_e32 vcc, s19, v12
	v_cmp_lt_i32_e64 s[0:1], s0, v1
	s_and_b64 vcc, vcc, s[0:1]
	v_sub_u32_e32 v12, v4, v188
	s_movk_i32 s0, 0xffe6
	v_cndmask_b32_e32 v86, v18, v96, vcc
	v_cmp_gt_u32_e32 vcc, s19, v12
	v_cmp_lt_i32_e64 s[0:1], s0, v1
	s_and_b64 vcc, vcc, s[0:1]
	v_sub_u32_e32 v12, v4, v187
	s_movk_i32 s0, 0xffe5
	v_cndmask_b32_e32 v87, v18, v97, vcc
	v_cmp_gt_u32_e32 vcc, s19, v12
	v_cmp_lt_i32_e64 s[0:1], s0, v1
	s_and_b64 vcc, vcc, s[0:1]
	v_sub_u32_e32 v4, v4, v186
	v_cndmask_b32_e32 v88, v18, v98, vcc
	v_cmp_gt_u32_e32 vcc, s19, v4
	v_max_f32_e32 v4, v6, v6
	v_max_f32_e32 v12, v5, v5
	v_max_f32_e32 v4, v12, v4
	v_max3_f32 v4, v4, v7, v8
	v_max3_f32 v4, v4, v9, v10
	s_movk_i32 s0, 0xffe4
	v_max3_f32 v4, v4, v11, v13
	v_cmp_lt_i32_e64 s[0:1], s0, v1
	v_max3_f32 v4, v4, v14, v15
	s_and_b64 vcc, vcc, s[0:1]
	v_max3_f32 v4, v4, v84, v85
	v_cndmask_b32_e32 v1, v18, v99, vcc
	v_max3_f32 v4, v4, v86, v87
	v_max3_f32 v4, v4, v88, v1
	v_mov_b32_e32 v12, v4
	s_nop 1
	v_permlane32_swap_b32_e32 v4, v12
	v_max3_f32 v12, v123, v4, v12
	v_sub_f32_e32 v5, v5, v12
	v_exp_f32_e32 v5, v5
	v_sub_f32_e32 v6, v6, v12
	v_exp_f32_e32 v6, v6
	v_sub_f32_e32 v7, v7, v12
	v_exp_f32_e32 v7, v7
	v_sub_f32_e32 v8, v8, v12
	v_exp_f32_e32 v8, v8
	v_sub_f32_e32 v9, v9, v12
	v_add_f32_e32 v89, 0, v5
	v_exp_f32_e32 v9, v9
	v_sub_f32_e32 v10, v10, v12
	v_add_f32_e32 v89, v6, v89
	v_exp_f32_e32 v10, v10
	v_sub_f32_e32 v11, v11, v12
	v_add_f32_e32 v89, v7, v89
	v_exp_f32_e32 v11, v11
	v_sub_f32_e32 v13, v13, v12
	v_add_f32_e32 v89, v8, v89
	v_exp_f32_e32 v90, v13
	v_add_f32_e32 v89, v9, v89
	v_add_f32_e32 v89, v10, v89
	v_add_f32_e32 v89, v11, v89
	v_sub_f32_e32 v14, v14, v12
	v_add_f32_e32 v13, v90, v89
	v_exp_f32_e32 v89, v14
	v_sub_f32_e32 v14, v15, v12
	v_exp_f32_e32 v91, v14
	v_sub_f32_e32 v14, v84, v12
	v_exp_f32_e32 v84, v14
	v_sub_f32_e32 v14, v85, v12
	v_exp_f32_e32 v85, v14
	v_sub_f32_e32 v14, v86, v12
	v_add_f32_e32 v13, v89, v13
	v_exp_f32_e32 v86, v14
	v_sub_f32_e32 v14, v87, v12
	v_add_f32_e32 v13, v91, v13
	v_exp_f32_e32 v87, v14
	v_sub_f32_e32 v14, v88, v12
	v_add_f32_e32 v13, v84, v13
	v_exp_f32_e32 v88, v14
	v_sub_f32_e32 v1, v1, v12
	v_add_f32_e32 v13, v85, v13
	v_exp_f32_e32 v1, v1
	v_add_f32_e32 v13, v86, v13
	v_add_f32_e32 v13, v87, v13
	v_sub_f32_e32 v4, v123, v12
	v_add_f32_e32 v13, v88, v13
	v_add_f32_e32 v14, v1, v13
	v_exp_f32_e32 v13, v4
	v_mov_b32_e32 v15, v14
	v_cvt_pk_bf16_f32 v4, v5, v6
	v_cvt_pk_bf16_f32 v5, v7, v8
	v_cvt_pk_bf16_f32 v6, v9, v10
	v_cvt_pk_bf16_f32 v7, v11, v90
	v_cvt_pk_bf16_f32 v8, v89, v91
	v_cvt_pk_bf16_f32 v9, v84, v85
	v_cvt_pk_bf16_f32 v10, v86, v87
	v_cvt_pk_bf16_f32 v11, v88, v1
	s_nop 1
	v_permlane32_swap_b32_e32 v14, v15
	v_permlane32_swap_b32_e32 v4, v6
	v_permlane32_swap_b32_e32 v5, v7
	v_permlane32_swap_b32_e32 v8, v10
	v_permlane32_swap_b32_e32 v9, v11
	v_cmp_gt_f32_e32 vcc, 1.0, v13
	s_cbranch_vccz .LBB0_1280
	s_and_saveexec_b64 s[0:1], s[6:7]
	ds_write_b32 v173, v13
	s_or_b64 exec, exec, s[0:1]
	v_lshl_add_u32 v1, v212, 2, s41
	ds_read_b128 v[84:87], v1 offset:96
	ds_read_b128 v[88:91], v1 offset:64
	ds_read_b128 v[92:95], v1 offset:32
	ds_read_b128 v[96:99], v1
	s_waitcnt lgkmcnt(0)
	v_pk_mul_f32 v[82:83], v[82:83], v[86:87]
	v_pk_mul_f32 v[78:79], v[78:79], v[90:91]
	v_pk_mul_f32 v[74:75], v[74:75], v[94:95]
	v_pk_mul_f32 v[70:71], v[70:71], v[98:99]
	v_pk_mul_f32 v[80:81], v[80:81], v[84:85]
	v_pk_mul_f32 v[76:77], v[76:77], v[88:89]
	v_pk_mul_f32 v[72:73], v[72:73], v[92:93]
	v_pk_mul_f32 v[68:69], v[68:69], v[96:97]
	v_pk_mul_f32 v[66:67], v[66:67], v[86:87]
	v_pk_mul_f32 v[62:63], v[62:63], v[90:91]
	v_pk_mul_f32 v[58:59], v[58:59], v[94:95]
	v_pk_mul_f32 v[54:55], v[54:55], v[98:99]
	v_pk_mul_f32 v[64:65], v[64:65], v[84:85]
	v_pk_mul_f32 v[60:61], v[60:61], v[88:89]
	v_pk_mul_f32 v[56:57], v[56:57], v[92:93]
	v_pk_mul_f32 v[52:53], v[52:53], v[96:97]

.LBB0_1284:
	s_or_b64 exec, exec, s[0:1]
	v_or_b32_e32 v1, s38, v212
	s_waitcnt lgkmcnt(0)
	v_lshl_add_u32 v1, v1, 7, v183
	v_cvt_pk_bf16_f32 v5, v68, v3
	ds_write_b16 v1, v5
	v_cvt_pk_bf16_f32 v5, v52, v3
	ds_write_b16 v1, v5 offset:64
	v_cvt_pk_bf16_f32 v1, v69, v3
	ds_write_b16 v4, v1 offset:4224
	v_cvt_pk_bf16_f32 v1, v53, v3
	ds_write_b16 v4, v1 offset:4288
	v_cvt_pk_bf16_f32 v1, v70, v3
	ds_write_b16 v4, v1 offset:4352
	v_cvt_pk_bf16_f32 v1, v54, v3
	ds_write_b16 v4, v1 offset:4416
	v_cvt_pk_bf16_f32 v1, v71, v3
	ds_write_b16 v4, v1 offset:4480
	v_cvt_pk_bf16_f32 v1, v55, v3
	ds_write_b16 v4, v1 offset:4544
	v_cvt_pk_bf16_f32 v1, v72, v3
	ds_write_b16 v4, v1 offset:5120
	v_cvt_pk_bf16_f32 v1, v56, v3
	ds_write_b16 v4, v1 offset:5184
	v_cvt_pk_bf16_f32 v1, v73, v3
	ds_write_b16 v4, v1 offset:5248
	v_cvt_pk_bf16_f32 v1, v57, v3
	ds_write_b16 v4, v1 offset:5312
	v_cvt_pk_bf16_f32 v1, v74, v3
	ds_write_b16 v4, v1 offset:5376
	v_cvt_pk_bf16_f32 v1, v58, v3
	ds_write_b16 v4, v1 offset:5440
	v_cvt_pk_bf16_f32 v1, v75, v3
	ds_write_b16 v4, v1 offset:5504
	v_cvt_pk_bf16_f32 v1, v59, v3
	ds_write_b16 v4, v1 offset:5568
	v_cvt_pk_bf16_f32 v1, v76, v3
	ds_write_b16 v4, v1 offset:6144
	v_cvt_pk_bf16_f32 v1, v60, v3
	ds_write_b16 v4, v1 offset:6208
	v_cvt_pk_bf16_f32 v1, v77, v3
	ds_write_b16 v4, v1 offset:6272
	v_cvt_pk_bf16_f32 v1, v61, v3
	ds_write_b16 v4, v1 offset:6336
	v_cvt_pk_bf16_f32 v1, v78, v3
	ds_write_b16 v4, v1 offset:6400
	v_cvt_pk_bf16_f32 v1, v62, v3
	ds_write_b16 v4, v1 offset:6464
	v_cvt_pk_bf16_f32 v1, v79, v3
	ds_write_b16 v4, v1 offset:6528
	v_cvt_pk_bf16_f32 v1, v63, v3
	ds_write_b16 v4, v1 offset:6592
	v_cvt_pk_bf16_f32 v1, v80, v3
	ds_write_b16 v4, v1 offset:7168
	v_cvt_pk_bf16_f32 v1, v64, v3
	ds_write_b16 v4, v1 offset:7232
	v_cvt_pk_bf16_f32 v1, v81, v3
	ds_write_b16 v4, v1 offset:7296
	v_cvt_pk_bf16_f32 v1, v65, v3
	ds_write_b16 v4, v1 offset:7360
	v_cvt_pk_bf16_f32 v1, v82, v3
	ds_write_b16 v4, v1 offset:7424
	v_cvt_pk_bf16_f32 v1, v66, v3
	ds_write_b16 v4, v1 offset:7488
	v_cvt_pk_bf16_f32 v1, v83, v3
	s_lshl_b32 s41, s37, 4
	ds_write_b16 v4, v1 offset:7552
	v_cvt_pk_bf16_f32 v1, v67, v3
	s_andn2_b32 s41, s41, 63
	ds_write_b16 v4, v1 offset:7616
	s_bfe_u32 s40, s39, 0x20006
	v_or_b32_e32 v1, s41, v210
	s_or_b32 s39, s41, 32
	v_or_b32_e32 v150, s39, v210
	s_or_b32 s3, s40, s26
	v_lshlrev_b32_e32 v214, 2, v1
	s_lshl_b32 s0, s37, 8
	v_add_u32_e32 v1, s3, v214
	v_mov_b64_e32 v[4:5], s[22:23]
	v_lshlrev_b32_e32 v213, 2, v150
	v_writelane_b32 v255, s0, 56
	s_add_i32 s38, s0, 0
	v_mad_i64_i32 v[6:7], s[0:1], v1, s4, v[4:5]
	v_add_u32_e32 v1, s3, v213
	s_add_i32 s2, s41, 0xffffff80
	v_mad_i64_i32 v[4:5], s[0:1], v1, s4, v[4:5]
	v_or_b32_e32 v1, s2, v210
	v_lshl_add_u32 v1, v1, 2, s3
	v_mov_b32_e32 v179, v3
	v_med3_i32 v1, v1, 0, v227
	v_lshl_add_u64 v[12:13], v[4:5], 0, v[178:179]
	v_mul_u32_u24_e32 v4, 0xa00, v1
	v_or_b32_e32 v1, s2, v211
	v_lshl_add_u32 v1, v1, 2, s3
	v_mov_b32_e32 v5, v3
	v_med3_i32 v1, v1, 0, v227
	v_lshl_add_u64 v[8:9], v[6:7], 0, v[178:179]
	v_mul_u32_u24_e32 v6, 0xa00, v1
	v_mov_b32_e32 v7, v3
	v_lshl_add_u64 v[4:5], v[4:5], 1, s[22:23]
	v_lshl_add_u64 v[6:7], v[6:7], 1, s[22:23]
	v_lshl_add_u64 v[26:27], v[4:5], 0, v[178:179]
	s_waitcnt lgkmcnt(0)
	s_waitcnt vmcnt(0) lgkmcnt(0)
	s_barrier
	v_lshl_add_u64 v[24:25], v[6:7], 0, v[178:179]
	global_load_dwordx4 v[20:23], v[26:27], off offset:3072
	global_load_dwordx4 v[130:133], v[8:9], off offset:2048
	global_load_dwordx4 v[126:129], v[8:9], off offset:2080
	global_load_dwordx4 v[114:117], v[12:13], off offset:2048
	global_load_dwordx4 v[4:7], v[12:13], off offset:2080
	global_load_dwordx4 v[122:125], v[8:9], off offset:2112
	global_load_dwordx4 v[118:121], v[8:9], off offset:2144
	s_nop 0
	global_load_dwordx4 v[8:11], v[12:13], off offset:2112
	s_nop 0
	global_load_dwordx4 v[12:15], v[12:13], off offset:2144
	v_or_b32_e32 v1, s2, v209
	global_load_dwordx4 v[36:39], v[26:27], off offset:3104
	global_load_dwordx4 v[40:43], v[26:27], off offset:3136
	global_load_dwordx4 v[44:47], v[26:27], off offset:3168
	v_lshl_add_u32 v1, v1, 2, s3
	v_med3_i32 v1, v1, 0, v227
	v_mul_u32_u24_e32 v26, 0xa00, v1
	v_mov_b32_e32 v27, v3
	v_or_b32_e32 v1, s2, v208
	v_lshl_add_u64 v[26:27], v[26:27], 1, s[20:21]
	v_mov_b32_e32 v17, v3
	v_lshl_add_u32 v1, v1, 2, s3
	s_mov_b32 m0, s27
	v_lshl_add_u64 v[26:27], v[26:27], 0, v[16:17]
	v_med3_i32 v1, v1, 0, v227
	global_load_lds_dwordx4 v[26:27], off
	v_mul_u32_u24_e32 v26, 0xa00, v1
	v_mov_b32_e32 v27, v3
	v_or_b32_e32 v1, s2, v207
	v_lshl_add_u64 v[26:27], v[26:27], 1, s[20:21]
	v_lshl_add_u32 v1, v1, 2, s3
	v_lshl_add_u64 v[26:27], v[26:27], 0, v[16:17]
	s_mov_b32 m0, s30
	v_med3_i32 v1, v1, 0, v227
	global_load_lds_dwordx4 v[26:27], off
	v_mul_u32_u24_e32 v26, 0xa00, v1
	v_mov_b32_e32 v27, v3
	v_or_b32_e32 v1, s2, v206
	v_lshl_add_u64 v[26:27], v[26:27], 1, s[20:21]
	v_lshl_add_u32 v1, v1, 2, s3
	s_lshl_b32 s18, s2, 2
	v_lshl_add_u64 v[26:27], v[26:27], 0, v[16:17]
	s_mov_b32 m0, s28
	v_med3_i32 v1, v1, 0, v227
	s_add_i32 s18, s18, s3
	global_load_lds_dwordx4 v[26:27], off
	v_mul_u32_u24_e32 v26, 0xa00, v1
	v_mov_b32_e32 v27, v3
	s_or_b32 s0, s18, 0x80
	v_lshl_add_u64 v[26:27], v[26:27], 1, s[20:21]
	v_lshlrev_b32_e32 v241, 2, v209
	v_lshl_add_u64 v[26:27], v[26:27], 0, v[16:17]
	s_mov_b32 m0, s29
	v_or_b32_e32 v1, s0, v241
	global_load_lds_dwordx4 v[26:27], off
	v_med3_i32 v1, v1, 0, v227
	global_load_dwordx4 v[82:85], v[24:25], off offset:3072
	global_load_dwordx4 v[86:89], v[24:25], off offset:3104
	global_load_dwordx4 v[90:93], v[24:25], off offset:3136
	global_load_dwordx4 v[94:97], v[24:25], off offset:3168
	v_mul_u32_u24_e32 v24, 0xa00, v1
	v_mov_b32_e32 v25, v3
	v_lshlrev_b32_e32 v240, 2, v208
	v_lshl_add_u64 v[24:25], v[24:25], 1, s[20:21]
	v_or_b32_e32 v1, s0, v240
	v_lshl_add_u64 v[24:25], v[24:25], 0, v[16:17]
	s_mov_b32 m0, s36
	v_med3_i32 v1, v1, 0, v227
	global_load_lds_dwordx4 v[24:25], off
	v_mul_u32_u24_e32 v24, 0xa00, v1
	v_mov_b32_e32 v25, v3
	v_lshlrev_b32_e32 v238, 2, v207
	v_lshl_add_u64 v[24:25], v[24:25], 1, s[20:21]
	v_or_b32_e32 v1, s0, v238
	v_lshl_add_u64 v[24:25], v[24:25], 0, v[16:17]
	s_mov_b32 m0, s34
	v_med3_i32 v1, v1, 0, v227
	global_load_lds_dwordx4 v[24:25], off
	v_mul_u32_u24_e32 v24, 0xa00, v1
	v_mov_b32_e32 v25, v3
	v_lshl_add_u64 v[24:25], v[24:25], 1, s[20:21]
	v_lshl_add_u64 v[48:49], v[24:25], 0, v[16:17]
	s_waitcnt vmcnt(0)
	v_mfma_f32_32x32x16_bf16 v[20:35], v[20:23], v[130:133], 0
	v_lshlrev_b32_e32 v239, 2, v206
	v_or_b32_e32 v1, s0, v239
	s_mov_b32 m0, s31
	v_med3_i32 v1, v1, 0, v227
	global_load_lds_dwordx4 v[48:49], off
	v_mul_u32_u24_e32 v48, 0xa00, v1
	v_mfma_f32_32x32x16_bf16 v[20:35], v[36:39], v[126:129], v[20:35]
	v_mov_b32_e32 v49, v3
	v_lshl_add_u64 v[36:37], v[48:49], 1, s[20:21]
	v_lshl_add_u64 v[36:37], v[36:37], 0, v[16:17]
	s_mov_b32 m0, s35
	s_add_i32 s38, s38, 0x21400
	global_load_lds_dwordx4 v[36:37], off
	v_mfma_f32_32x32x16_bf16 v[20:35], v[40:43], v[122:125], v[20:35]
	s_cmp_gt_i32 s18, -1
	v_readlane_b32 s0, v255, 22
	s_cselect_b64 s[94:95], -1, 0
	v_readlane_b32 s1, v255, 23
	v_or_b32_e32 v19, s18, v2
	s_and_b64 vcc, s[0:1], s[94:95]
	v_readlane_b32 s0, v255, 24
	v_mfma_f32_32x32x16_bf16 v[20:35], v[44:47], v[118:121], v[20:35]
	v_readlane_b32 s1, v255, 25
	s_waitcnt vmcnt(8)
	ds_read_b64_tr_b16 v[78:79], v181 offset:0
	ds_read_b64_tr_b16 v[80:81], v181 offset:0x400
	ds_read_b64_tr_b16 v[74:75], v181 offset:0x800
	ds_read_b64_tr_b16 v[76:77], v181 offset:0xc00
	ds_read_b64_tr_b16 v[70:71], v181 offset:0x200
	s_nop 10
	v_cndmask_b32_e32 v1, v18, v20, vcc
	v_cmp_lt_i32_e32 vcc, -5, v19
	s_and_b64 vcc, s[0:1], vcc
	v_readlane_b32 s0, v255, 26
	v_cndmask_b32_e32 v17, v18, v21, vcc
	v_cmp_lt_i32_e32 vcc, -9, v19
	v_readlane_b32 s1, v255, 27
	s_and_b64 vcc, s[0:1], vcc
	v_readlane_b32 s0, v255, 28
	v_cndmask_b32_e32 v20, v18, v22, vcc
	v_cmp_lt_i32_e32 vcc, -13, v19
	v_readlane_b32 s1, v255, 29
	s_and_b64 vcc, s[0:1], vcc
	v_readlane_b32 s0, v255, 30
	v_cndmask_b32_e32 v21, v18, v23, vcc
	v_cmp_lt_i32_e32 vcc, s10, v19
	v_readlane_b32 s1, v255, 31
	s_and_b64 vcc, s[0:1], vcc
	v_readlane_b32 s0, v255, 32
	v_cndmask_b32_e32 v22, v18, v24, vcc
	v_cmp_lt_i32_e32 vcc, s33, v19
	v_readlane_b32 s1, v255, 33
	s_and_b64 vcc, s[0:1], vcc
	v_readlane_b32 s0, v255, 34
	v_cndmask_b32_e32 v23, v18, v25, vcc
	v_cmp_lt_i32_e32 vcc, s96, v19
	v_readlane_b32 s1, v255, 35
	s_and_b64 vcc, s[0:1], vcc
	v_readlane_b32 s0, v255, 36
	v_cndmask_b32_e32 v24, v18, v26, vcc
	v_cmp_lt_i32_e32 vcc, s97, v19
	v_readlane_b32 s1, v255, 37
	s_and_b64 vcc, s[0:1], vcc
	s_movk_i32 s0, 0xffbf
	v_cndmask_b32_e32 v25, v18, v27, vcc
	v_cmp_lt_i32_e32 vcc, s0, v19
	v_readlane_b32 s0, v255, 38
	v_readlane_b32 s1, v255, 39
	s_and_b64 vcc, s[0:1], vcc
	s_movk_i32 s0, 0xffbb
	v_cndmask_b32_e32 v26, v18, v28, vcc
	v_cmp_lt_i32_e32 vcc, s0, v19
	v_readlane_b32 s0, v255, 40
	v_readlane_b32 s1, v255, 41
	s_and_b64 vcc, s[0:1], vcc
	s_movk_i32 s0, 0xffb7
	v_cndmask_b32_e32 v27, v18, v29, vcc
	v_cmp_lt_i32_e32 vcc, s0, v19
	v_readlane_b32 s0, v255, 42
	v_readlane_b32 s1, v255, 43
	s_and_b64 vcc, s[0:1], vcc
	s_movk_i32 s0, 0xffb3
	v_cndmask_b32_e32 v28, v18, v30, vcc
	v_cmp_lt_i32_e32 vcc, s0, v19
	v_readlane_b32 s0, v255, 44
	v_readlane_b32 s1, v255, 45
	s_and_b64 vcc, s[0:1], vcc
	s_movk_i32 s0, 0xff9f
	v_cndmask_b32_e32 v29, v18, v31, vcc
	v_cmp_lt_i32_e32 vcc, s0, v19
	v_readlane_b32 s0, v255, 46
	v_readlane_b32 s1, v255, 47
	s_and_b64 vcc, s[0:1], vcc
	s_movk_i32 s0, 0xff9b
	v_cndmask_b32_e32 v30, v18, v32, vcc
	v_cmp_lt_i32_e32 vcc, s0, v19
	v_readlane_b32 s0, v255, 48
	v_readlane_b32 s1, v255, 49
	s_and_b64 vcc, s[0:1], vcc
	s_movk_i32 s0, 0xff97
	v_cndmask_b32_e32 v31, v18, v33, vcc
	v_cmp_lt_i32_e32 vcc, s0, v19
	v_readlane_b32 s0, v255, 50
	v_readlane_b32 s1, v255, 51
	s_and_b64 vcc, s[0:1], vcc
	s_movk_i32 s0, 0xff93
	v_cndmask_b32_e32 v32, v18, v34, vcc
	v_cmp_lt_i32_e32 vcc, s0, v19
	v_readlane_b32 s0, v255, 52
	v_readlane_b32 s1, v255, 53
	s_and_b64 vcc, s[0:1], vcc
	v_cndmask_b32_e32 v33, v18, v35, vcc
	v_max_f32_e32 v34, v17, v17
	v_max_f32_e32 v35, v1, v1
	v_max_f32_e32 v34, v35, v34
	v_max3_f32 v34, v34, v20, v21
	v_max3_f32 v34, v34, v22, v23
	v_max3_f32 v34, v34, v24, v25
	v_max3_f32 v34, v34, v26, v27
	v_max3_f32 v34, v34, v28, v29
	v_max3_f32 v34, v34, v30, v31
	v_max3_f32 v34, v34, v32, v33
	v_mov_b32_e32 v35, v34
	s_nop 1
	v_permlane32_swap_b32_e32 v34, v35
	s_mov_b32 s0, 0xf149f2ca
	v_max3_f32 v152, v34, v35, s0
	v_sub_f32_e32 v1, v1, v152
	v_exp_f32_e32 v1, v1
	v_sub_f32_e32 v17, v17, v152
	v_exp_f32_e32 v17, v17
	v_sub_f32_e32 v20, v20, v152
	v_exp_f32_e32 v35, v20
	v_sub_f32_e32 v20, v21, v152
	v_exp_f32_e32 v21, v20
	v_sub_f32_e32 v22, v22, v152
	v_add_f32_e32 v20, 0, v1
	v_exp_f32_e32 v22, v22
	v_sub_f32_e32 v23, v23, v152
	v_add_f32_e32 v20, v17, v20
	v_exp_f32_e32 v23, v23
	v_sub_f32_e32 v24, v24, v152
	v_add_f32_e32 v20, v35, v20
	v_exp_f32_e32 v24, v24
	v_sub_f32_e32 v25, v25, v152
	v_add_f32_e32 v20, v21, v20
	v_exp_f32_e32 v25, v25
	v_sub_f32_e32 v26, v26, v152
	v_add_f32_e32 v20, v22, v20
	v_exp_f32_e32 v26, v26
	v_sub_f32_e32 v27, v27, v152
	v_add_f32_e32 v20, v23, v20
	v_exp_f32_e32 v27, v27
	v_sub_f32_e32 v28, v28, v152
	v_add_f32_e32 v20, v24, v20
	v_exp_f32_e32 v28, v28
	v_sub_f32_e32 v29, v29, v152
	v_add_f32_e32 v20, v25, v20
	v_exp_f32_e32 v29, v29
	v_sub_f32_e32 v30, v30, v152
	v_add_f32_e32 v20, v26, v20
	v_exp_f32_e32 v30, v30
	v_sub_f32_e32 v31, v31, v152
	v_add_f32_e32 v20, v27, v20
	v_exp_f32_e32 v31, v31
	v_sub_f32_e32 v32, v32, v152
	v_add_f32_e32 v20, v28, v20
	v_exp_f32_e32 v32, v32
	v_sub_f32_e32 v33, v33, v152
	v_add_f32_e32 v20, v29, v20
	v_exp_f32_e32 v33, v33
	v_sub_f32_e32 v34, 0xf149f2ca, v152
	v_add_f32_e32 v20, v30, v20
	ds_read_b64_tr_b16 v[72:73], v181 offset:0x600
	v_add_f32_e32 v20, v31, v20
	v_exp_f32_e32 v229, v34
	ds_read_b64_tr_b16 v[66:67], v181 offset:0xa00
	v_add_f32_e32 v20, v32, v20
	ds_read_b64_tr_b16 v[68:69], v181 offset:0xe00
	v_add_f32_e32 v230, v33, v20
	v_mov_b32_e32 v231, v230
	v_cvt_pk_bf16_f32 v20, v1, v17
	v_cvt_pk_bf16_f32 v21, v35, v21
	v_cvt_pk_bf16_f32 v22, v22, v23
	v_cvt_pk_bf16_f32 v23, v24, v25
	v_cvt_pk_bf16_f32 v24, v26, v27
	v_cvt_pk_bf16_f32 v25, v28, v29
	v_cvt_pk_bf16_f32 v26, v30, v31
	v_cvt_pk_bf16_f32 v27, v32, v33
	v_lshl_add_u32 v185, v210, 2, s38
	s_nop 0
	v_permlane32_swap_b32_e32 v230, v231
	v_permlane32_swap_b32_e32 v20, v22
	v_permlane32_swap_b32_e32 v21, v23
	v_permlane32_swap_b32_e32 v24, v26
	v_permlane32_swap_b32_e32 v25, v27
	v_cmp_gt_f32_e32 vcc, 1.0, v229
	s_cbranch_vccz .LBB0_1288
	s_and_saveexec_b64 s[0:1], s[6:7]
	ds_write_b32 v185, v229
	s_or_b64 exec, exec, s[0:1]
	v_lshl_add_u32 v1, v212, 2, s38
	ds_read_b128 v[28:31], v1 offset:96
	ds_read_b128 v[32:35], v1 offset:64
	ds_read_b128 v[38:41], v1 offset:32
	ds_read_b128 v[50:53], v1
	s_waitcnt lgkmcnt(0)
	v_pk_mul_f32 v[48:49], v[30:31], 0 op_sel_hi:[1,0]
	v_pk_mul_f32 v[44:45], v[34:35], 0 op_sel_hi:[1,0]
	v_pk_mul_f32 v[40:41], v[40:41], 0 op_sel_hi:[1,0]
	v_pk_mul_f32 v[36:37], v[52:53], 0 op_sel_hi:[1,0]
	v_pk_mul_f32 v[46:47], v[28:29], 0 op_sel_hi:[1,0]
	v_pk_mul_f32 v[42:43], v[32:33], 0 op_sel_hi:[1,0]
	v_pk_mul_f32 v[38:39], v[38:39], 0 op_sel_hi:[1,0]
	v_pk_mul_f32 v[34:35], v[50:51], 0 op_sel_hi:[1,0]
	s_branch .LBB0_1289

.LBB0_1291:
	s_nop 10
	v_max_f32_e32 v1, v67, v67
	v_max_f32_e32 v17, v66, v66
	v_max_f32_e32 v1, v17, v1
	v_max3_f32 v1, v1, v68, v69
	v_max3_f32 v1, v1, v70, v71
	v_max3_f32 v1, v1, v72, v73
	v_max3_f32 v1, v1, v74, v75
	v_max3_f32 v1, v1, v76, v77
	v_max3_f32 v1, v1, v78, v79
	v_max3_f32 v1, v1, v80, v81
	v_mov_b32_e32 v17, v1
	s_nop 1
	v_permlane32_swap_b32_e32 v1, v17
	v_max3_f32 v28, v152, v1, v17
	v_sub_f32_e32 v17, v66, v28
	v_exp_f32_e32 v17, v17
	v_sub_f32_e32 v19, v67, v28
	v_exp_f32_e32 v20, v19
	v_sub_f32_e32 v19, v68, v28
	v_exp_f32_e32 v21, v19
	v_sub_f32_e32 v19, v69, v28
	v_exp_f32_e32 v22, v19
	v_sub_f32_e32 v23, v70, v28
	v_add_f32_e32 v19, 0, v17
	v_exp_f32_e32 v23, v23
	v_sub_f32_e32 v24, v71, v28
	v_add_f32_e32 v19, v20, v19
	v_exp_f32_e32 v24, v24
	v_sub_f32_e32 v25, v72, v28
	v_add_f32_e32 v19, v21, v19
	v_exp_f32_e32 v25, v25
	v_sub_f32_e32 v26, v73, v28
	v_add_f32_e32 v19, v22, v19
	v_exp_f32_e32 v26, v26
	v_sub_f32_e32 v27, v74, v28
	v_add_f32_e32 v19, v23, v19
	v_exp_f32_e32 v27, v27
	v_sub_f32_e32 v29, v75, v28
	v_add_f32_e32 v19, v24, v19
	v_exp_f32_e32 v29, v29
	v_sub_f32_e32 v30, v76, v28
	v_add_f32_e32 v19, v25, v19
	v_exp_f32_e32 v30, v30
	v_sub_f32_e32 v31, v77, v28
	v_add_f32_e32 v19, v26, v19
	v_exp_f32_e32 v31, v31
	v_sub_f32_e32 v32, v78, v28
	v_add_f32_e32 v19, v27, v19
	v_exp_f32_e32 v32, v32
	v_sub_f32_e32 v33, v79, v28
	v_add_f32_e32 v19, v29, v19
	v_exp_f32_e32 v33, v33
	v_sub_f32_e32 v66, v80, v28
	v_add_f32_e32 v19, v30, v19
	v_exp_f32_e32 v66, v66
	v_sub_f32_e32 v67, v81, v28
	v_add_f32_e32 v19, v31, v19
	v_exp_f32_e32 v67, v67
	v_add_f32_e32 v19, v32, v19
	v_add_f32_e32 v19, v33, v19
	v_sub_f32_e32 v1, v152, v28
	v_add_f32_e32 v19, v66, v19
	v_add_f32_e32 v232, v67, v19
	v_exp_f32_e32 v19, v1
	v_mov_b32_e32 v233, v232
	v_cvt_pk_bf16_f32 v20, v17, v20
	v_cvt_pk_bf16_f32 v21, v21, v22
	v_cvt_pk_bf16_f32 v22, v23, v24
	v_cvt_pk_bf16_f32 v23, v25, v26
	v_cvt_pk_bf16_f32 v24, v27, v29
	v_cvt_pk_bf16_f32 v25, v30, v31
	v_cvt_pk_bf16_f32 v26, v32, v33
	v_cvt_pk_bf16_f32 v27, v66, v67
	s_nop 1
	v_permlane32_swap_b32_e32 v232, v233
	v_permlane32_swap_b32_e32 v20, v22
	v_permlane32_swap_b32_e32 v21, v23
	v_permlane32_swap_b32_e32 v24, v26
	v_permlane32_swap_b32_e32 v25, v27
	v_cmp_gt_f32_e32 vcc, 1.0, v19
	s_movk_i32 s8, 0xffdf
	s_cbranch_vccz .LBB0_1295
	s_and_saveexec_b64 s[0:1], s[6:7]
	ds_write_b32 v185, v19
	s_or_b64 exec, exec, s[0:1]
	v_lshl_add_u32 v1, v212, 2, s38
	ds_read_b128 v[30:33], v1 offset:96
	ds_read_b128 v[66:69], v1 offset:64
	ds_read_b128 v[70:73], v1 offset:32
	ds_read_b128 v[74:77], v1
	s_waitcnt lgkmcnt(0)
	v_pk_mul_f32 v[64:65], v[64:65], v[32:33]
	v_pk_mul_f32 v[60:61], v[60:61], v[68:69]
	v_pk_mul_f32 v[56:57], v[56:57], v[72:73]
	v_pk_mul_f32 v[52:53], v[52:53], v[76:77]
	v_pk_mul_f32 v[62:63], v[62:63], v[30:31]
	v_pk_mul_f32 v[58:59], v[58:59], v[66:67]
	v_pk_mul_f32 v[54:55], v[54:55], v[70:71]
	v_pk_mul_f32 v[50:51], v[50:51], v[74:75]
	v_pk_mul_f32 v[48:49], v[48:49], v[32:33]
	v_pk_mul_f32 v[44:45], v[44:45], v[68:69]
	v_pk_mul_f32 v[40:41], v[40:41], v[72:73]
	v_pk_mul_f32 v[36:37], v[36:37], v[76:77]
	v_pk_mul_f32 v[46:47], v[46:47], v[30:31]
	v_pk_mul_f32 v[42:43], v[42:43], v[66:67]
	v_pk_mul_f32 v[38:39], v[38:39], v[70:71]
	v_pk_mul_f32 v[34:35], v[34:35], v[74:75]
.LBB0_1295:
	s_waitcnt lgkmcnt(0)
	v_subrev_u32_e32 v237, s2, v150
	v_mfma_f32_32x32x16_bf16 v[66:81], v[82:85], v[114:117], 0
	v_subrev_u32_e32 v1, 32, v237
	v_sub_u32_e32 v17, v1, v212
	v_cmp_gt_u32_e32 vcc, s19, v17
	s_and_b64 vcc, vcc, s[94:95]
	v_cmp_lt_i32_e64 s[0:1], -5, v151
	v_sub_u32_e32 v29, v1, v192
	v_sub_u32_e32 v30, v1, v191
	v_mfma_f32_32x32x16_bf16 v[66:81], v[86:89], v[4:7], v[66:81]
	v_sub_u32_e32 v31, v1, v190
	v_sub_u32_e32 v32, v1, v189
	v_sub_u32_e32 v33, v1, v188
	v_mfma_f32_32x32x16_bf16 v[66:81], v[90:93], v[8:11], v[66:81]
	v_mfma_f32_32x32x16_bf16 v[66:81], v[94:97], v[12:15], v[66:81]
	v_mfma_f32_32x32x16_bf16 v[50:65], v[20:23], v[110:113], v[50:65]
	s_nop 10
	v_cndmask_b32_e32 v17, v18, v66, vcc
	v_sub_u32_e32 v66, v1, v187
	v_mfma_f32_32x32x16_bf16 v[34:49], v[20:23], v[102:105], v[34:49]
	v_sub_u32_e32 v20, v1, v204
	v_cmp_gt_u32_e32 vcc, s19, v20
	s_and_b64 vcc, vcc, s[0:1]
	v_sub_u32_e32 v21, v1, v199
	v_cndmask_b32_e32 v20, v18, v67, vcc
	v_cmp_gt_u32_e32 vcc, s19, v21
	v_cmp_lt_i32_e64 s[0:1], -9, v151
	s_and_b64 vcc, vcc, s[0:1]
	v_sub_u32_e32 v22, v1, v198
	v_cndmask_b32_e32 v21, v18, v68, vcc
	v_cmp_gt_u32_e32 vcc, s19, v22
	v_cmp_lt_i32_e64 s[0:1], -13, v151
	s_and_b64 vcc, vcc, s[0:1]
	v_sub_u32_e32 v23, v1, v197
	v_cndmask_b32_e32 v22, v18, v69, vcc
	v_cmp_gt_u32_e32 vcc, s19, v23
	v_cmp_lt_i32_e64 s[0:1], s8, v151
	v_mfma_f32_32x32x16_bf16 v[50:65], v[24:27], v[106:109], v[50:65]
	s_and_b64 vcc, vcc, s[0:1]
	v_cndmask_b32_e32 v23, v18, v70, vcc
	v_cmp_lt_i32_e64 s[0:1], s33, v151
	v_max_f32_e32 v67, v20, v20
	v_max_f32_e32 v68, v17, v17
	v_max_f32_e32 v67, v68, v67
	v_max3_f32 v67, v67, v21, v22
	v_mfma_f32_32x32x16_bf16 v[34:49], v[24:27], v[98:101], v[34:49]
	v_sub_u32_e32 v24, v1, v196
	v_cmp_gt_u32_e32 vcc, s19, v24
	s_and_b64 vcc, vcc, s[0:1]
	v_sub_u32_e32 v25, v1, v195
	v_cndmask_b32_e32 v24, v18, v71, vcc
	v_cmp_gt_u32_e32 vcc, s19, v25
	v_cmp_lt_i32_e64 s[0:1], s96, v151
	s_and_b64 vcc, vcc, s[0:1]
	v_sub_u32_e32 v26, v1, v194
	v_cndmask_b32_e32 v25, v18, v72, vcc
	v_cmp_gt_u32_e32 vcc, s19, v26
	v_cmp_lt_i32_e64 s[0:1], s97, v151
	s_and_b64 vcc, vcc, s[0:1]
	v_sub_u32_e32 v27, v1, v193
	s_movk_i32 s0, 0xffbf
	v_cndmask_b32_e32 v26, v18, v73, vcc
	v_cmp_gt_u32_e32 vcc, s19, v27
	v_cmp_lt_i32_e64 s[0:1], s0, v151
	s_and_b64 vcc, vcc, s[0:1]
	s_movk_i32 s0, 0xffbb
	v_cndmask_b32_e32 v27, v18, v74, vcc
	v_cmp_gt_u32_e32 vcc, s19, v29
	v_cmp_lt_i32_e64 s[0:1], s0, v151
	s_and_b64 vcc, vcc, s[0:1]
	s_movk_i32 s0, 0xffb7
	v_cndmask_b32_e32 v29, v18, v75, vcc
	v_cmp_gt_u32_e32 vcc, s19, v30
	v_cmp_lt_i32_e64 s[0:1], s0, v151
	s_and_b64 vcc, vcc, s[0:1]
	s_movk_i32 s0, 0xffb3
	v_cndmask_b32_e32 v30, v18, v76, vcc
	v_cmp_gt_u32_e32 vcc, s19, v31
	v_cmp_lt_i32_e64 s[0:1], s0, v151
	s_and_b64 vcc, vcc, s[0:1]
	s_movk_i32 s0, 0xff9f
	v_cndmask_b32_e32 v31, v18, v77, vcc
	v_cmp_gt_u32_e32 vcc, s19, v32
	v_cmp_lt_i32_e64 s[0:1], s0, v151
	s_and_b64 vcc, vcc, s[0:1]
	s_movk_i32 s0, 0xff9b
	v_cndmask_b32_e32 v32, v18, v78, vcc
	v_cmp_gt_u32_e32 vcc, s19, v33
	v_cmp_lt_i32_e64 s[0:1], s0, v151
	s_and_b64 vcc, vcc, s[0:1]
	s_movk_i32 s0, 0xff97
	v_cndmask_b32_e32 v33, v18, v79, vcc
	v_cmp_gt_u32_e32 vcc, s19, v66
	v_cmp_lt_i32_e64 s[0:1], s0, v151
	v_max3_f32 v67, v67, v23, v24
	s_and_b64 vcc, vcc, s[0:1]
	v_sub_u32_e32 v1, v1, v186
	s_movk_i32 s0, 0xff93
	v_max3_f32 v67, v67, v25, v26
	v_cndmask_b32_e32 v66, v18, v80, vcc
	v_cmp_gt_u32_e32 vcc, s19, v1
	v_cmp_lt_i32_e64 s[0:1], s0, v151
	v_max3_f32 v67, v67, v27, v29
	s_and_b64 vcc, vcc, s[0:1]
	v_max3_f32 v67, v67, v30, v31
	v_cndmask_b32_e32 v1, v18, v81, vcc
	v_max3_f32 v67, v67, v32, v33
	v_max3_f32 v67, v67, v66, v1
	v_mov_b32_e32 v68, v67
	s_nop 1
	v_permlane32_swap_b32_e32 v67, v68
	s_mov_b32 s0, 0xf149f2ca
	v_max3_f32 v234, v67, v68, s0
	v_sub_f32_e32 v17, v17, v234
	v_exp_f32_e32 v17, v17
	v_sub_f32_e32 v20, v20, v234
	v_exp_f32_e32 v20, v20
	v_sub_f32_e32 v21, v21, v234
	v_exp_f32_e32 v21, v21
	v_sub_f32_e32 v22, v22, v234
	v_exp_f32_e32 v22, v22
	v_sub_f32_e32 v23, v23, v234
	v_add_f32_e32 v68, 0, v17
	v_exp_f32_e32 v23, v23
	v_sub_f32_e32 v24, v24, v234
	v_add_f32_e32 v68, v20, v68
	v_exp_f32_e32 v69, v24
	v_add_f32_e32 v68, v21, v68
	v_add_f32_e32 v68, v22, v68
	v_add_f32_e32 v68, v23, v68
	v_sub_f32_e32 v25, v25, v234
	v_add_f32_e32 v24, v69, v68
	v_exp_f32_e32 v68, v25
	v_sub_f32_e32 v25, v26, v234
	v_exp_f32_e32 v70, v25
	v_sub_f32_e32 v25, v27, v234
	v_exp_f32_e32 v71, v25
	v_sub_f32_e32 v25, v29, v234
	v_exp_f32_e32 v29, v25
	v_sub_f32_e32 v25, v30, v234
	v_add_f32_e32 v24, v68, v24
	v_exp_f32_e32 v30, v25
	v_sub_f32_e32 v25, v31, v234
	v_add_f32_e32 v24, v70, v24
	v_exp_f32_e32 v31, v25
	v_sub_f32_e32 v25, v32, v234
	v_add_f32_e32 v24, v71, v24
	v_exp_f32_e32 v72, v25
	v_sub_f32_e32 v25, v33, v234
	v_add_f32_e32 v24, v29, v24
	v_exp_f32_e32 v73, v25
	v_sub_f32_e32 v25, v66, v234
	v_add_f32_e32 v24, v30, v24
	v_exp_f32_e32 v66, v25
	v_sub_f32_e32 v1, v1, v234
	v_add_f32_e32 v24, v31, v24
	v_exp_f32_e32 v1, v1
	v_sub_f32_e32 v67, 0xf149f2ca, v234
	v_add_f32_e32 v24, v72, v24
	v_add_f32_e32 v24, v73, v24
	v_exp_f32_e32 v32, v67
	v_add_f32_e32 v24, v66, v24
	v_add_f32_e32 v33, v1, v24
	v_mov_b32_e32 v215, v33
	v_cvt_pk_bf16_f32 v24, v17, v20
	v_cvt_pk_bf16_f32 v25, v21, v22
	v_cvt_pk_bf16_f32 v26, v23, v69
	v_cvt_pk_bf16_f32 v27, v68, v70
	v_cvt_pk_bf16_f32 v20, v71, v29
	v_cvt_pk_bf16_f32 v21, v30, v31
	v_cvt_pk_bf16_f32 v22, v72, v73
	v_cvt_pk_bf16_f32 v23, v66, v1
	s_nop 1
	v_permlane32_swap_b32_e32 v33, v215
	v_permlane32_swap_b32_e32 v24, v26
	v_permlane32_swap_b32_e32 v25, v27
	v_permlane32_swap_b32_e32 v20, v22
	v_permlane32_swap_b32_e32 v21, v23
	v_cmp_gt_f32_e32 vcc, 1.0, v32
	s_cbranch_vccz .LBB0_1299
	s_and_saveexec_b64 s[0:1], s[6:7]
	ds_write_b32 v185, v32
	s_or_b64 exec, exec, s[0:1]
	v_lshl_add_u32 v1, v212, 2, s38
	ds_read_b128 v[66:69], v1 offset:96
	ds_read_b128 v[70:73], v1 offset:64
	ds_read_b128 v[82:85], v1 offset:32
	ds_read_b128 v[86:89], v1
	s_waitcnt lgkmcnt(0)
	v_pk_mul_f32 v[80:81], v[68:69], 0 op_sel_hi:[1,0]
	v_pk_mul_f32 v[76:77], v[72:73], 0 op_sel_hi:[1,0]
	v_pk_mul_f32 v[72:73], v[84:85], 0 op_sel_hi:[1,0]
	v_pk_mul_f32 v[68:69], v[88:89], 0 op_sel_hi:[1,0]
	v_pk_mul_f32 v[78:79], v[66:67], 0 op_sel_hi:[1,0]
	v_pk_mul_f32 v[74:75], v[70:71], 0 op_sel_hi:[1,0]
	v_pk_mul_f32 v[70:71], v[82:83], 0 op_sel_hi:[1,0]
	v_pk_mul_f32 v[66:67], v[86:87], 0 op_sel_hi:[1,0]
	s_branch .LBB0_1300

.LBB0_1302:
	s_nop 10
	v_max_f32_e32 v1, v99, v99
	v_max_f32_e32 v17, v98, v98
	v_max_f32_e32 v1, v17, v1
	v_max3_f32 v1, v1, v100, v101
	v_max3_f32 v1, v1, v102, v103
	v_max3_f32 v1, v1, v104, v105
	v_max3_f32 v1, v1, v106, v107
	v_max3_f32 v1, v1, v108, v109
	v_max3_f32 v1, v1, v110, v111
	v_max3_f32 v1, v1, v112, v113
	v_mov_b32_e32 v17, v1
	s_nop 1
	v_permlane32_swap_b32_e32 v1, v17
	v_max3_f32 v247, v28, v1, v17
	v_sub_f32_e32 v17, v98, v247
	v_exp_f32_e32 v17, v17
	v_sub_f32_e32 v24, v99, v247
	v_exp_f32_e32 v24, v24
	v_sub_f32_e32 v25, v100, v247
	v_exp_f32_e32 v25, v25
	v_sub_f32_e32 v26, v101, v247
	v_sub_f32_e32 v1, v28, v247
	v_exp_f32_e32 v26, v26
	v_sub_f32_e32 v28, v102, v247
	v_add_f32_e32 v27, 0, v17
	v_exp_f32_e32 v28, v28
	v_sub_f32_e32 v29, v103, v247
	v_add_f32_e32 v27, v24, v27
	v_exp_f32_e32 v29, v29
	v_sub_f32_e32 v30, v104, v247
	v_add_f32_e32 v27, v25, v27
	v_exp_f32_e32 v30, v30
	v_sub_f32_e32 v31, v105, v247
	v_add_f32_e32 v27, v26, v27
	v_exp_f32_e32 v31, v31
	v_sub_f32_e32 v98, v106, v247
	v_add_f32_e32 v27, v28, v27
	v_exp_f32_e32 v98, v98
	v_sub_f32_e32 v99, v107, v247
	v_add_f32_e32 v27, v29, v27
	v_exp_f32_e32 v99, v99
	v_sub_f32_e32 v100, v108, v247
	v_add_f32_e32 v27, v30, v27
	v_exp_f32_e32 v100, v100
	v_sub_f32_e32 v101, v109, v247
	v_add_f32_e32 v27, v31, v27
	v_exp_f32_e32 v101, v101
	v_sub_f32_e32 v102, v110, v247
	v_add_f32_e32 v27, v98, v27
	v_exp_f32_e32 v102, v102
	v_sub_f32_e32 v103, v111, v247
	v_add_f32_e32 v27, v99, v27
	v_exp_f32_e32 v103, v103
	v_sub_f32_e32 v104, v112, v247
	v_add_f32_e32 v27, v100, v27
	v_exp_f32_e32 v104, v104
	v_sub_f32_e32 v105, v113, v247
	v_add_f32_e32 v27, v101, v27
	v_exp_f32_e32 v105, v105
	v_add_f32_e32 v27, v102, v27
	v_add_f32_e32 v27, v103, v27
	v_exp_f32_e32 v242, v1
	v_add_f32_e32 v27, v104, v27
	v_add_f32_e32 v243, v105, v27
	v_mov_b32_e32 v244, v243
	v_cvt_pk_bf16_f32 v24, v17, v24
	v_cvt_pk_bf16_f32 v25, v25, v26
	v_cvt_pk_bf16_f32 v26, v28, v29
	v_cvt_pk_bf16_f32 v27, v30, v31
	v_cvt_pk_bf16_f32 v28, v98, v99
	v_cvt_pk_bf16_f32 v29, v100, v101
	v_cvt_pk_bf16_f32 v30, v102, v103
	v_cvt_pk_bf16_f32 v31, v104, v105
	s_nop 1
	v_permlane32_swap_b32_e32 v243, v244
	v_permlane32_swap_b32_e32 v24, v26
	v_permlane32_swap_b32_e32 v25, v27
	v_permlane32_swap_b32_e32 v28, v30
	v_permlane32_swap_b32_e32 v29, v31
	v_cmp_gt_f32_e32 vcc, 1.0, v242
	s_cbranch_vccz .LBB0_1306
	s_and_saveexec_b64 s[0:1], s[6:7]
	ds_write_b32 v185, v242
	s_or_b64 exec, exec, s[0:1]
	v_lshl_add_u32 v1, v212, 2, s38
	ds_read_b128 v[98:101], v1 offset:96
	ds_read_b128 v[102:105], v1 offset:64
	ds_read_b128 v[106:109], v1 offset:32
	ds_read_b128 v[110:113], v1
	s_waitcnt lgkmcnt(0)
	v_pk_mul_f32 v[64:65], v[64:65], v[100:101]
	v_pk_mul_f32 v[60:61], v[60:61], v[104:105]
	v_pk_mul_f32 v[56:57], v[56:57], v[108:109]
	v_pk_mul_f32 v[52:53], v[52:53], v[112:113]
	v_pk_mul_f32 v[62:63], v[62:63], v[98:99]
	v_pk_mul_f32 v[58:59], v[58:59], v[102:103]
	v_pk_mul_f32 v[54:55], v[54:55], v[106:107]
	v_pk_mul_f32 v[50:51], v[50:51], v[110:111]
	v_pk_mul_f32 v[48:49], v[48:49], v[100:101]
	v_pk_mul_f32 v[44:45], v[44:45], v[104:105]
	v_pk_mul_f32 v[40:41], v[40:41], v[108:109]
	v_pk_mul_f32 v[36:37], v[36:37], v[112:113]
	v_pk_mul_f32 v[46:47], v[46:47], v[98:99]
	v_pk_mul_f32 v[42:43], v[42:43], v[102:103]
	v_pk_mul_f32 v[38:39], v[38:39], v[106:107]
	v_pk_mul_f32 v[34:35], v[34:35], v[110:111]

.LBB0_1308:
	s_nop 10
	v_max_f32_e32 v1, v99, v99
	v_max_f32_e32 v17, v98, v98
	v_max_f32_e32 v1, v17, v1
	v_max3_f32 v1, v1, v100, v101
	v_max3_f32 v1, v1, v102, v103
	v_max3_f32 v1, v1, v104, v105
	v_max3_f32 v1, v1, v106, v107
	v_max3_f32 v1, v1, v108, v109
	v_max3_f32 v1, v1, v110, v111
	v_max3_f32 v1, v1, v112, v113
	v_mov_b32_e32 v17, v1
	s_nop 1
	v_permlane32_swap_b32_e32 v1, v17
	v_max3_f32 v142, v234, v1, v17
	v_sub_f32_e32 v17, v98, v142
	v_exp_f32_e32 v17, v17
	v_sub_f32_e32 v24, v99, v142
	v_exp_f32_e32 v24, v24
	v_sub_f32_e32 v25, v100, v142
	v_exp_f32_e32 v25, v25
	v_sub_f32_e32 v26, v101, v142
	v_exp_f32_e32 v26, v26
	v_sub_f32_e32 v28, v102, v142
	v_add_f32_e32 v27, 0, v17
	v_exp_f32_e32 v28, v28
	v_sub_f32_e32 v29, v103, v142
	v_add_f32_e32 v27, v24, v27
	v_exp_f32_e32 v29, v29
	v_sub_f32_e32 v30, v104, v142
	v_add_f32_e32 v27, v25, v27
	v_exp_f32_e32 v30, v30
	v_sub_f32_e32 v31, v105, v142
	v_add_f32_e32 v27, v26, v27
	v_exp_f32_e32 v31, v31
	v_sub_f32_e32 v98, v106, v142
	v_add_f32_e32 v27, v28, v27
	v_exp_f32_e32 v98, v98
	v_sub_f32_e32 v99, v107, v142
	v_add_f32_e32 v27, v29, v27
	v_exp_f32_e32 v99, v99
	v_sub_f32_e32 v100, v108, v142
	v_add_f32_e32 v27, v30, v27
	v_exp_f32_e32 v100, v100
	v_sub_f32_e32 v101, v109, v142
	v_add_f32_e32 v27, v31, v27
	v_exp_f32_e32 v101, v101
	v_sub_f32_e32 v102, v110, v142
	v_add_f32_e32 v27, v98, v27
	v_exp_f32_e32 v106, v102
	v_sub_f32_e32 v102, v111, v142
	v_add_f32_e32 v27, v99, v27
	v_exp_f32_e32 v107, v102
	v_sub_f32_e32 v102, v112, v142
	v_add_f32_e32 v27, v100, v27
	v_exp_f32_e32 v108, v102
	v_sub_f32_e32 v102, v113, v142
	v_add_f32_e32 v27, v101, v27
	v_exp_f32_e32 v109, v102
	v_sub_f32_e32 v1, v234, v142
	v_add_f32_e32 v27, v106, v27
	v_add_f32_e32 v27, v107, v27
	v_exp_f32_e32 v234, v1
	v_add_f32_e32 v27, v108, v27
	v_add_f32_e32 v235, v109, v27
	v_mov_b32_e32 v236, v235
	v_cvt_pk_bf16_f32 v102, v17, v24
	v_cvt_pk_bf16_f32 v103, v25, v26
	v_cvt_pk_bf16_f32 v104, v28, v29
	v_cvt_pk_bf16_f32 v105, v30, v31
	v_cvt_pk_bf16_f32 v98, v98, v99
	v_cvt_pk_bf16_f32 v99, v100, v101
	v_cvt_pk_bf16_f32 v100, v106, v107
	v_cvt_pk_bf16_f32 v101, v108, v109
	s_nop 1
	v_permlane32_swap_b32_e32 v235, v236
	v_permlane32_swap_b32_e32 v102, v104
	v_permlane32_swap_b32_e32 v103, v105
	v_permlane32_swap_b32_e32 v98, v100
	v_permlane32_swap_b32_e32 v99, v101
	v_cmp_gt_f32_e32 vcc, 1.0, v234
	s_cbranch_vccz .LBB0_1312
	s_and_saveexec_b64 s[0:1], s[6:7]
	ds_write_b32 v185, v234
	s_or_b64 exec, exec, s[0:1]
	v_lshl_add_u32 v1, v212, 2, s38
	ds_read_b128 v[24:27], v1 offset:96
	ds_read_b128 v[28:31], v1 offset:64
	ds_read_b128 v[106:109], v1 offset:32
	ds_read_b128 v[110:113], v1
	s_waitcnt lgkmcnt(0)
	v_pk_mul_f32 v[96:97], v[96:97], v[26:27]
	v_pk_mul_f32 v[92:93], v[92:93], v[30:31]
	v_pk_mul_f32 v[88:89], v[88:89], v[108:109]
	v_pk_mul_f32 v[84:85], v[84:85], v[112:113]
	v_pk_mul_f32 v[94:95], v[94:95], v[24:25]
	v_pk_mul_f32 v[90:91], v[90:91], v[28:29]
	v_pk_mul_f32 v[86:87], v[86:87], v[106:107]
	v_pk_mul_f32 v[82:83], v[82:83], v[110:111]
	v_pk_mul_f32 v[80:81], v[80:81], v[26:27]
	v_pk_mul_f32 v[76:77], v[76:77], v[30:31]
	v_pk_mul_f32 v[72:73], v[72:73], v[108:109]
	v_pk_mul_f32 v[68:69], v[68:69], v[112:113]
	v_pk_mul_f32 v[78:79], v[78:79], v[24:25]
	v_pk_mul_f32 v[74:75], v[74:75], v[28:29]
	v_pk_mul_f32 v[70:71], v[70:71], v[106:107]
	v_pk_mul_f32 v[66:67], v[66:67], v[110:111]

.LBB0_1314:
	s_nop 10
	v_max_f32_e32 v1, v99, v99
	v_max_f32_e32 v17, v98, v98
	v_max_f32_e32 v1, v17, v1
	v_max3_f32 v1, v1, v100, v101
	v_max3_f32 v1, v1, v102, v103
	v_max3_f32 v1, v1, v104, v105
	v_max3_f32 v1, v1, v106, v107
	v_max3_f32 v1, v1, v108, v109
	v_max3_f32 v1, v1, v110, v111
	v_max3_f32 v1, v1, v112, v113
	v_mov_b32_e32 v17, v1
	s_nop 1
	v_permlane32_swap_b32_e32 v1, v17
	v_max3_f32 v249, v247, v1, v17
	v_sub_f32_e32 v17, v98, v249
	v_exp_f32_e32 v17, v17
	v_sub_f32_e32 v98, v99, v249
	v_exp_f32_e32 v98, v98
	v_sub_f32_e32 v99, v100, v249
	v_exp_f32_e32 v99, v99
	v_sub_f32_e32 v100, v101, v249
	v_exp_f32_e32 v100, v100
	v_sub_f32_e32 v102, v102, v249
	v_add_f32_e32 v101, 0, v17
	v_exp_f32_e32 v102, v102
	v_sub_f32_e32 v103, v103, v249
	v_add_f32_e32 v101, v98, v101
	v_exp_f32_e32 v103, v103
	v_sub_f32_e32 v104, v104, v249
	v_add_f32_e32 v101, v99, v101
	v_exp_f32_e32 v104, v104
	v_sub_f32_e32 v105, v105, v249
	v_add_f32_e32 v101, v100, v101
	v_exp_f32_e32 v105, v105
	v_sub_f32_e32 v106, v106, v249
	v_add_f32_e32 v101, v102, v101
	v_exp_f32_e32 v106, v106
	v_sub_f32_e32 v107, v107, v249
	v_add_f32_e32 v101, v103, v101
	v_exp_f32_e32 v107, v107
	v_sub_f32_e32 v108, v108, v249
	v_add_f32_e32 v101, v104, v101
	v_exp_f32_e32 v108, v108
	v_sub_f32_e32 v109, v109, v249
	v_add_f32_e32 v101, v105, v101
	v_exp_f32_e32 v109, v109
	v_sub_f32_e32 v110, v110, v249
	v_add_f32_e32 v101, v106, v101
	v_exp_f32_e32 v110, v110
	v_sub_f32_e32 v111, v111, v249
	v_add_f32_e32 v101, v107, v101
	v_exp_f32_e32 v111, v111
	v_sub_f32_e32 v112, v112, v249
	v_add_f32_e32 v101, v108, v101
	v_exp_f32_e32 v112, v112
	v_sub_f32_e32 v113, v113, v249
	v_add_f32_e32 v101, v109, v101
	v_exp_f32_e32 v113, v113
	v_sub_f32_e32 v1, v247, v249
	v_add_f32_e32 v101, v110, v101
	v_add_f32_e32 v101, v111, v101
	v_exp_f32_e32 v245, v1
	v_add_f32_e32 v101, v112, v101
	v_add_f32_e32 v246, v113, v101
	v_mov_b32_e32 v247, v246
	v_cvt_pk_bf16_f32 v98, v17, v98
	v_cvt_pk_bf16_f32 v99, v99, v100
	v_cvt_pk_bf16_f32 v100, v102, v103
	v_cvt_pk_bf16_f32 v101, v104, v105
	v_cvt_pk_bf16_f32 v102, v106, v107
	v_cvt_pk_bf16_f32 v103, v108, v109
	v_cvt_pk_bf16_f32 v104, v110, v111
	v_cvt_pk_bf16_f32 v105, v112, v113
	s_nop 1
	v_permlane32_swap_b32_e32 v246, v247
	v_permlane32_swap_b32_e32 v98, v100
	v_permlane32_swap_b32_e32 v99, v101
	v_permlane32_swap_b32_e32 v102, v104
	v_permlane32_swap_b32_e32 v103, v105
	v_cmp_gt_f32_e32 vcc, 1.0, v245
	s_cbranch_vccz .LBB0_1318
	s_and_saveexec_b64 s[0:1], s[6:7]
	ds_write_b32 v185, v245
	s_or_b64 exec, exec, s[0:1]
	v_lshl_add_u32 v1, v212, 2, s38
	ds_read_b128 v[106:109], v1 offset:96
	ds_read_b128 v[110:113], v1 offset:64
	ds_read_b128 v[144:147], v1 offset:32
	ds_read_b128 v[200:203], v1
	s_waitcnt lgkmcnt(0)
	v_pk_mul_f32 v[64:65], v[64:65], v[108:109]
	v_pk_mul_f32 v[60:61], v[60:61], v[112:113]
	v_pk_mul_f32 v[56:57], v[56:57], v[146:147]
	v_pk_mul_f32 v[52:53], v[52:53], v[202:203]
	v_pk_mul_f32 v[62:63], v[62:63], v[106:107]
	v_pk_mul_f32 v[58:59], v[58:59], v[110:111]
	v_pk_mul_f32 v[54:55], v[54:55], v[144:145]
	v_pk_mul_f32 v[50:51], v[50:51], v[200:201]
	v_pk_mul_f32 v[48:49], v[48:49], v[108:109]
	v_pk_mul_f32 v[44:45], v[44:45], v[112:113]
	v_pk_mul_f32 v[40:41], v[40:41], v[146:147]
	v_pk_mul_f32 v[36:37], v[36:37], v[202:203]
	v_pk_mul_f32 v[46:47], v[46:47], v[106:107]
	v_pk_mul_f32 v[42:43], v[42:43], v[110:111]
	v_pk_mul_f32 v[38:39], v[38:39], v[144:145]
	v_pk_mul_f32 v[34:35], v[34:35], v[200:201]

.LBB0_1320:
	s_nop 10
	v_max_f32_e32 v1, v99, v99
	v_max_f32_e32 v17, v98, v98
	v_max_f32_e32 v1, v17, v1
	v_max3_f32 v1, v1, v100, v101
	v_max3_f32 v1, v1, v102, v103
	v_max3_f32 v1, v1, v104, v105
	v_max3_f32 v1, v1, v106, v107
	v_max3_f32 v1, v1, v108, v109
	v_max3_f32 v1, v1, v110, v111
	v_max3_f32 v1, v1, v112, v113
	v_mov_b32_e32 v17, v1
	s_nop 1
	v_permlane32_swap_b32_e32 v1, v17
	v_max3_f32 v161, v142, v1, v17
	v_sub_f32_e32 v17, v98, v161
	v_exp_f32_e32 v17, v17
	v_sub_f32_e32 v98, v99, v161
	v_exp_f32_e32 v98, v98
	v_sub_f32_e32 v99, v100, v161
	v_exp_f32_e32 v99, v99
	v_sub_f32_e32 v100, v101, v161
	v_exp_f32_e32 v100, v100
	v_sub_f32_e32 v102, v102, v161
	v_add_f32_e32 v101, 0, v17
	v_exp_f32_e32 v102, v102
	v_sub_f32_e32 v103, v103, v161
	v_add_f32_e32 v101, v98, v101
	v_exp_f32_e32 v103, v103
	v_sub_f32_e32 v104, v104, v161
	v_add_f32_e32 v101, v99, v101
	v_exp_f32_e32 v104, v104
	v_sub_f32_e32 v105, v105, v161
	v_add_f32_e32 v101, v100, v101
	v_exp_f32_e32 v105, v105
	v_sub_f32_e32 v106, v106, v161
	v_add_f32_e32 v101, v102, v101
	v_exp_f32_e32 v106, v106
	v_sub_f32_e32 v107, v107, v161
	v_add_f32_e32 v101, v103, v101
	v_exp_f32_e32 v107, v107
	v_sub_f32_e32 v108, v108, v161
	v_add_f32_e32 v101, v104, v101
	v_exp_f32_e32 v108, v108
	v_sub_f32_e32 v109, v109, v161
	v_add_f32_e32 v101, v105, v101
	v_exp_f32_e32 v109, v109
	v_sub_f32_e32 v110, v110, v161
	v_add_f32_e32 v101, v106, v101
	v_exp_f32_e32 v110, v110
	v_sub_f32_e32 v111, v111, v161
	v_add_f32_e32 v101, v107, v101
	v_exp_f32_e32 v111, v111
	v_sub_f32_e32 v112, v112, v161
	v_add_f32_e32 v101, v108, v101
	v_exp_f32_e32 v112, v112
	v_sub_f32_e32 v113, v113, v161
	v_add_f32_e32 v101, v109, v101
	v_exp_f32_e32 v113, v113
	v_sub_f32_e32 v1, v142, v161
	v_add_f32_e32 v101, v110, v101
	v_add_f32_e32 v101, v111, v101
	v_exp_f32_e32 v158, v1
	v_add_f32_e32 v101, v112, v101
	v_add_f32_e32 v159, v113, v101
	v_mov_b32_e32 v160, v159
	v_cvt_pk_bf16_f32 v98, v17, v98
	v_cvt_pk_bf16_f32 v99, v99, v100
	v_cvt_pk_bf16_f32 v100, v102, v103
	v_cvt_pk_bf16_f32 v101, v104, v105
	v_cvt_pk_bf16_f32 v154, v106, v107
	v_cvt_pk_bf16_f32 v155, v108, v109
	v_cvt_pk_bf16_f32 v156, v110, v111
	v_cvt_pk_bf16_f32 v157, v112, v113
	s_nop 1
	v_permlane32_swap_b32_e32 v159, v160
	v_permlane32_swap_b32_e32 v98, v100
	v_permlane32_swap_b32_e32 v99, v101
	v_permlane32_swap_b32_e32 v154, v156
	v_permlane32_swap_b32_e32 v155, v157
	v_cmp_gt_f32_e32 vcc, 1.0, v158
	s_cbranch_vccz .LBB0_1324
	s_and_saveexec_b64 s[0:1], s[6:7]
	ds_write_b32 v185, v158
	s_or_b64 exec, exec, s[0:1]
	v_lshl_add_u32 v1, v212, 2, s38
	ds_read_b128 v[102:105], v1 offset:96
	ds_read_b128 v[106:109], v1 offset:64
	ds_read_b128 v[110:113], v1 offset:32
	ds_read_b128 v[142:145], v1
	s_waitcnt lgkmcnt(0)
	v_pk_mul_f32 v[96:97], v[96:97], v[104:105]
	v_pk_mul_f32 v[92:93], v[92:93], v[108:109]
	v_pk_mul_f32 v[88:89], v[88:89], v[112:113]
	v_pk_mul_f32 v[84:85], v[84:85], v[144:145]
	v_pk_mul_f32 v[94:95], v[94:95], v[102:103]
	v_pk_mul_f32 v[90:91], v[90:91], v[106:107]
	v_pk_mul_f32 v[86:87], v[86:87], v[110:111]
	v_pk_mul_f32 v[82:83], v[82:83], v[142:143]
	v_pk_mul_f32 v[80:81], v[80:81], v[104:105]
	v_pk_mul_f32 v[76:77], v[76:77], v[108:109]
	v_pk_mul_f32 v[72:73], v[72:73], v[112:113]
	v_pk_mul_f32 v[68:69], v[68:69], v[144:145]
	v_pk_mul_f32 v[78:79], v[78:79], v[102:103]
	v_pk_mul_f32 v[74:75], v[74:75], v[106:107]
	v_pk_mul_f32 v[70:71], v[70:71], v[110:111]
	v_pk_mul_f32 v[66:67], v[66:67], v[142:143]
.LBB0_1324:
	v_or_b32_e32 v1, 0x280, v248
	v_add_u32_e32 v1, s18, v1
	v_med3_i32 v1, v1, 0, v227
	v_mul_u32_u24_e32 v102, 0xa00, v1
	v_mov_b32_e32 v103, v3
	s_waitcnt lgkmcnt(0)
	v_lshl_add_u64 v[102:103], v[102:103], 1, s[22:23]
	v_mov_b32_e32 v179, v3
	s_movk_i32 s42, 0xffd3
	s_movk_i32 s33, 0xffd7
	s_movk_i32 s19, 0xffdb
	s_add_i32 s0, s18, 0x280
	v_or_b32_e32 v1, 0x200, v2
	v_lshl_add_u64 v[102:103], v[102:103], 0, v[178:179]
	v_add_u32_e32 v1, s18, v1
	v_or_b32_e32 v17, s0, v241
	v_mfma_f32_32x32x16_bf16 v[82:97], v[98:101], v[138:141], v[82:97]
	v_med3_i32 v17, v17, 0, v227
	global_load_dwordx4 v[150:153], v[102:103], off offset:3072
	global_load_dwordx4 v[138:141], v[102:103], off offset:3104
	global_load_dwordx4 v[142:145], v[102:103], off offset:3136
	global_load_dwordx4 v[146:149], v[102:103], off offset:3168
	v_mul_u32_u24_e32 v102, 0xa00, v17
	v_mov_b32_e32 v103, v3
	v_lshl_add_u64 v[102:103], v[102:103], 1, s[20:21]
	v_mov_b32_e32 v17, v3
	s_mov_b32 m0, s36
	v_mfma_f32_32x32x16_bf16 v[66:81], v[98:101], v[170:173], v[66:81]
	v_or_b32_e32 v98, s0, v240
	v_med3_i32 v98, v98, 0, v227
	v_mul_u32_u24_e32 v98, 0xa00, v98
	v_mov_b32_e32 v99, v3
	v_lshl_add_u64 v[102:103], v[102:103], 0, v[16:17]
	v_lshl_add_u64 v[98:99], v[98:99], 1, s[20:21]
	global_load_lds_dwordx4 v[102:103], off
	v_lshl_add_u64 v[162:163], v[98:99], 0, v[16:17]
	s_waitcnt vmcnt(0)
	v_mfma_f32_32x32x16_bf16 v[98:113], v[134:137], v[130:133], 0
	v_or_b32_e32 v130, s0, v238
	v_med3_i32 v130, v130, 0, v227
	v_mul_u32_u24_e32 v130, 0xa00, v130
	v_mov_b32_e32 v131, v3
	s_mov_b32 m0, s34
	v_lshl_add_u64 v[130:131], v[130:131], 1, s[20:21]
	global_load_lds_dwordx4 v[162:163], off
	v_mfma_f32_32x32x16_bf16 v[98:113], v[28:31], v[126:129], v[98:113]
	v_or_b32_e32 v126, s0, v239
	v_med3_i32 v126, v126, 0, v227
	v_mul_u32_u24_e32 v126, 0xa00, v126
	v_mov_b32_e32 v127, v3
	v_lshl_add_u64 v[130:131], v[130:131], 0, v[16:17]
	s_mov_b32 m0, s31
	v_lshl_add_u64 v[126:127], v[126:127], 1, s[20:21]
	global_load_lds_dwordx4 v[130:131], off
	v_lshl_add_u64 v[126:127], v[126:127], 0, v[16:17]
	s_mov_b32 m0, s35
	v_mfma_f32_32x32x16_bf16 v[98:113], v[24:27], v[122:125], v[98:113]
	global_load_lds_dwordx4 v[126:127], off
	v_cmp_lt_i32_e64 s[92:93], -1, v1
	s_and_b64 vcc, s[14:15], s[92:93]
	v_cmp_lt_i32_e64 s[88:89], -5, v1
	v_cmp_lt_i32_e64 s[96:97], -9, v1
	v_cmp_lt_i32_e64 s[94:95], -13, v1
	v_mfma_f32_32x32x16_bf16 v[98:113], v[20:23], v[118:121], v[98:113]
	v_cmp_lt_i32_e64 s[90:91], s8, v1
	v_cmp_lt_i32_e64 s[86:87], s19, v1
	v_cmp_lt_i32_e64 s[84:85], s33, v1
	v_readlane_b32 s0, v255, 54
	v_cmp_lt_i32_e64 s[82:83], s42, v1
	v_readlane_b32 s1, v255, 55
	s_waitcnt vmcnt(8)
	s_nop 5
	v_cndmask_b32_e32 v17, v18, v98, vcc
	s_and_b64 vcc, s[70:71], s[88:89]
	v_cndmask_b32_e32 v98, v18, v99, vcc
	s_and_b64 vcc, s[16:17], s[96:97]
	v_cndmask_b32_e32 v99, v18, v100, vcc
	s_and_b64 vcc, s[66:67], s[94:95]
	v_cndmask_b32_e32 v100, v18, v101, vcc
	s_and_b64 vcc, s[64:65], s[90:91]
	v_cndmask_b32_e32 v101, v18, v102, vcc
	s_and_b64 vcc, s[62:63], s[86:87]
	v_cndmask_b32_e32 v102, v18, v103, vcc
	s_and_b64 vcc, s[44:45], s[84:85]
	v_cndmask_b32_e32 v103, v18, v104, vcc
	s_and_b64 vcc, s[0:1], s[82:83]
	s_movk_i32 s0, 0xffbf
	v_cmp_lt_i32_e64 s[80:81], s0, v1
	s_movk_i32 s0, 0xffbb
	v_cndmask_b32_e32 v104, v18, v105, vcc
	s_and_b64 vcc, s[46:47], s[80:81]
	v_cmp_lt_i32_e64 s[78:79], s0, v1
	s_movk_i32 s0, 0xffb7
	v_cndmask_b32_e32 v105, v18, v106, vcc
	s_and_b64 vcc, s[52:53], s[78:79]
	v_cmp_lt_i32_e64 s[76:77], s0, v1
	s_movk_i32 s0, 0xffb3
	v_cndmask_b32_e32 v106, v18, v107, vcc
	s_and_b64 vcc, s[48:49], s[76:77]
	v_cmp_lt_i32_e64 s[10:11], s0, v1
	s_movk_i32 s0, 0xff9f
	v_cndmask_b32_e32 v107, v18, v108, vcc
	s_and_b64 vcc, s[54:55], s[10:11]
	v_cmp_lt_i32_e64 s[8:9], s0, v1
	s_movk_i32 s0, 0xff9b
	v_cndmask_b32_e32 v108, v18, v109, vcc
	s_and_b64 vcc, s[50:51], s[8:9]
	v_cmp_lt_i32_e64 s[4:5], s0, v1
	s_movk_i32 s0, 0xff97
	v_cndmask_b32_e32 v109, v18, v110, vcc
	s_and_b64 vcc, s[56:57], s[4:5]
	v_cmp_lt_i32_e64 s[12:13], s0, v1
	s_movk_i32 s0, 0xff93
	v_cndmask_b32_e32 v110, v18, v111, vcc
	s_and_b64 vcc, s[60:61], s[12:13]
	v_cmp_lt_i32_e64 s[0:1], s0, v1
	v_cndmask_b32_e32 v111, v18, v112, vcc
	s_and_b64 vcc, s[58:59], s[0:1]
	v_cndmask_b32_e32 v1, v18, v113, vcc
	v_max_f32_e32 v112, v98, v98
	v_max_f32_e32 v113, v17, v17
	v_max_f32_e32 v112, v113, v112
	v_max3_f32 v112, v112, v99, v100
	v_max3_f32 v112, v112, v101, v102
	v_max3_f32 v112, v112, v103, v104
	v_max3_f32 v112, v112, v105, v106
	v_max3_f32 v112, v112, v107, v108
	v_max3_f32 v112, v112, v109, v110
	v_max3_f32 v112, v112, v111, v1
	v_mov_b32_e32 v113, v112
	s_nop 1
	v_permlane32_swap_b32_e32 v112, v113
	v_mfma_f32_32x32x16_bf16 v[82:97], v[154:157], v[174:177], v[82:97]
	ds_read_b64_tr_b16 v[122:123], v181 offset:0
	ds_read_b64_tr_b16 v[124:125], v181 offset:0x400
	ds_read_b64_tr_b16 v[126:127], v181 offset:0x800
	ds_read_b64_tr_b16 v[128:129], v181 offset:0xc00
	ds_read_b64_tr_b16 v[130:131], v181 offset:0x200
	ds_read_b64_tr_b16 v[132:133], v181 offset:0x600
	ds_read_b64_tr_b16 v[118:119], v181 offset:0xa00
	v_mfma_f32_32x32x16_bf16 v[66:81], v[154:157], v[166:169], v[66:81]
	v_max3_f32 v154, v249, v112, v113
	v_sub_f32_e32 v17, v17, v154
	v_exp_f32_e32 v17, v17
	v_sub_f32_e32 v98, v98, v154
	v_exp_f32_e32 v98, v98
	v_sub_f32_e32 v99, v99, v154
	v_exp_f32_e32 v99, v99
	v_sub_f32_e32 v100, v100, v154
	v_exp_f32_e32 v100, v100
	v_sub_f32_e32 v101, v101, v154
	v_add_f32_e32 v113, 0, v17
	v_exp_f32_e32 v101, v101
	v_sub_f32_e32 v102, v102, v154
	v_add_f32_e32 v113, v98, v113
	v_exp_f32_e32 v102, v102
	v_sub_f32_e32 v103, v103, v154
	v_add_f32_e32 v113, v99, v113
	v_exp_f32_e32 v103, v103
	v_sub_f32_e32 v104, v104, v154
	v_add_f32_e32 v113, v100, v113
	v_exp_f32_e32 v104, v104
	v_sub_f32_e32 v105, v105, v154
	v_add_f32_e32 v113, v101, v113
	v_exp_f32_e32 v105, v105
	v_sub_f32_e32 v106, v106, v154
	v_add_f32_e32 v113, v102, v113
	v_exp_f32_e32 v106, v106
	v_sub_f32_e32 v107, v107, v154
	v_add_f32_e32 v113, v103, v113
	v_exp_f32_e32 v107, v107
	v_sub_f32_e32 v108, v108, v154
	v_add_f32_e32 v113, v104, v113
	v_exp_f32_e32 v108, v108
	v_sub_f32_e32 v109, v109, v154
	v_add_f32_e32 v113, v105, v113
	v_exp_f32_e32 v109, v109
	v_sub_f32_e32 v110, v110, v154
	v_add_f32_e32 v113, v106, v113
	v_exp_f32_e32 v110, v110
	v_sub_f32_e32 v111, v111, v154
	v_add_f32_e32 v113, v107, v113
	v_exp_f32_e32 v111, v111
	v_sub_f32_e32 v1, v1, v154
	v_add_f32_e32 v113, v108, v113
	v_exp_f32_e32 v1, v1
	v_sub_f32_e32 v112, v249, v154
	v_add_f32_e32 v113, v109, v113
	v_add_f32_e32 v113, v110, v113
	v_exp_f32_e32 v155, v112
	v_add_f32_e32 v113, v111, v113
	ds_read_b64_tr_b16 v[120:121], v181 offset:0xe00
	v_add_f32_e32 v156, v1, v113
	v_mov_b32_e32 v157, v156
	v_cvt_pk_bf16_f32 v98, v17, v98
	v_cvt_pk_bf16_f32 v99, v99, v100
	v_cvt_pk_bf16_f32 v100, v101, v102
	v_cvt_pk_bf16_f32 v101, v103, v104
	v_cvt_pk_bf16_f32 v102, v105, v106
	v_cvt_pk_bf16_f32 v103, v107, v108
	v_cvt_pk_bf16_f32 v104, v109, v110
	v_cvt_pk_bf16_f32 v105, v111, v1
	s_nop 1
	v_permlane32_swap_b32_e32 v156, v157
	v_permlane32_swap_b32_e32 v98, v100
	v_permlane32_swap_b32_e32 v99, v101
	v_permlane32_swap_b32_e32 v102, v104
	v_permlane32_swap_b32_e32 v103, v105
	v_cmp_gt_f32_e32 vcc, 1.0, v155
	s_cbranch_vccz .LBB0_1328
	s_and_saveexec_b64 vcc, s[6:7]
	ds_write_b32 v185, v155
	s_or_b64 exec, exec, vcc
	v_lshl_add_u32 v1, v212, 2, s38
	ds_read_b128 v[106:109], v1 offset:96
	ds_read_b128 v[110:113], v1 offset:64
	ds_read_b128 v[162:165], v1 offset:32
	ds_read_b128 v[166:169], v1
	s_waitcnt lgkmcnt(0)
	v_pk_mul_f32 v[64:65], v[64:65], v[108:109]
	v_pk_mul_f32 v[60:61], v[60:61], v[112:113]
	v_pk_mul_f32 v[56:57], v[56:57], v[164:165]
	v_pk_mul_f32 v[52:53], v[52:53], v[168:169]
	v_pk_mul_f32 v[62:63], v[62:63], v[106:107]
	v_pk_mul_f32 v[58:59], v[58:59], v[110:111]
	v_pk_mul_f32 v[54:55], v[54:55], v[162:163]
	v_pk_mul_f32 v[50:51], v[50:51], v[166:167]
	v_pk_mul_f32 v[48:49], v[48:49], v[108:109]
	v_pk_mul_f32 v[44:45], v[44:45], v[112:113]
	v_pk_mul_f32 v[40:41], v[40:41], v[164:165]
	v_pk_mul_f32 v[36:37], v[36:37], v[168:169]
	v_pk_mul_f32 v[46:47], v[46:47], v[106:107]
	v_pk_mul_f32 v[42:43], v[42:43], v[110:111]
	v_pk_mul_f32 v[38:39], v[38:39], v[162:163]
	v_pk_mul_f32 v[34:35], v[34:35], v[166:167]

.LBB0_1331:
	s_nop 4
	v_max_f32_e32 v1, v99, v99
	v_max_f32_e32 v17, v98, v98
	v_max_f32_e32 v1, v17, v1
	v_max3_f32 v1, v1, v100, v101
	v_max3_f32 v1, v1, v102, v103
	v_max3_f32 v1, v1, v104, v105
	v_max3_f32 v1, v1, v106, v107
	v_max3_f32 v1, v1, v108, v109
	v_max3_f32 v1, v1, v110, v111
	v_max3_f32 v1, v1, v112, v113
	v_mov_b32_e32 v17, v1
	s_nop 1
	v_permlane32_swap_b32_e32 v1, v17
	v_max3_f32 v136, v161, v1, v17
	v_sub_f32_e32 v17, v98, v136
	v_exp_f32_e32 v20, v17
	v_sub_f32_e32 v17, v99, v136
	v_exp_f32_e32 v21, v17
	v_sub_f32_e32 v17, v100, v136
	v_exp_f32_e32 v22, v17
	v_sub_f32_e32 v17, v101, v136
	v_exp_f32_e32 v23, v17
	v_sub_f32_e32 v24, v102, v136
	v_add_f32_e32 v17, 0, v20
	v_exp_f32_e32 v24, v24
	v_sub_f32_e32 v25, v103, v136
	v_add_f32_e32 v17, v21, v17
	v_exp_f32_e32 v25, v25
	v_sub_f32_e32 v26, v104, v136
	v_add_f32_e32 v17, v22, v17
	v_exp_f32_e32 v26, v26
	v_sub_f32_e32 v27, v105, v136
	v_add_f32_e32 v17, v23, v17
	v_exp_f32_e32 v27, v27
	v_sub_f32_e32 v28, v106, v136
	v_add_f32_e32 v17, v24, v17
	v_exp_f32_e32 v28, v28
	v_sub_f32_e32 v29, v107, v136
	v_add_f32_e32 v17, v25, v17
	v_exp_f32_e32 v29, v29
	v_sub_f32_e32 v30, v108, v136
	v_add_f32_e32 v17, v26, v17
	v_exp_f32_e32 v30, v30
	v_sub_f32_e32 v31, v109, v136
	v_add_f32_e32 v17, v27, v17
	v_exp_f32_e32 v31, v31
	v_sub_f32_e32 v98, v110, v136
	v_add_f32_e32 v17, v28, v17
	v_exp_f32_e32 v98, v98
	v_sub_f32_e32 v99, v111, v136
	v_add_f32_e32 v17, v29, v17
	v_exp_f32_e32 v99, v99
	v_sub_f32_e32 v100, v112, v136
	v_add_f32_e32 v17, v30, v17
	v_exp_f32_e32 v100, v100
	v_sub_f32_e32 v101, v113, v136
	v_add_f32_e32 v17, v31, v17
	v_exp_f32_e32 v101, v101
	v_add_f32_e32 v17, v98, v17
	v_add_f32_e32 v17, v99, v17
	v_sub_f32_e32 v1, v161, v136
	v_add_f32_e32 v17, v100, v17
	v_add_f32_e32 v134, v101, v17
	v_exp_f32_e32 v17, v1
	v_mov_b32_e32 v135, v134
	v_cvt_pk_bf16_f32 v20, v20, v21
	v_cvt_pk_bf16_f32 v21, v22, v23
	v_cvt_pk_bf16_f32 v22, v24, v25
	v_cvt_pk_bf16_f32 v23, v26, v27
	v_cvt_pk_bf16_f32 v24, v28, v29
	v_cvt_pk_bf16_f32 v25, v30, v31
	v_cvt_pk_bf16_f32 v26, v98, v99
	v_cvt_pk_bf16_f32 v27, v100, v101
	s_movk_i32 s90, 0xffef
	s_movk_i32 s13, 0xffdf
	s_movk_i32 s43, 0xffcf
	s_movk_i32 s76, 0xff7f
	s_movk_i32 s77, 0xff6f
	s_movk_i32 s78, 0xff5f
	s_movk_i32 s79, 0xff4f
	s_movk_i32 s80, 0xfeff
	s_movk_i32 s81, 0xfeef
	s_movk_i32 s82, 0xfedf
	s_movk_i32 s83, 0xfecf
	s_movk_i32 s84, 0xfe7f
	s_movk_i32 s85, 0xfe6f
	s_movk_i32 s86, 0xfe5f
	s_movk_i32 s87, 0xfe4f
	v_permlane32_swap_b32_e32 v134, v135
	v_permlane32_swap_b32_e32 v20, v22
	v_permlane32_swap_b32_e32 v21, v23
	v_permlane32_swap_b32_e32 v24, v26
	v_permlane32_swap_b32_e32 v25, v27
	v_cmp_gt_f32_e32 vcc, 1.0, v17
	s_cbranch_vccz .LBB0_1335
	s_and_saveexec_b64 s[0:1], s[6:7]
	ds_write_b32 v185, v17
	s_or_b64 exec, exec, s[0:1]
	v_lshl_add_u32 v1, v212, 2, s38
	ds_read_b128 v[28:31], v1 offset:96
	ds_read_b128 v[98:101], v1 offset:64
	ds_read_b128 v[102:105], v1 offset:32
	ds_read_b128 v[106:109], v1
	s_waitcnt lgkmcnt(0)
	v_pk_mul_f32 v[96:97], v[96:97], v[30:31]
	v_pk_mul_f32 v[92:93], v[92:93], v[100:101]
	v_pk_mul_f32 v[88:89], v[88:89], v[104:105]
	v_pk_mul_f32 v[84:85], v[84:85], v[108:109]
	v_pk_mul_f32 v[94:95], v[94:95], v[28:29]
	v_pk_mul_f32 v[90:91], v[90:91], v[98:99]
	v_pk_mul_f32 v[86:87], v[86:87], v[102:103]
	v_pk_mul_f32 v[82:83], v[82:83], v[106:107]
	v_pk_mul_f32 v[80:81], v[80:81], v[30:31]
	v_pk_mul_f32 v[76:77], v[76:77], v[100:101]
	v_pk_mul_f32 v[72:73], v[72:73], v[104:105]
	v_pk_mul_f32 v[68:69], v[68:69], v[108:109]
	v_pk_mul_f32 v[78:79], v[78:79], v[28:29]
	v_pk_mul_f32 v[74:75], v[74:75], v[98:99]
	v_pk_mul_f32 v[70:71], v[70:71], v[102:103]
	v_pk_mul_f32 v[66:67], v[66:67], v[106:107]
.LBB0_1335:
	s_waitcnt lgkmcnt(0)
	v_or_b32_e32 v1, 0x280, v2
	v_add_u32_e32 v1, s18, v1
	v_mfma_f32_32x32x16_bf16 v[98:113], v[150:153], v[114:117], 0
	v_add_u32_e32 v2, 0xffffff60, v237
	v_cmp_lt_i32_e64 s[0:1], -1, v1
	s_waitcnt vmcnt(0)
	v_mfma_f32_32x32x16_bf16 v[98:113], v[138:141], v[4:7], v[98:113]
	v_sub_u32_e32 v4, v2, v212
	v_cmp_gt_u32_e32 vcc, s97, v4
	s_and_b64 vcc, vcc, s[0:1]
	v_sub_u32_e32 v5, v2, v204
	v_cmp_lt_i32_e64 s[0:1], -5, v1
	v_sub_u32_e32 v6, v2, v199
	v_sub_u32_e32 v7, v2, v198
	v_mfma_f32_32x32x16_bf16 v[98:113], v[142:145], v[8:11], v[98:113]
	v_sub_u32_e32 v8, v2, v197
	v_sub_u32_e32 v9, v2, v196
	v_sub_u32_e32 v10, v2, v195
	v_sub_u32_e32 v11, v2, v194
	v_mfma_f32_32x32x16_bf16 v[98:113], v[146:149], v[12:15], v[98:113]
	v_sub_u32_e32 v12, v2, v193
	v_sub_u32_e32 v13, v2, v192
	v_sub_u32_e32 v14, v2, v191
	v_sub_u32_e32 v15, v2, v190
	v_mfma_f32_32x32x16_bf16 v[66:81], v[20:23], v[130:133], v[66:81]
	s_nop 6
	v_cndmask_b32_e32 v4, v18, v98, vcc
	v_cmp_gt_u32_e32 vcc, s97, v5
	s_and_b64 vcc, vcc, s[0:1]
	v_cmp_lt_i32_e64 s[0:1], -9, v1
	v_cndmask_b32_e32 v5, v18, v99, vcc
	v_cmp_gt_u32_e32 vcc, s97, v6
	s_and_b64 vcc, vcc, s[0:1]
	v_cmp_lt_i32_e64 s[0:1], -13, v1
	v_cndmask_b32_e32 v6, v18, v100, vcc
	v_cmp_gt_u32_e32 vcc, s97, v7
	s_and_b64 vcc, vcc, s[0:1]
	v_cmp_lt_i32_e64 s[0:1], s13, v1
	v_cndmask_b32_e32 v7, v18, v101, vcc
	v_cmp_gt_u32_e32 vcc, s97, v8
	s_and_b64 vcc, vcc, s[0:1]
	v_cmp_lt_i32_e64 s[0:1], s19, v1
	v_cndmask_b32_e32 v8, v18, v102, vcc
	v_cmp_gt_u32_e32 vcc, s97, v9
	s_and_b64 vcc, vcc, s[0:1]
	v_cmp_lt_i32_e64 s[0:1], s33, v1
	v_cndmask_b32_e32 v9, v18, v103, vcc
	v_cmp_gt_u32_e32 vcc, s97, v10
	s_and_b64 vcc, vcc, s[0:1]
	v_cmp_lt_i32_e64 s[0:1], s42, v1
	v_cndmask_b32_e32 v10, v18, v104, vcc
	v_cmp_gt_u32_e32 vcc, s97, v11
	s_and_b64 vcc, vcc, s[0:1]
	s_movk_i32 s0, 0xffbf
	v_cndmask_b32_e32 v11, v18, v105, vcc
	v_cmp_gt_u32_e32 vcc, s97, v12
	v_cmp_lt_i32_e64 s[0:1], s0, v1
	s_and_b64 vcc, vcc, s[0:1]
	s_movk_i32 s0, 0xffbb
	v_cndmask_b32_e32 v12, v18, v106, vcc
	v_cmp_gt_u32_e32 vcc, s97, v13
	v_cmp_lt_i32_e64 s[0:1], s0, v1
	s_and_b64 vcc, vcc, s[0:1]
	s_movk_i32 s0, 0xffb7
	v_cndmask_b32_e32 v13, v18, v107, vcc
	v_cmp_gt_u32_e32 vcc, s97, v14
	v_cmp_lt_i32_e64 s[0:1], s0, v1
	s_and_b64 vcc, vcc, s[0:1]
	s_movk_i32 s0, 0xffb3
	v_cndmask_b32_e32 v14, v18, v108, vcc
	v_cmp_gt_u32_e32 vcc, s97, v15
	v_cmp_lt_i32_e64 s[0:1], s0, v1
	s_and_b64 vcc, vcc, s[0:1]
	v_sub_u32_e32 v98, v2, v189
	s_movk_i32 s0, 0xff9f
	v_cndmask_b32_e32 v15, v18, v109, vcc
	v_cmp_gt_u32_e32 vcc, s97, v98
	v_cmp_lt_i32_e64 s[0:1], s0, v1
	s_and_b64 vcc, vcc, s[0:1]
	v_sub_u32_e32 v99, v2, v188
	s_movk_i32 s0, 0xff9b
	v_cndmask_b32_e32 v98, v18, v110, vcc
	v_cmp_gt_u32_e32 vcc, s97, v99
	v_cmp_lt_i32_e64 s[0:1], s0, v1
	s_and_b64 vcc, vcc, s[0:1]
	v_sub_u32_e32 v100, v2, v187
	s_movk_i32 s0, 0xff97
	v_cndmask_b32_e32 v99, v18, v111, vcc
	v_cmp_gt_u32_e32 vcc, s97, v100
	v_cmp_lt_i32_e64 s[0:1], s0, v1
	s_and_b64 vcc, vcc, s[0:1]
	v_sub_u32_e32 v2, v2, v186
	v_cndmask_b32_e32 v100, v18, v112, vcc
	v_cmp_gt_u32_e32 vcc, s97, v2
	v_max_f32_e32 v2, v5, v5
	v_max_f32_e32 v101, v4, v4
	v_max_f32_e32 v2, v101, v2
	v_max3_f32 v2, v2, v6, v7
	v_max3_f32 v2, v2, v8, v9
	s_movk_i32 s0, 0xff93
	v_max3_f32 v2, v2, v10, v11
	v_cmp_lt_i32_e64 s[0:1], s0, v1
	v_max3_f32 v2, v2, v12, v13
	s_and_b64 vcc, vcc, s[0:1]
	v_max3_f32 v2, v2, v14, v15
	v_cndmask_b32_e32 v1, v18, v113, vcc
	v_max3_f32 v2, v2, v98, v99
	v_max3_f32 v2, v2, v100, v1
	v_mov_b32_e32 v101, v2
	s_nop 1
	v_permlane32_swap_b32_e32 v2, v101
	v_max3_f32 v2, v136, v2, v101
	v_sub_f32_e32 v4, v4, v2
	v_exp_f32_e32 v4, v4
	v_sub_f32_e32 v5, v5, v2
	v_exp_f32_e32 v5, v5
	v_sub_f32_e32 v6, v6, v2
	v_exp_f32_e32 v6, v6
	v_sub_f32_e32 v7, v7, v2
	v_exp_f32_e32 v7, v7
	v_sub_f32_e32 v8, v8, v2
	v_add_f32_e32 v102, 0, v4
	v_exp_f32_e32 v8, v8
	v_sub_f32_e32 v9, v9, v2
	v_add_f32_e32 v102, v5, v102
	v_exp_f32_e32 v9, v9
	v_sub_f32_e32 v10, v10, v2
	v_add_f32_e32 v102, v6, v102
	v_exp_f32_e32 v10, v10
	v_sub_f32_e32 v11, v11, v2
	v_add_f32_e32 v102, v7, v102
	v_exp_f32_e32 v11, v11
	v_sub_f32_e32 v12, v12, v2
	v_add_f32_e32 v102, v8, v102
	v_exp_f32_e32 v103, v12
	v_add_f32_e32 v102, v9, v102
	v_add_f32_e32 v102, v10, v102
	v_mfma_f32_32x32x16_bf16 v[82:97], v[20:23], v[122:125], v[82:97]
	v_add_f32_e32 v102, v11, v102
	v_sub_f32_e32 v13, v13, v2
	v_add_f32_e32 v12, v103, v102
	v_exp_f32_e32 v102, v13
	v_sub_f32_e32 v13, v14, v2
	v_exp_f32_e32 v104, v13
	v_sub_f32_e32 v13, v15, v2
	v_exp_f32_e32 v15, v13
	v_sub_f32_e32 v13, v98, v2
	v_exp_f32_e32 v98, v13
	v_sub_f32_e32 v13, v99, v2
	v_add_f32_e32 v12, v102, v12
	v_exp_f32_e32 v99, v13
	v_sub_f32_e32 v13, v100, v2
	v_mfma_f32_32x32x16_bf16 v[66:81], v[24:27], v[118:121], v[66:81]
	ds_read_b64_tr_b16 v[118:119], v182 offset:0
	v_add_f32_e32 v12, v104, v12
	v_exp_f32_e32 v100, v13
	v_sub_f32_e32 v1, v1, v2
	ds_read_b64_tr_b16 v[120:121], v182 offset:0x400
	v_add_f32_e32 v12, v15, v12
	v_exp_f32_e32 v1, v1
	v_mfma_f32_32x32x16_bf16 v[82:97], v[24:27], v[126:129], v[82:97]
	ds_read_b64_tr_b16 v[28:29], v182 offset:0x800
	v_add_f32_e32 v12, v98, v12
	ds_read_b64_tr_b16 v[30:31], v182 offset:0xc00
	v_add_f32_e32 v12, v99, v12
	ds_read_b64_tr_b16 v[24:25], v182 offset:0x200
	v_sub_f32_e32 v101, v136, v2
	v_add_f32_e32 v12, v100, v12
	ds_read_b64_tr_b16 v[26:27], v182 offset:0x600
	v_add_f32_e32 v13, v1, v12
	v_exp_f32_e32 v12, v101
	ds_read_b64_tr_b16 v[20:21], v182 offset:0xa00
	ds_read_b64_tr_b16 v[22:23], v182 offset:0xe00
	v_mov_b32_e32 v14, v13
	v_cvt_pk_bf16_f32 v4, v4, v5
	v_cvt_pk_bf16_f32 v5, v6, v7
	v_cvt_pk_bf16_f32 v6, v8, v9
	v_cvt_pk_bf16_f32 v7, v10, v11
	v_cvt_pk_bf16_f32 v8, v103, v102
	v_cvt_pk_bf16_f32 v9, v104, v15
	v_cvt_pk_bf16_f32 v10, v98, v99
	v_cvt_pk_bf16_f32 v11, v100, v1
	s_nop 1
	v_permlane32_swap_b32_e32 v13, v14
	v_permlane32_swap_b32_e32 v4, v6
	v_permlane32_swap_b32_e32 v5, v7
	v_permlane32_swap_b32_e32 v8, v10
	v_permlane32_swap_b32_e32 v9, v11
	v_cmp_gt_f32_e32 vcc, 1.0, v12
	s_cbranch_vccz .LBB0_1339
	s_and_saveexec_b64 s[0:1], s[6:7]
	ds_write_b32 v185, v12
	s_or_b64 exec, exec, s[0:1]
	v_lshl_add_u32 v1, v212, 2, s38
	ds_read_b128 v[98:101], v1 offset:96
	ds_read_b128 v[102:105], v1 offset:64
	ds_read_b128 v[106:109], v1 offset:32
	ds_read_b128 v[110:113], v1
	s_waitcnt lgkmcnt(0)
	v_pk_mul_f32 v[96:97], v[96:97], v[100:101]
	v_pk_mul_f32 v[92:93], v[92:93], v[104:105]
	v_pk_mul_f32 v[88:89], v[88:89], v[108:109]
	v_pk_mul_f32 v[84:85], v[84:85], v[112:113]
	v_pk_mul_f32 v[94:95], v[94:95], v[98:99]
	v_pk_mul_f32 v[90:91], v[90:91], v[102:103]
	v_pk_mul_f32 v[86:87], v[86:87], v[106:107]
	v_pk_mul_f32 v[82:83], v[82:83], v[110:111]
	v_pk_mul_f32 v[80:81], v[80:81], v[100:101]
	v_pk_mul_f32 v[76:77], v[76:77], v[104:105]
	v_pk_mul_f32 v[72:73], v[72:73], v[108:109]
	v_pk_mul_f32 v[68:69], v[68:69], v[112:113]
	v_pk_mul_f32 v[78:79], v[78:79], v[98:99]
	v_pk_mul_f32 v[74:75], v[74:75], v[102:103]
	v_pk_mul_f32 v[70:71], v[70:71], v[106:107]
	v_pk_mul_f32 v[66:67], v[66:67], v[110:111]

.LBB0_1343:
	s_or_b64 exec, exec, s[0:1]
	s_waitcnt lgkmcnt(0)
	v_or_b32_e32 v1, s39, v212
	v_lshl_add_u32 v1, v1, 9, v4
	ds_read2_b32 v[6:7], v19 offset1:32
	ds_read_u16 v2, v1
	s_lshl_b32 s8, s37, 1
	v_lshlrev_b32_e32 v118, 4, v210
	v_or_b32_e32 v146, s26, v118
	v_mov_b32_e32 v179, v3
	s_waitcnt lgkmcnt(0)
	v_lshlrev_b32_e32 v2, 16, v2
	v_mul_f32_e32 v2, v6, v2
	v_fmac_f32_e32 v2, v82, v7
	v_cvt_pk_bf16_f32 v2, v2, v3
	ds_write_b16 v1, v2
	ds_read_u16 v2, v1 offset:64
	s_add_i32 s10, s8, s26
	v_lshl_add_u64 v[116:117], s[22:23], 0, v[178:179]
	s_add_i32 s9, s10, 0xfffff800
	v_lshlrev_b32_e32 v119, 4, v209
	s_waitcnt lgkmcnt(0)
	v_lshlrev_b32_e32 v2, 16, v2
	v_mul_f32_e32 v2, v6, v2
	v_fmac_f32_e32 v2, v66, v7
	v_cvt_pk_bf16_f32 v2, v2, v3
	ds_write_b16 v1, v2 offset:64
	v_or_b32_e32 v1, s39, v204
	v_lshl_add_u32 v1, v1, 9, v4
	ds_read2_b32 v[6:7], v19 offset0:1 offset1:33
	ds_read_u16 v2, v1
	v_lshlrev_b32_e32 v121, 4, v208
	v_lshlrev_b32_e32 v123, 4, v207
	v_mov_b32_e32 v17, v3
	s_mov_b32 m0, s27
	s_waitcnt lgkmcnt(0)
	v_lshlrev_b32_e32 v2, 16, v2
	v_mul_f32_e32 v2, v6, v2
	v_fmac_f32_e32 v2, v83, v7
	v_cvt_pk_bf16_f32 v2, v2, v3
	ds_write_b16 v1, v2
	ds_read_u16 v2, v1 offset:64
	v_lshlrev_b32_e32 v124, 4, v206
	v_lshlrev_b32_e32 v137, 4, v211
	v_lshlrev_b32_e32 v120, 6, v184
	s_waitcnt lgkmcnt(0)
	v_lshlrev_b32_e32 v2, 16, v2
	v_mul_f32_e32 v2, v6, v2
	v_fmac_f32_e32 v2, v67, v7
	v_cvt_pk_bf16_f32 v2, v2, v3
	ds_write_b16 v1, v2 offset:64
	v_or_b32_e32 v1, s39, v199
	v_lshl_add_u32 v1, v1, 9, v4
	ds_read2_b32 v[6:7], v19 offset0:2 offset1:34
	ds_read_u16 v2, v1
	s_waitcnt lgkmcnt(0)
	v_lshlrev_b32_e32 v2, 16, v2
	v_mul_f32_e32 v2, v6, v2
	v_fmac_f32_e32 v2, v84, v7
	v_cvt_pk_bf16_f32 v2, v2, v3
	ds_write_b16 v1, v2
	ds_read_u16 v2, v1 offset:64
	s_waitcnt lgkmcnt(0)
	v_lshlrev_b32_e32 v2, 16, v2
	v_mul_f32_e32 v2, v6, v2
	v_fmac_f32_e32 v2, v68, v7
	v_cvt_pk_bf16_f32 v2, v2, v3
	ds_write_b16 v1, v2 offset:64
	v_or_b32_e32 v1, s39, v198
	v_lshl_add_u32 v1, v1, 9, v4
	ds_read2_b32 v[6:7], v19 offset0:3 offset1:35
	ds_read_u16 v2, v1
	s_waitcnt lgkmcnt(0)
	v_lshlrev_b32_e32 v2, 16, v2
	v_mul_f32_e32 v2, v6, v2
	v_fmac_f32_e32 v2, v85, v7
	v_cvt_pk_bf16_f32 v2, v2, v3
	ds_write_b16 v1, v2
	ds_read_u16 v2, v1 offset:64
	s_waitcnt lgkmcnt(0)
	v_lshlrev_b32_e32 v2, 16, v2
	v_mul_f32_e32 v2, v6, v2
	v_fmac_f32_e32 v2, v69, v7
	v_cvt_pk_bf16_f32 v2, v2, v3
	ds_write_b16 v1, v2 offset:64
	v_or_b32_e32 v1, s39, v197
	v_lshl_add_u32 v1, v1, 9, v4
	ds_read2_b32 v[6:7], v19 offset0:8 offset1:40
	ds_read_u16 v2, v1
	s_waitcnt lgkmcnt(0)
	v_lshlrev_b32_e32 v2, 16, v2
	v_mul_f32_e32 v2, v6, v2
	v_fmac_f32_e32 v2, v86, v7
	v_cvt_pk_bf16_f32 v2, v2, v3
	ds_write_b16 v1, v2
	ds_read_u16 v2, v1 offset:64
	s_waitcnt lgkmcnt(0)
	v_lshlrev_b32_e32 v2, 16, v2
	v_mul_f32_e32 v2, v6, v2
	v_fmac_f32_e32 v2, v70, v7
	v_cvt_pk_bf16_f32 v2, v2, v3
	ds_write_b16 v1, v2 offset:64
	v_or_b32_e32 v1, s39, v196
	v_lshl_add_u32 v1, v1, 9, v4
	ds_read2_b32 v[6:7], v19 offset0:9 offset1:41
	ds_read_u16 v2, v1
	s_waitcnt lgkmcnt(0)
	v_lshlrev_b32_e32 v2, 16, v2
	v_mul_f32_e32 v2, v6, v2
	v_fmac_f32_e32 v2, v87, v7
	v_cvt_pk_bf16_f32 v2, v2, v3
	ds_write_b16 v1, v2
	ds_read_u16 v2, v1 offset:64
	s_waitcnt lgkmcnt(0)
	v_lshlrev_b32_e32 v2, 16, v2
	v_mul_f32_e32 v2, v6, v2
	v_fmac_f32_e32 v2, v71, v7
	v_cvt_pk_bf16_f32 v2, v2, v3
	ds_write_b16 v1, v2 offset:64
	v_or_b32_e32 v1, s39, v195
	v_lshl_add_u32 v1, v1, 9, v4
	ds_read2_b32 v[6:7], v19 offset0:10 offset1:42
	ds_read_u16 v2, v1
	s_waitcnt lgkmcnt(0)
	v_lshlrev_b32_e32 v2, 16, v2
	v_mul_f32_e32 v2, v6, v2
	v_fmac_f32_e32 v2, v88, v7
	v_cvt_pk_bf16_f32 v2, v2, v3
	ds_write_b16 v1, v2
	ds_read_u16 v2, v1 offset:64
	s_waitcnt lgkmcnt(0)
	v_lshlrev_b32_e32 v2, 16, v2
	v_mul_f32_e32 v2, v6, v2
	v_fmac_f32_e32 v2, v72, v7
	v_cvt_pk_bf16_f32 v2, v2, v3
	ds_write_b16 v1, v2 offset:64
	v_or_b32_e32 v1, s39, v194
	v_lshl_add_u32 v1, v1, 9, v4
	ds_read2_b32 v[6:7], v19 offset0:11 offset1:43
	ds_read_u16 v2, v1
	s_waitcnt lgkmcnt(0)
	v_lshlrev_b32_e32 v2, 16, v2
	v_mul_f32_e32 v2, v6, v2
	v_fmac_f32_e32 v2, v89, v7
	v_cvt_pk_bf16_f32 v2, v2, v3
	ds_write_b16 v1, v2
	ds_read_u16 v2, v1 offset:64
	s_waitcnt lgkmcnt(0)
	v_lshlrev_b32_e32 v2, 16, v2
	v_mul_f32_e32 v2, v6, v2
	v_fmac_f32_e32 v2, v73, v7
	v_cvt_pk_bf16_f32 v2, v2, v3
	ds_write_b16 v1, v2 offset:64
	v_or_b32_e32 v1, s39, v193
	v_lshl_add_u32 v1, v1, 9, v4
	ds_read2_b32 v[6:7], v19 offset0:16 offset1:48
	ds_read_u16 v2, v1
	s_waitcnt lgkmcnt(0)
	v_lshlrev_b32_e32 v2, 16, v2
	v_mul_f32_e32 v2, v6, v2
	v_fmac_f32_e32 v2, v90, v7
	v_cvt_pk_bf16_f32 v2, v2, v3
	ds_write_b16 v1, v2
	ds_read_u16 v2, v1 offset:64
	s_waitcnt lgkmcnt(0)
	v_lshlrev_b32_e32 v2, 16, v2
	v_mul_f32_e32 v2, v6, v2
	v_fmac_f32_e32 v2, v74, v7
	v_cvt_pk_bf16_f32 v2, v2, v3
	ds_write_b16 v1, v2 offset:64
	v_or_b32_e32 v1, s39, v192
	v_lshl_add_u32 v1, v1, 9, v4
	ds_read2_b32 v[6:7], v19 offset0:17 offset1:49
	ds_read_u16 v2, v1
	s_waitcnt lgkmcnt(0)
	v_lshlrev_b32_e32 v2, 16, v2
	v_mul_f32_e32 v2, v6, v2
	v_fmac_f32_e32 v2, v91, v7
	v_cvt_pk_bf16_f32 v2, v2, v3
	ds_write_b16 v1, v2
	ds_read_u16 v2, v1 offset:64
	s_waitcnt lgkmcnt(0)
	v_lshlrev_b32_e32 v2, 16, v2
	v_mul_f32_e32 v2, v6, v2
	v_fmac_f32_e32 v2, v75, v7
	v_cvt_pk_bf16_f32 v2, v2, v3
	ds_write_b16 v1, v2 offset:64
	v_or_b32_e32 v1, s39, v191
	v_lshl_add_u32 v1, v1, 9, v4
	ds_read2_b32 v[6:7], v19 offset0:18 offset1:50
	ds_read_u16 v2, v1
	s_waitcnt lgkmcnt(0)
	v_lshlrev_b32_e32 v2, 16, v2
	v_mul_f32_e32 v2, v6, v2
	v_fmac_f32_e32 v2, v92, v7
	v_cvt_pk_bf16_f32 v2, v2, v3
	ds_write_b16 v1, v2
	ds_read_u16 v2, v1 offset:64
	s_waitcnt lgkmcnt(0)
	v_lshlrev_b32_e32 v2, 16, v2
	v_mul_f32_e32 v2, v6, v2
	v_fmac_f32_e32 v2, v76, v7
	v_cvt_pk_bf16_f32 v2, v2, v3
	ds_write_b16 v1, v2 offset:64
	v_or_b32_e32 v1, s39, v190
	v_lshl_add_u32 v1, v1, 9, v4
	ds_read2_b32 v[6:7], v19 offset0:19 offset1:51
	ds_read_u16 v2, v1
	s_waitcnt lgkmcnt(0)
	v_lshlrev_b32_e32 v2, 16, v2
	v_mul_f32_e32 v2, v6, v2
	v_fmac_f32_e32 v2, v93, v7
	v_cvt_pk_bf16_f32 v2, v2, v3
	ds_write_b16 v1, v2
	ds_read_u16 v2, v1 offset:64
	s_waitcnt lgkmcnt(0)
	v_lshlrev_b32_e32 v2, 16, v2
	v_mul_f32_e32 v2, v6, v2
	v_fmac_f32_e32 v2, v77, v7
	v_cvt_pk_bf16_f32 v2, v2, v3
	ds_write_b16 v1, v2 offset:64
	v_or_b32_e32 v1, s39, v189
	v_lshl_add_u32 v1, v1, 9, v4
	ds_read2_b32 v[6:7], v19 offset0:24 offset1:56
	ds_read_u16 v2, v1
	s_waitcnt lgkmcnt(0)
	v_lshlrev_b32_e32 v2, 16, v2
	v_mul_f32_e32 v2, v6, v2
	v_fmac_f32_e32 v2, v94, v7
	v_cvt_pk_bf16_f32 v2, v2, v3
	ds_write_b16 v1, v2
	ds_read_u16 v2, v1 offset:64
	s_waitcnt lgkmcnt(0)
	v_lshlrev_b32_e32 v2, 16, v2
	v_mul_f32_e32 v2, v6, v2
	v_fmac_f32_e32 v2, v78, v7
	v_cvt_pk_bf16_f32 v2, v2, v3
	ds_write_b16 v1, v2 offset:64
	v_or_b32_e32 v1, s39, v188
	v_lshl_add_u32 v1, v1, 9, v4
	ds_read2_b32 v[6:7], v19 offset0:25 offset1:57
	ds_read_u16 v2, v1
	s_waitcnt lgkmcnt(0)
	v_lshlrev_b32_e32 v2, 16, v2
	v_mul_f32_e32 v2, v6, v2
	v_fmac_f32_e32 v2, v95, v7
	v_cvt_pk_bf16_f32 v2, v2, v3
	ds_write_b16 v1, v2
	ds_read_u16 v2, v1 offset:64
	s_waitcnt lgkmcnt(0)
	v_lshlrev_b32_e32 v2, 16, v2
	v_mul_f32_e32 v2, v6, v2
	v_fmac_f32_e32 v2, v79, v7
	v_cvt_pk_bf16_f32 v2, v2, v3
	ds_write_b16 v1, v2 offset:64
	v_or_b32_e32 v1, s39, v187
	v_lshl_add_u32 v1, v1, 9, v4
	ds_read2_b32 v[6:7], v19 offset0:26 offset1:58
	ds_read_u16 v2, v1
	s_waitcnt lgkmcnt(0)
	v_lshlrev_b32_e32 v2, 16, v2
	v_mul_f32_e32 v2, v6, v2
	v_fmac_f32_e32 v2, v96, v7
	v_cvt_pk_bf16_f32 v2, v2, v3
	ds_write_b16 v1, v2
	ds_read_u16 v2, v1 offset:64
	s_waitcnt lgkmcnt(0)
	v_lshlrev_b32_e32 v2, 16, v2
	v_mul_f32_e32 v2, v6, v2
	v_fmac_f32_e32 v2, v80, v7
	v_cvt_pk_bf16_f32 v2, v2, v3
	ds_write_b16 v1, v2 offset:64
	v_or_b32_e32 v1, s39, v186
	v_lshl_add_u32 v1, v1, 9, v4
	ds_read2_b32 v[4:5], v19 offset0:27 offset1:59
	ds_read_u16 v2, v1
	s_waitcnt lgkmcnt(0)
	v_lshlrev_b32_e32 v2, 16, v2
	v_mul_f32_e32 v2, v4, v2
	v_fmac_f32_e32 v2, v97, v5
	v_cvt_pk_bf16_f32 v2, v2, v3
	ds_write_b16 v1, v2
	ds_read_u16 v2, v1 offset:64
	s_waitcnt lgkmcnt(0)
	v_lshlrev_b32_e32 v2, 16, v2
	v_mul_f32_e32 v2, v4, v2
	v_fmac_f32_e32 v2, v81, v5
	v_cvt_pk_bf16_f32 v2, v2, v3
	ds_write_b16 v1, v2 offset:64
	v_add_u32_e32 v1, s8, v146
	v_mad_i64_i32 v[12:13], s[0:1], v1, s96, v[116:117]
	v_add_u32_e32 v1, s9, v118
	v_med3_i32 v1, v1, 0, v227
	v_mul_u32_u24_e32 v2, 0xa00, v1
	v_lshl_add_u64 v[24:25], v[2:3], 1, v[116:117]
	s_waitcnt lgkmcnt(0)
	s_waitcnt vmcnt(0) lgkmcnt(0)
	s_barrier
	global_load_dwordx4 v[68:71], v[12:13], off offset:2048
	global_load_dwordx4 v[4:7], v[12:13], off offset:2080
	global_load_dwordx4 v[8:11], v[12:13], off offset:2112
	s_nop 0
	global_load_dwordx4 v[12:15], v[12:13], off offset:2144
	s_nop 0
	global_load_dwordx4 v[20:23], v[24:25], off offset:3072
	global_load_dwordx4 v[36:39], v[24:25], off offset:3104
	global_load_dwordx4 v[40:43], v[24:25], off offset:3136
	global_load_dwordx4 v[44:47], v[24:25], off offset:3168
	v_add_u32_e32 v1, s9, v119
	v_med3_i32 v1, v1, 0, v227
	v_mul_u32_u24_e32 v2, 0xa00, v1
	v_add_u32_e32 v1, s9, v121
	v_med3_i32 v1, v1, 0, v227
	v_lshl_add_u64 v[24:25], v[2:3], 1, s[20:21]
	v_mul_u32_u24_e32 v2, 0xa00, v1
	v_add_u32_e32 v1, s9, v123
	v_lshl_add_u64 v[24:25], v[24:25], 0, v[16:17]
	v_med3_i32 v1, v1, 0, v227
	global_load_lds_dwordx4 v[24:25], off
	v_lshl_add_u64 v[24:25], v[2:3], 1, s[20:21]
	v_mul_u32_u24_e32 v2, 0xa00, v1
	v_add_u32_e32 v1, s9, v124
	v_lshl_add_u64 v[24:25], v[24:25], 0, v[16:17]
	s_mov_b32 m0, s30
	v_med3_i32 v1, v1, 0, v227
	global_load_lds_dwordx4 v[24:25], off
	v_lshl_add_u64 v[24:25], v[2:3], 1, s[20:21]
	v_mul_u32_u24_e32 v2, 0xa00, v1
	v_add_u32_e32 v1, s9, v137
	v_lshl_add_u64 v[24:25], v[24:25], 0, v[16:17]
	s_mov_b32 m0, s28
	v_med3_i32 v1, v1, 0, v227
	s_add_i32 s0, s10, 0xfffffa00
	global_load_lds_dwordx4 v[24:25], off
	v_lshl_add_u64 v[24:25], v[2:3], 1, s[20:21]
	v_mul_u32_u24_e32 v2, 0xa00, v1
	v_add_u32_e32 v1, s0, v119
	v_lshl_add_u64 v[24:25], v[24:25], 0, v[16:17]
	s_mov_b32 m0, s29
	v_med3_i32 v1, v1, 0, v227
	global_load_lds_dwordx4 v[24:25], off
	v_lshl_add_u64 v[24:25], v[2:3], 1, v[116:117]
	v_mul_u32_u24_e32 v2, 0xa00, v1
	v_add_u32_e32 v1, s0, v121
	global_load_dwordx4 v[52:55], v[24:25], off offset:3072
	global_load_dwordx4 v[80:83], v[24:25], off offset:3104
	global_load_dwordx4 v[76:79], v[24:25], off offset:3136
	global_load_dwordx4 v[72:75], v[24:25], off offset:3168
	v_lshl_add_u64 v[24:25], v[2:3], 1, s[20:21]
	v_med3_i32 v1, v1, 0, v227
	v_lshl_add_u64 v[24:25], v[24:25], 0, v[16:17]
	s_mov_b32 m0, s36
	v_mul_u32_u24_e32 v2, 0xa00, v1
	v_add_u32_e32 v1, s0, v123
	global_load_lds_dwordx4 v[24:25], off
	v_lshl_add_u64 v[24:25], v[2:3], 1, s[20:21]
	v_med3_i32 v1, v1, 0, v227
	v_lshl_add_u64 v[24:25], v[24:25], 0, v[16:17]
	s_mov_b32 m0, s34
	v_mul_u32_u24_e32 v2, 0xa00, v1
	v_add_u32_e32 v1, s0, v124
	global_load_lds_dwordx4 v[24:25], off
	v_lshl_add_u64 v[24:25], v[2:3], 1, s[20:21]
	v_med3_i32 v1, v1, 0, v227
	v_lshl_add_u64 v[24:25], v[24:25], 0, v[16:17]
	s_mov_b32 m0, s31
	v_mul_u32_u24_e32 v2, 0xa00, v1
	global_load_lds_dwordx4 v[24:25], off
	v_lshl_add_u64 v[24:25], v[2:3], 1, s[20:21]
	v_lshl_add_u64 v[24:25], v[24:25], 0, v[16:17]
	s_mov_b32 m0, s35
	v_add_u32_e32 v1, s9, v120
	global_load_lds_dwordx4 v[24:25], off
	s_waitcnt vmcnt(0)
	v_mfma_f32_32x32x16_bf16 v[20:35], v[20:23], v[68:71], 0
	v_readlane_b32 s0, v255, 22
	v_cmp_lt_i32_e32 vcc, -1, v1
	v_readlane_b32 s1, v255, 23
	s_and_b64 vcc, s[0:1], vcc
	v_readlane_b32 s0, v255, 24
	v_readlane_b32 s1, v255, 25
	s_waitcnt vmcnt(8)
	v_mfma_f32_32x32x16_bf16 v[20:35], v[36:39], v[4:7], v[20:35]
	ds_read_b64_tr_b16 v[84:85], v181 offset:0
	ds_read_b64_tr_b16 v[86:87], v181 offset:0x400
	ds_read_b64_tr_b16 v[64:65], v181 offset:0x800
	ds_read_b64_tr_b16 v[66:67], v181 offset:0xc00
	ds_read_b64_tr_b16 v[60:61], v181 offset:0x200
	ds_read_b64_tr_b16 v[62:63], v181 offset:0x600
	ds_read_b64_tr_b16 v[56:57], v181 offset:0xa00
	v_mfma_f32_32x32x16_bf16 v[20:35], v[40:43], v[8:11], v[20:35]
	ds_read_b64_tr_b16 v[58:59], v181 offset:0xe00
	v_mfma_f32_32x32x16_bf16 v[20:35], v[44:47], v[12:15], v[20:35]
	s_nop 11
	v_cndmask_b32_e32 v2, v18, v20, vcc
	v_cmp_lt_i32_e32 vcc, s90, v1
	s_and_b64 vcc, s[0:1], vcc
	v_readlane_b32 s0, v255, 26
	v_cndmask_b32_e32 v17, v18, v21, vcc
	v_cmp_lt_i32_e32 vcc, s13, v1
	v_readlane_b32 s1, v255, 27
	s_and_b64 vcc, s[0:1], vcc
	v_readlane_b32 s0, v255, 28
	v_cndmask_b32_e32 v20, v18, v22, vcc
	v_cmp_lt_i32_e32 vcc, s43, v1
	v_readlane_b32 s1, v255, 29
	s_and_b64 vcc, s[0:1], vcc
	v_readlane_b32 s0, v255, 30
	v_cndmask_b32_e32 v21, v18, v23, vcc
	v_cmp_lt_i32_e32 vcc, s76, v1
	v_readlane_b32 s1, v255, 31
	s_and_b64 vcc, s[0:1], vcc
	v_readlane_b32 s0, v255, 32
	v_cndmask_b32_e32 v22, v18, v24, vcc
	v_cmp_lt_i32_e32 vcc, s77, v1
	v_readlane_b32 s1, v255, 33
	s_and_b64 vcc, s[0:1], vcc
	v_readlane_b32 s0, v255, 34
	v_cndmask_b32_e32 v23, v18, v25, vcc
	v_cmp_lt_i32_e32 vcc, s78, v1
	v_readlane_b32 s1, v255, 35
	s_and_b64 vcc, s[0:1], vcc
	v_readlane_b32 s0, v255, 36
	v_cndmask_b32_e32 v24, v18, v26, vcc
	v_cmp_lt_i32_e32 vcc, s79, v1
	v_readlane_b32 s1, v255, 37
	s_and_b64 vcc, s[0:1], vcc
	v_readlane_b32 s0, v255, 38
	v_cndmask_b32_e32 v25, v18, v27, vcc
	v_cmp_lt_i32_e32 vcc, s80, v1
	v_readlane_b32 s1, v255, 39
	s_and_b64 vcc, s[0:1], vcc
	v_readlane_b32 s0, v255, 40
	v_cndmask_b32_e32 v26, v18, v28, vcc
	v_cmp_lt_i32_e32 vcc, s81, v1
	v_readlane_b32 s1, v255, 41
	s_and_b64 vcc, s[0:1], vcc
	v_readlane_b32 s0, v255, 42
	v_cndmask_b32_e32 v27, v18, v29, vcc
	v_cmp_lt_i32_e32 vcc, s82, v1
	v_readlane_b32 s1, v255, 43
	s_and_b64 vcc, s[0:1], vcc
	v_readlane_b32 s0, v255, 44
	v_cndmask_b32_e32 v28, v18, v30, vcc
	v_cmp_lt_i32_e32 vcc, s83, v1
	v_readlane_b32 s1, v255, 45
	s_and_b64 vcc, s[0:1], vcc
	v_readlane_b32 s0, v255, 46
	v_cndmask_b32_e32 v29, v18, v31, vcc
	v_cmp_lt_i32_e32 vcc, s84, v1
	v_readlane_b32 s1, v255, 47
	s_and_b64 vcc, s[0:1], vcc
	v_readlane_b32 s0, v255, 48
	v_cndmask_b32_e32 v30, v18, v32, vcc
	v_cmp_lt_i32_e32 vcc, s85, v1
	v_readlane_b32 s1, v255, 49
	s_and_b64 vcc, s[0:1], vcc
	v_readlane_b32 s0, v255, 50
	v_cndmask_b32_e32 v31, v18, v33, vcc
	v_cmp_lt_i32_e32 vcc, s86, v1
	v_readlane_b32 s1, v255, 51
	s_and_b64 vcc, s[0:1], vcc
	v_cndmask_b32_e32 v32, v18, v34, vcc
	v_max_f32_e32 v33, v17, v17
	v_max_f32_e32 v34, v2, v2
	v_max_f32_e32 v33, v34, v33
	v_max3_f32 v33, v33, v20, v21
	v_max3_f32 v33, v33, v22, v23
	v_readlane_b32 s0, v255, 52
	v_max3_f32 v33, v33, v24, v25
	v_cmp_lt_i32_e32 vcc, s87, v1
	v_readlane_b32 s1, v255, 53
	v_max3_f32 v33, v33, v26, v27
	s_and_b64 vcc, s[0:1], vcc
	v_max3_f32 v33, v33, v28, v29
	v_cndmask_b32_e32 v1, v18, v35, vcc
	v_max3_f32 v33, v33, v30, v31
	v_max3_f32 v33, v33, v32, v1
	v_mov_b32_e32 v34, v33
	s_nop 1
	v_permlane32_swap_b32_e32 v33, v34
	s_mov_b32 s0, 0xf149f2ca
	v_max3_f32 v127, v33, v34, s0
	v_sub_f32_e32 v2, v2, v127
	v_exp_f32_e32 v2, v2
	v_sub_f32_e32 v17, v17, v127
	v_exp_f32_e32 v17, v17
	v_sub_f32_e32 v20, v20, v127
	v_exp_f32_e32 v20, v20
	v_sub_f32_e32 v21, v21, v127
	v_exp_f32_e32 v21, v21
	v_sub_f32_e32 v22, v22, v127
	v_add_f32_e32 v34, 0, v2
	v_exp_f32_e32 v22, v22
	v_sub_f32_e32 v23, v23, v127
	v_add_f32_e32 v34, v17, v34
	v_exp_f32_e32 v23, v23
	v_sub_f32_e32 v24, v24, v127
	v_add_f32_e32 v34, v20, v34
	v_exp_f32_e32 v24, v24
	v_sub_f32_e32 v25, v25, v127
	v_add_f32_e32 v34, v21, v34
	v_exp_f32_e32 v25, v25
	v_sub_f32_e32 v26, v26, v127
	v_add_f32_e32 v34, v22, v34
	v_exp_f32_e32 v26, v26
	v_sub_f32_e32 v27, v27, v127
	v_add_f32_e32 v34, v23, v34
	v_exp_f32_e32 v27, v27
	v_sub_f32_e32 v28, v28, v127
	v_add_f32_e32 v34, v24, v34
	v_exp_f32_e32 v28, v28
	v_sub_f32_e32 v29, v29, v127
	v_add_f32_e32 v34, v25, v34
	v_exp_f32_e32 v29, v29
	v_sub_f32_e32 v30, v30, v127
	v_add_f32_e32 v34, v26, v34
	v_exp_f32_e32 v30, v30
	v_sub_f32_e32 v31, v31, v127
	v_add_f32_e32 v34, v27, v34
	v_exp_f32_e32 v31, v31
	v_sub_f32_e32 v32, v32, v127
	v_add_f32_e32 v34, v28, v34
	v_exp_f32_e32 v32, v32
	v_sub_f32_e32 v1, v1, v127
	v_add_f32_e32 v34, v29, v34
	v_exp_f32_e32 v1, v1
	v_sub_f32_e32 v33, 0xf149f2ca, v127
	v_add_f32_e32 v34, v30, v34
	v_add_f32_e32 v34, v31, v34
	v_exp_f32_e32 v125, v33
	v_add_f32_e32 v34, v32, v34
	v_add_f32_e32 v130, v1, v34
	v_mov_b32_e32 v131, v130
	v_cvt_pk_bf16_f32 v104, v2, v17
	v_cvt_pk_bf16_f32 v105, v20, v21
	v_cvt_pk_bf16_f32 v106, v22, v23
	v_cvt_pk_bf16_f32 v107, v24, v25
	v_cvt_pk_bf16_f32 v100, v26, v27
	v_cvt_pk_bf16_f32 v101, v28, v29
	v_cvt_pk_bf16_f32 v102, v30, v31
	v_cvt_pk_bf16_f32 v103, v32, v1
	s_nop 1
	v_permlane32_swap_b32_e32 v130, v131
	v_permlane32_swap_b32_e32 v104, v106
	v_permlane32_swap_b32_e32 v105, v107
	v_permlane32_swap_b32_e32 v100, v102
	v_permlane32_swap_b32_e32 v101, v103
	v_cmp_gt_f32_e32 vcc, 1.0, v125
	s_cbranch_vccz .LBB0_1347
	s_and_saveexec_b64 s[0:1], s[6:7]
	ds_write_b32 v185, v125
	s_or_b64 exec, exec, s[0:1]
	ds_read_b128 v[20:23], v19 offset:96
	ds_read_b128 v[24:27], v19 offset:64
	ds_read_b128 v[36:39], v19 offset:32
	ds_read_b128 v[40:43], v19
	s_waitcnt lgkmcnt(0)
	v_pk_mul_f32 v[34:35], v[22:23], 0 op_sel_hi:[1,0]
	v_pk_mul_f32 v[30:31], v[26:27], 0 op_sel_hi:[1,0]
	v_pk_mul_f32 v[26:27], v[38:39], 0 op_sel_hi:[1,0]
	v_pk_mul_f32 v[22:23], v[42:43], 0 op_sel_hi:[1,0]
	v_pk_mul_f32 v[32:33], v[20:21], 0 op_sel_hi:[1,0]
	v_pk_mul_f32 v[28:29], v[24:25], 0 op_sel_hi:[1,0]
	v_pk_mul_f32 v[24:25], v[36:37], 0 op_sel_hi:[1,0]
	v_pk_mul_f32 v[20:21], v[40:41], 0 op_sel_hi:[1,0]
	s_branch .LBB0_1348

.LBB0_1350:
	s_nop 10
	v_max_f32_e32 v1, v53, v53
	v_max_f32_e32 v2, v52, v52
	v_max_f32_e32 v1, v2, v1
	v_max3_f32 v1, v1, v54, v55
	v_max3_f32 v1, v1, v56, v57
	v_max3_f32 v1, v1, v58, v59
	v_max3_f32 v1, v1, v60, v61
	v_max3_f32 v1, v1, v62, v63
	v_max3_f32 v1, v1, v64, v65
	v_max3_f32 v1, v1, v66, v67
	v_mov_b32_e32 v2, v1
	s_nop 1
	v_permlane32_swap_b32_e32 v1, v2
	v_max3_f32 v129, v127, v1, v2
	v_sub_f32_e32 v2, v52, v129
	v_exp_f32_e32 v2, v2
	v_sub_f32_e32 v17, v53, v129
	v_exp_f32_e32 v17, v17
	v_sub_f32_e32 v52, v54, v129
	v_exp_f32_e32 v52, v52
	v_sub_f32_e32 v53, v55, v129
	v_exp_f32_e32 v53, v53
	v_sub_f32_e32 v55, v56, v129
	v_add_f32_e32 v54, 0, v2
	v_exp_f32_e32 v55, v55
	v_sub_f32_e32 v56, v57, v129
	v_add_f32_e32 v54, v17, v54
	v_exp_f32_e32 v72, v56
	v_sub_f32_e32 v56, v58, v129
	v_add_f32_e32 v54, v52, v54
	v_exp_f32_e32 v73, v56
	v_sub_f32_e32 v56, v59, v129
	v_add_f32_e32 v54, v53, v54
	v_exp_f32_e32 v59, v56
	v_sub_f32_e32 v56, v60, v129
	v_add_f32_e32 v54, v55, v54
	v_exp_f32_e32 v60, v56
	v_sub_f32_e32 v56, v61, v129
	v_add_f32_e32 v54, v72, v54
	v_exp_f32_e32 v61, v56
	v_sub_f32_e32 v56, v62, v129
	v_add_f32_e32 v54, v73, v54
	v_exp_f32_e32 v62, v56
	v_sub_f32_e32 v56, v63, v129
	v_add_f32_e32 v54, v59, v54
	v_exp_f32_e32 v63, v56
	v_sub_f32_e32 v56, v64, v129
	v_add_f32_e32 v54, v60, v54
	v_exp_f32_e32 v64, v56
	v_sub_f32_e32 v56, v65, v129
	v_add_f32_e32 v54, v61, v54
	v_exp_f32_e32 v65, v56
	v_sub_f32_e32 v56, v66, v129
	v_add_f32_e32 v54, v62, v54
	v_exp_f32_e32 v66, v56
	v_sub_f32_e32 v56, v67, v129
	v_add_f32_e32 v54, v63, v54
	v_exp_f32_e32 v67, v56
	v_sub_f32_e32 v1, v127, v129
	v_add_f32_e32 v54, v64, v54
	v_add_f32_e32 v54, v65, v54
	v_exp_f32_e32 v132, v1
	v_add_f32_e32 v54, v66, v54
	v_add_f32_e32 v133, v67, v54
	v_mov_b32_e32 v134, v133
	v_cvt_pk_bf16_f32 v56, v2, v17
	v_cvt_pk_bf16_f32 v57, v52, v53
	v_cvt_pk_bf16_f32 v58, v55, v72
	v_cvt_pk_bf16_f32 v59, v73, v59
	v_cvt_pk_bf16_f32 v52, v60, v61
	v_cvt_pk_bf16_f32 v53, v62, v63
	v_cvt_pk_bf16_f32 v54, v64, v65
	v_cvt_pk_bf16_f32 v55, v66, v67
	s_nop 1
	v_permlane32_swap_b32_e32 v133, v134
	v_permlane32_swap_b32_e32 v56, v58
	v_permlane32_swap_b32_e32 v57, v59
	v_permlane32_swap_b32_e32 v52, v54
	v_permlane32_swap_b32_e32 v53, v55
	v_cmp_gt_f32_e32 vcc, 1.0, v132
	s_cbranch_vccz .LBB0_1354
	s_and_saveexec_b64 s[4:5], s[6:7]
	ds_write_b32 v185, v132
	s_or_b64 exec, exec, s[4:5]
	ds_read_b128 v[60:63], v19 offset:96
	ds_read_b128 v[64:67], v19 offset:64
	ds_read_b128 v[72:75], v19 offset:32
	ds_read_b128 v[76:79], v19
	s_waitcnt lgkmcnt(0)
	v_pk_mul_f32 v[50:51], v[50:51], v[62:63]
	v_pk_mul_f32 v[46:47], v[46:47], v[66:67]
	v_pk_mul_f32 v[42:43], v[42:43], v[74:75]
	v_pk_mul_f32 v[38:39], v[38:39], v[78:79]
	v_pk_mul_f32 v[48:49], v[48:49], v[60:61]
	v_pk_mul_f32 v[44:45], v[44:45], v[64:65]
	v_pk_mul_f32 v[40:41], v[40:41], v[72:73]
	v_pk_mul_f32 v[36:37], v[36:37], v[76:77]
	v_pk_mul_f32 v[34:35], v[34:35], v[62:63]
	v_pk_mul_f32 v[30:31], v[30:31], v[66:67]
	v_pk_mul_f32 v[26:27], v[26:27], v[74:75]
	v_pk_mul_f32 v[22:23], v[22:23], v[78:79]
	v_pk_mul_f32 v[32:33], v[32:33], v[60:61]
	v_pk_mul_f32 v[28:29], v[28:29], v[64:65]
	v_pk_mul_f32 v[24:25], v[24:25], v[72:73]
	v_pk_mul_f32 v[20:21], v[20:21], v[76:77]

.LBB0_1356:
	s_nop 10
	v_max_f32_e32 v1, v53, v53
	v_max_f32_e32 v2, v52, v52
	v_max_f32_e32 v1, v2, v1
	v_max3_f32 v1, v1, v54, v55
	v_max3_f32 v1, v1, v56, v57
	v_max3_f32 v1, v1, v58, v59
	v_max3_f32 v1, v1, v60, v61
	v_max3_f32 v1, v1, v62, v63
	v_max3_f32 v1, v1, v64, v65
	v_max3_f32 v1, v1, v66, v67
	v_mov_b32_e32 v2, v1
	s_nop 1
	v_permlane32_swap_b32_e32 v1, v2
	v_max3_f32 v127, v129, v1, v2
	v_sub_f32_e32 v2, v52, v127
	v_exp_f32_e32 v2, v2
	v_sub_f32_e32 v17, v53, v127
	v_exp_f32_e32 v17, v17
	v_sub_f32_e32 v52, v54, v127
	v_exp_f32_e32 v52, v52
	v_sub_f32_e32 v53, v55, v127
	v_exp_f32_e32 v53, v53
	v_sub_f32_e32 v55, v56, v127
	v_add_f32_e32 v54, 0, v2
	v_exp_f32_e32 v55, v55
	v_sub_f32_e32 v56, v57, v127
	v_add_f32_e32 v54, v17, v54
	v_exp_f32_e32 v84, v56
	v_sub_f32_e32 v56, v58, v127
	v_add_f32_e32 v54, v52, v54
	v_exp_f32_e32 v85, v56
	v_sub_f32_e32 v56, v59, v127
	v_add_f32_e32 v54, v53, v54
	v_exp_f32_e32 v59, v56
	v_sub_f32_e32 v56, v60, v127
	v_add_f32_e32 v54, v55, v54
	v_exp_f32_e32 v60, v56
	v_sub_f32_e32 v56, v61, v127
	v_add_f32_e32 v54, v84, v54
	v_exp_f32_e32 v61, v56
	v_sub_f32_e32 v56, v62, v127
	v_add_f32_e32 v54, v85, v54
	v_exp_f32_e32 v62, v56
	v_sub_f32_e32 v56, v63, v127
	v_add_f32_e32 v54, v59, v54
	v_exp_f32_e32 v63, v56
	v_sub_f32_e32 v56, v64, v127
	v_add_f32_e32 v54, v60, v54
	v_exp_f32_e32 v64, v56
	v_sub_f32_e32 v56, v65, v127
	v_add_f32_e32 v54, v61, v54
	v_exp_f32_e32 v65, v56
	v_sub_f32_e32 v56, v66, v127
	v_add_f32_e32 v54, v62, v54
	v_exp_f32_e32 v66, v56
	v_sub_f32_e32 v56, v67, v127
	v_add_f32_e32 v54, v63, v54
	v_exp_f32_e32 v67, v56
	v_sub_f32_e32 v1, v129, v127
	v_add_f32_e32 v54, v64, v54
	v_add_f32_e32 v54, v65, v54
	v_exp_f32_e32 v135, v1
	v_add_f32_e32 v54, v66, v54
	v_add_f32_e32 v136, v67, v54
	v_mov_b32_e32 v138, v136
	v_cvt_pk_bf16_f32 v56, v2, v17
	v_cvt_pk_bf16_f32 v57, v52, v53
	v_cvt_pk_bf16_f32 v58, v55, v84
	v_cvt_pk_bf16_f32 v59, v85, v59
	v_cvt_pk_bf16_f32 v52, v60, v61
	v_cvt_pk_bf16_f32 v53, v62, v63
	v_cvt_pk_bf16_f32 v54, v64, v65
	v_cvt_pk_bf16_f32 v55, v66, v67
	s_nop 1
	v_permlane32_swap_b32_e32 v136, v138
	v_permlane32_swap_b32_e32 v56, v58
	v_permlane32_swap_b32_e32 v57, v59
	v_permlane32_swap_b32_e32 v52, v54
	v_permlane32_swap_b32_e32 v53, v55
	v_cmp_gt_f32_e32 vcc, 1.0, v135
	s_cbranch_vccz .LBB0_1360
	s_and_saveexec_b64 s[0:1], s[6:7]
	ds_write_b32 v185, v135
	s_or_b64 exec, exec, s[0:1]
	ds_read_b128 v[60:63], v19 offset:96
	ds_read_b128 v[64:67], v19 offset:64
	ds_read_b128 v[84:87], v19 offset:32
	ds_read_b128 v[88:91], v19
	s_waitcnt lgkmcnt(0)
	v_pk_mul_f32 v[50:51], v[50:51], v[62:63]
	v_pk_mul_f32 v[46:47], v[46:47], v[66:67]
	v_pk_mul_f32 v[42:43], v[42:43], v[86:87]
	v_pk_mul_f32 v[38:39], v[38:39], v[90:91]
	v_pk_mul_f32 v[48:49], v[48:49], v[60:61]
	v_pk_mul_f32 v[44:45], v[44:45], v[64:65]
	v_pk_mul_f32 v[40:41], v[40:41], v[84:85]
	v_pk_mul_f32 v[36:37], v[36:37], v[88:89]
	v_pk_mul_f32 v[34:35], v[34:35], v[62:63]
	v_pk_mul_f32 v[30:31], v[30:31], v[66:67]
	v_pk_mul_f32 v[26:27], v[26:27], v[86:87]
	v_pk_mul_f32 v[22:23], v[22:23], v[90:91]
	v_pk_mul_f32 v[32:33], v[32:33], v[60:61]
	v_pk_mul_f32 v[28:29], v[28:29], v[64:65]
	v_pk_mul_f32 v[24:25], v[24:25], v[84:85]
	v_pk_mul_f32 v[20:21], v[20:21], v[88:89]

.LBB0_1362:
	s_nop 10
	v_max_f32_e32 v1, v53, v53
	v_max_f32_e32 v2, v52, v52
	v_max_f32_e32 v1, v2, v1
	v_max3_f32 v1, v1, v54, v55
	v_max3_f32 v1, v1, v56, v57
	v_max3_f32 v1, v1, v58, v59
	v_max3_f32 v1, v1, v60, v61
	v_max3_f32 v1, v1, v62, v63
	v_max3_f32 v1, v1, v64, v65
	v_max3_f32 v1, v1, v66, v67
	v_mov_b32_e32 v2, v1
	s_nop 1
	v_permlane32_swap_b32_e32 v1, v2
	v_max3_f32 v109, v127, v1, v2
	v_sub_f32_e32 v2, v52, v109
	v_exp_f32_e32 v52, v2
	v_sub_f32_e32 v2, v53, v109
	v_exp_f32_e32 v53, v2
	v_sub_f32_e32 v2, v54, v109
	v_exp_f32_e32 v54, v2
	v_sub_f32_e32 v2, v55, v109
	v_exp_f32_e32 v55, v2
	v_sub_f32_e32 v17, v56, v109
	v_add_f32_e32 v2, 0, v52
	v_exp_f32_e32 v56, v17
	v_sub_f32_e32 v17, v57, v109
	v_add_f32_e32 v2, v53, v2
	v_exp_f32_e32 v57, v17
	v_sub_f32_e32 v17, v58, v109
	v_add_f32_e32 v2, v54, v2
	v_exp_f32_e32 v58, v17
	v_sub_f32_e32 v17, v59, v109
	v_add_f32_e32 v2, v55, v2
	v_exp_f32_e32 v59, v17
	v_sub_f32_e32 v17, v60, v109
	v_add_f32_e32 v2, v56, v2
	v_exp_f32_e32 v60, v17
	v_sub_f32_e32 v17, v61, v109
	v_add_f32_e32 v2, v57, v2
	v_exp_f32_e32 v61, v17
	v_sub_f32_e32 v17, v62, v109
	v_add_f32_e32 v2, v58, v2
	v_exp_f32_e32 v62, v17
	v_sub_f32_e32 v17, v63, v109
	v_add_f32_e32 v2, v59, v2
	v_exp_f32_e32 v63, v17
	v_sub_f32_e32 v17, v64, v109
	v_add_f32_e32 v2, v60, v2
	v_exp_f32_e32 v64, v17
	v_sub_f32_e32 v17, v65, v109
	v_add_f32_e32 v2, v61, v2
	v_exp_f32_e32 v65, v17
	v_sub_f32_e32 v17, v66, v109
	v_add_f32_e32 v2, v62, v2
	v_exp_f32_e32 v66, v17
	v_sub_f32_e32 v17, v67, v109
	v_add_f32_e32 v2, v63, v2
	v_exp_f32_e32 v67, v17
	v_add_f32_e32 v2, v64, v2
	v_add_f32_e32 v2, v65, v2
	v_sub_f32_e32 v1, v127, v109
	v_add_f32_e32 v2, v66, v2
	v_add_f32_e32 v17, v67, v2
	v_exp_f32_e32 v2, v1
	v_mov_b32_e32 v108, v17
	v_cvt_pk_bf16_f32 v52, v52, v53
	v_cvt_pk_bf16_f32 v53, v54, v55
	v_cvt_pk_bf16_f32 v54, v56, v57
	v_cvt_pk_bf16_f32 v55, v58, v59
	v_cvt_pk_bf16_f32 v56, v60, v61
	v_cvt_pk_bf16_f32 v57, v62, v63
	v_cvt_pk_bf16_f32 v58, v64, v65
	v_cvt_pk_bf16_f32 v59, v66, v67
	s_mov_b32 s74, 0x3c800000
	s_nop 0
	v_permlane32_swap_b32_e32 v17, v108
	v_permlane32_swap_b32_e32 v52, v54
	v_permlane32_swap_b32_e32 v53, v55
	v_permlane32_swap_b32_e32 v56, v58
	v_permlane32_swap_b32_e32 v57, v59
	v_cmp_gt_f32_e32 vcc, 1.0, v2
	s_cbranch_vccz .LBB0_1366
	s_and_saveexec_b64 s[0:1], s[6:7]
	ds_write_b32 v185, v2
	s_or_b64 exec, exec, s[0:1]
	ds_read_b128 v[60:63], v19 offset:96
	ds_read_b128 v[64:67], v19 offset:64
	ds_read_b128 v[72:75], v19 offset:32
	ds_read_b128 v[110:113], v19
	s_waitcnt lgkmcnt(0)
	v_pk_mul_f32 v[50:51], v[50:51], v[62:63]
	v_pk_mul_f32 v[46:47], v[46:47], v[66:67]
	v_pk_mul_f32 v[42:43], v[42:43], v[74:75]
	v_pk_mul_f32 v[38:39], v[38:39], v[112:113]
	v_pk_mul_f32 v[48:49], v[48:49], v[60:61]
	v_pk_mul_f32 v[44:45], v[44:45], v[64:65]
	v_pk_mul_f32 v[40:41], v[40:41], v[72:73]
	v_pk_mul_f32 v[36:37], v[36:37], v[110:111]
	v_pk_mul_f32 v[34:35], v[34:35], v[62:63]
	v_pk_mul_f32 v[30:31], v[30:31], v[66:67]
	v_pk_mul_f32 v[26:27], v[26:27], v[74:75]
	v_pk_mul_f32 v[22:23], v[22:23], v[112:113]
	v_pk_mul_f32 v[32:33], v[32:33], v[60:61]
	v_pk_mul_f32 v[28:29], v[28:29], v[64:65]
	v_pk_mul_f32 v[24:25], v[24:25], v[72:73]
	v_pk_mul_f32 v[20:21], v[20:21], v[110:111]
.LBB0_1366:
	s_waitcnt lgkmcnt(0)
	v_or_b32_e32 v127, 0x800, v120
	v_mfma_f32_32x32x16_bf16 v[36:51], v[52:55], v[80:83], v[36:51]
	v_add_u32_e32 v1, s9, v127
	v_cmp_lt_i32_e32 vcc, -1, v1
	s_and_b64 vcc, s[14:15], vcc
	v_readlane_b32 s0, v255, 54
	v_readlane_b32 s1, v255, 55
	s_waitcnt vmcnt(0)
	v_mfma_f32_32x32x16_bf16 v[20:35], v[52:55], v[84:87], v[20:35]
	ds_read_b64_tr_b16 v[84:85], v181 offset:0
	ds_read_b64_tr_b16 v[86:87], v181 offset:0x400
	ds_read_b64_tr_b16 v[80:81], v181 offset:0x800
	ds_read_b64_tr_b16 v[82:83], v181 offset:0xc00
	v_mfma_f32_32x32x16_bf16 v[36:51], v[56:59], v[76:79], v[36:51]
	ds_read_b64_tr_b16 v[76:77], v181 offset:0x200
	ds_read_b64_tr_b16 v[78:79], v181 offset:0x600
	ds_read_b64_tr_b16 v[72:73], v181 offset:0xa00
	ds_read_b64_tr_b16 v[74:75], v181 offset:0xe00
	v_mfma_f32_32x32x16_bf16 v[20:35], v[56:59], v[100:103], v[20:35]
	s_waitcnt vmcnt(0)
	v_mfma_f32_32x32x16_bf16 v[52:67], v[104:107], v[68:71], 0
	v_mfma_f32_32x32x16_bf16 v[52:67], v[88:91], v[4:7], v[52:67]
	v_mfma_f32_32x32x16_bf16 v[52:67], v[92:95], v[8:11], v[52:67]
	v_mfma_f32_32x32x16_bf16 v[52:67], v[96:99], v[12:15], v[52:67]
	s_nop 11
	v_cndmask_b32_e32 v4, v18, v52, vcc
	v_cmp_lt_i32_e32 vcc, s90, v1
	s_and_b64 vcc, s[70:71], vcc
	s_nop 0
	v_cndmask_b32_e32 v5, v18, v53, vcc
	v_cmp_lt_i32_e32 vcc, s13, v1
	s_and_b64 vcc, s[16:17], vcc
	v_max_f32_e32 v12, v5, v5
	v_cndmask_b32_e32 v6, v18, v54, vcc
	v_cmp_lt_i32_e32 vcc, s43, v1
	s_and_b64 vcc, s[66:67], vcc
	s_nop 0
	v_cndmask_b32_e32 v7, v18, v55, vcc
	v_cmp_lt_i32_e32 vcc, s76, v1
	s_and_b64 vcc, s[64:65], vcc
	s_nop 0
	v_cndmask_b32_e32 v8, v18, v56, vcc
	v_cmp_lt_i32_e32 vcc, s77, v1
	s_and_b64 vcc, s[62:63], vcc
	v_max_f32_e32 v56, v4, v4
	v_cndmask_b32_e32 v9, v18, v57, vcc
	v_cmp_lt_i32_e32 vcc, s78, v1
	s_and_b64 vcc, s[44:45], vcc
	v_max_f32_e32 v12, v56, v12
	v_cndmask_b32_e32 v10, v18, v58, vcc
	v_cmp_lt_i32_e32 vcc, s79, v1
	s_and_b64 vcc, s[0:1], vcc
	v_max3_f32 v12, v12, v6, v7
	v_cndmask_b32_e32 v11, v18, v59, vcc
	v_cmp_lt_i32_e32 vcc, s80, v1
	s_and_b64 vcc, s[46:47], vcc
	v_max3_f32 v12, v12, v8, v9
	v_cndmask_b32_e32 v13, v18, v60, vcc
	v_cmp_lt_i32_e32 vcc, s81, v1
	s_and_b64 vcc, s[52:53], vcc
	v_max3_f32 v12, v12, v10, v11
	v_cndmask_b32_e32 v14, v18, v61, vcc
	v_cmp_lt_i32_e32 vcc, s82, v1
	s_and_b64 vcc, s[48:49], vcc
	v_max3_f32 v12, v12, v13, v14
	v_cndmask_b32_e32 v15, v18, v62, vcc
	v_cmp_lt_i32_e32 vcc, s83, v1
	s_and_b64 vcc, s[54:55], vcc
	s_nop 0
	v_cndmask_b32_e32 v52, v18, v63, vcc
	v_cmp_lt_i32_e32 vcc, s84, v1
	s_and_b64 vcc, s[50:51], vcc
	v_max3_f32 v12, v12, v15, v52
	v_cndmask_b32_e32 v53, v18, v64, vcc
	v_cmp_lt_i32_e32 vcc, s85, v1
	s_and_b64 vcc, s[56:57], vcc
	s_nop 0
	v_cndmask_b32_e32 v54, v18, v65, vcc
	v_cmp_lt_i32_e32 vcc, s86, v1
	s_and_b64 vcc, s[60:61], vcc
	v_max3_f32 v12, v12, v53, v54
	v_cndmask_b32_e32 v55, v18, v66, vcc
	v_cmp_lt_i32_e32 vcc, s87, v1
	s_and_b64 vcc, s[58:59], vcc
	s_nop 0
	v_cndmask_b32_e32 v1, v18, v67, vcc
	v_max3_f32 v12, v12, v55, v1
	v_mov_b32_e32 v56, v12
	s_nop 1
	v_permlane32_swap_b32_e32 v12, v56
	v_max3_f32 v12, v109, v12, v56
	v_sub_f32_e32 v4, v4, v12
	v_exp_f32_e32 v4, v4
	v_sub_f32_e32 v5, v5, v12
	v_exp_f32_e32 v5, v5
	v_sub_f32_e32 v6, v6, v12
	v_exp_f32_e32 v6, v6
	v_sub_f32_e32 v7, v7, v12
	v_exp_f32_e32 v7, v7
	v_sub_f32_e32 v8, v8, v12
	v_add_f32_e32 v57, 0, v4
	v_exp_f32_e32 v8, v8
	v_sub_f32_e32 v9, v9, v12
	v_add_f32_e32 v57, v5, v57
	v_exp_f32_e32 v9, v9
	v_sub_f32_e32 v10, v10, v12
	v_add_f32_e32 v57, v6, v57
	v_exp_f32_e32 v10, v10
	v_sub_f32_e32 v11, v11, v12
	v_add_f32_e32 v57, v7, v57
	v_exp_f32_e32 v11, v11
	v_sub_f32_e32 v13, v13, v12
	v_add_f32_e32 v57, v8, v57
	v_exp_f32_e32 v58, v13
	v_add_f32_e32 v57, v9, v57
	v_add_f32_e32 v57, v10, v57
	v_add_f32_e32 v57, v11, v57
	v_sub_f32_e32 v14, v14, v12
	v_add_f32_e32 v13, v58, v57
	v_exp_f32_e32 v57, v14
	v_sub_f32_e32 v14, v15, v12
	v_exp_f32_e32 v59, v14
	v_sub_f32_e32 v14, v52, v12
	v_exp_f32_e32 v52, v14
	v_sub_f32_e32 v14, v53, v12
	v_exp_f32_e32 v53, v14
	v_sub_f32_e32 v14, v54, v12
	v_add_f32_e32 v13, v57, v13
	v_exp_f32_e32 v54, v14
	v_sub_f32_e32 v14, v55, v12
	v_add_f32_e32 v13, v59, v13
	v_exp_f32_e32 v55, v14
	v_sub_f32_e32 v1, v1, v12
	v_add_f32_e32 v13, v52, v13
	v_exp_f32_e32 v1, v1
	v_add_f32_e32 v13, v53, v13
	v_add_f32_e32 v13, v54, v13
	v_sub_f32_e32 v56, v109, v12
	v_add_f32_e32 v13, v55, v13
	v_add_f32_e32 v14, v1, v13
	v_exp_f32_e32 v13, v56
	v_mov_b32_e32 v15, v14
	v_cvt_pk_bf16_f32 v4, v4, v5
	v_cvt_pk_bf16_f32 v5, v6, v7
	v_cvt_pk_bf16_f32 v6, v8, v9
	v_cvt_pk_bf16_f32 v7, v10, v11
	v_cvt_pk_bf16_f32 v8, v58, v57
	v_cvt_pk_bf16_f32 v9, v59, v52
	v_cvt_pk_bf16_f32 v10, v53, v54
	v_cvt_pk_bf16_f32 v11, v55, v1
	s_nop 1
	v_permlane32_swap_b32_e32 v14, v15
	v_permlane32_swap_b32_e32 v4, v6
	v_permlane32_swap_b32_e32 v5, v7
	v_permlane32_swap_b32_e32 v8, v10
	v_permlane32_swap_b32_e32 v9, v11
	v_cmp_gt_f32_e32 vcc, 1.0, v13
	s_cbranch_vccz .LBB0_1370
	s_and_saveexec_b64 s[0:1], s[6:7]
	ds_write_b32 v185, v13
	s_or_b64 exec, exec, s[0:1]
	ds_read_b128 v[52:55], v19 offset:96
	ds_read_b128 v[56:59], v19 offset:64
	ds_read_b128 v[60:63], v19 offset:32
	ds_read_b128 v[64:67], v19
	s_waitcnt lgkmcnt(0)
	v_pk_mul_f32 v[50:51], v[50:51], v[54:55]
	v_pk_mul_f32 v[46:47], v[46:47], v[58:59]
	v_pk_mul_f32 v[42:43], v[42:43], v[62:63]
	v_pk_mul_f32 v[38:39], v[38:39], v[66:67]
	v_pk_mul_f32 v[48:49], v[48:49], v[52:53]
	v_pk_mul_f32 v[44:45], v[44:45], v[56:57]
	v_pk_mul_f32 v[40:41], v[40:41], v[60:61]
	v_pk_mul_f32 v[36:37], v[36:37], v[64:65]
	v_pk_mul_f32 v[34:35], v[34:35], v[54:55]
	v_pk_mul_f32 v[30:31], v[30:31], v[58:59]
	v_pk_mul_f32 v[26:27], v[26:27], v[62:63]
	v_pk_mul_f32 v[22:23], v[22:23], v[66:67]
	v_pk_mul_f32 v[32:33], v[32:33], v[52:53]
	v_pk_mul_f32 v[28:29], v[28:29], v[56:57]
	v_pk_mul_f32 v[24:25], v[24:25], v[60:61]
	v_pk_mul_f32 v[20:21], v[20:21], v[64:65]

.LBB0_1372:
	s_or_b64 exec, exec, s[0:1]
	v_readlane_b32 s0, v255, 56
	v_lshlrev_b32_e32 v148, 13, v184
	s_waitcnt lgkmcnt(0)
	v_lshlrev_b32_e32 v149, 11, v204
	v_add_u32_e32 v1, s0, v183
	v_add_u32_e32 v2, v1, v148
	ds_read2_b32 v[4:5], v19 offset1:32
	ds_read_u16 v6, v2
	v_lshlrev_b32_e32 v147, 11, v199
	v_lshlrev_b32_e32 v145, 11, v198
	v_lshlrev_b32_e32 v142, 11, v197
	v_lshlrev_b32_e32 v141, 11, v196
	s_waitcnt lgkmcnt(0)
	v_lshlrev_b32_e32 v6, 16, v6
	v_mul_f32_e32 v6, v4, v6
	v_fmac_f32_e32 v6, v36, v5
	v_cvt_pk_bf16_f32 v6, v6, v3
	ds_write_b16 v2, v6
	ds_read_u16 v6, v2 offset:64
	v_lshlrev_b32_e32 v140, 11, v195
	v_lshlrev_b32_e32 v138, 11, v194
	v_lshlrev_b32_e32 v136, 11, v193
	v_lshlrev_b32_e32 v135, 11, v192
	s_waitcnt lgkmcnt(0)
	v_lshlrev_b32_e32 v6, 16, v6
	v_mul_f32_e32 v4, v4, v6
	v_fmac_f32_e32 v4, v20, v5
	v_cvt_pk_bf16_f32 v4, v4, v3
	ds_write_b16 v2, v4 offset:64
	v_add_u32_e32 v2, v1, v149
	ds_read2_b32 v[4:5], v19 offset0:1 offset1:33
	ds_read_u16 v6, v2
	v_lshlrev_b32_e32 v134, 11, v191
	v_lshlrev_b32_e32 v133, 11, v190
	v_lshlrev_b32_e32 v132, 11, v189
	v_lshlrev_b32_e32 v131, 11, v188
	s_waitcnt lgkmcnt(0)
	v_lshlrev_b32_e32 v6, 16, v6
	v_mul_f32_e32 v6, v4, v6
	v_fmac_f32_e32 v6, v37, v5
	v_cvt_pk_bf16_f32 v6, v6, v3
	ds_write_b16 v2, v6
	ds_read_u16 v6, v2 offset:64
	v_lshlrev_b32_e32 v130, 11, v187
	v_lshlrev_b32_e32 v125, 11, v186
	s_or_b32 s10, s8, 1
	s_add_i32 s12, s10, s26
	s_waitcnt lgkmcnt(0)
	v_lshlrev_b32_e32 v6, 16, v6
	v_mul_f32_e32 v4, v4, v6
	v_fmac_f32_e32 v4, v21, v5
	v_cvt_pk_bf16_f32 v4, v4, v3
	ds_write_b16 v2, v4 offset:64
	v_add_u32_e32 v2, v1, v147
	ds_read2_b32 v[4:5], v19 offset0:2 offset1:34
	ds_read_u16 v6, v2
	s_add_i32 s11, s12, 0xfffff800
	v_mov_b32_e32 v17, v3
	s_mov_b32 m0, s27
	s_waitcnt lgkmcnt(0)
	v_lshlrev_b32_e32 v6, 16, v6
	v_mul_f32_e32 v6, v4, v6
	v_fmac_f32_e32 v6, v38, v5
	v_cvt_pk_bf16_f32 v6, v6, v3
	ds_write_b16 v2, v6
	ds_read_u16 v6, v2 offset:64
	s_waitcnt lgkmcnt(0)
	v_lshlrev_b32_e32 v6, 16, v6
	v_mul_f32_e32 v4, v4, v6
	v_fmac_f32_e32 v4, v22, v5
	v_cvt_pk_bf16_f32 v4, v4, v3
	ds_write_b16 v2, v4 offset:64
	v_add_u32_e32 v2, v1, v145
	ds_read2_b32 v[4:5], v19 offset0:3 offset1:35
	ds_read_u16 v6, v2
	s_waitcnt lgkmcnt(0)
	v_lshlrev_b32_e32 v6, 16, v6
	v_mul_f32_e32 v6, v4, v6
	v_fmac_f32_e32 v6, v39, v5
	v_cvt_pk_bf16_f32 v6, v6, v3
	ds_write_b16 v2, v6
	ds_read_u16 v6, v2 offset:64
	s_waitcnt lgkmcnt(0)
	v_lshlrev_b32_e32 v6, 16, v6
	v_mul_f32_e32 v4, v4, v6
	v_fmac_f32_e32 v4, v23, v5
	v_cvt_pk_bf16_f32 v4, v4, v3
	ds_write_b16 v2, v4 offset:64
	v_add_u32_e32 v2, v1, v142
	ds_read2_b32 v[4:5], v19 offset0:8 offset1:40
	ds_read_u16 v6, v2
	s_waitcnt lgkmcnt(0)
	v_lshlrev_b32_e32 v6, 16, v6
	v_mul_f32_e32 v6, v4, v6
	v_fmac_f32_e32 v6, v40, v5
	v_cvt_pk_bf16_f32 v6, v6, v3
	ds_write_b16 v2, v6
	ds_read_u16 v6, v2 offset:64
	s_waitcnt lgkmcnt(0)
	v_lshlrev_b32_e32 v6, 16, v6
	v_mul_f32_e32 v4, v4, v6
	v_fmac_f32_e32 v4, v24, v5
	v_cvt_pk_bf16_f32 v4, v4, v3
	ds_write_b16 v2, v4 offset:64
	v_add_u32_e32 v2, v1, v141
	ds_read2_b32 v[4:5], v19 offset0:9 offset1:41
	ds_read_u16 v6, v2
	s_waitcnt lgkmcnt(0)
	v_lshlrev_b32_e32 v6, 16, v6
	v_mul_f32_e32 v6, v4, v6
	v_fmac_f32_e32 v6, v41, v5
	v_cvt_pk_bf16_f32 v6, v6, v3
	ds_write_b16 v2, v6
	ds_read_u16 v6, v2 offset:64
	s_waitcnt lgkmcnt(0)
	v_lshlrev_b32_e32 v6, 16, v6
	v_mul_f32_e32 v4, v4, v6
	v_fmac_f32_e32 v4, v25, v5
	v_cvt_pk_bf16_f32 v4, v4, v3
	ds_write_b16 v2, v4 offset:64
	v_add_u32_e32 v2, v1, v140
	ds_read2_b32 v[4:5], v19 offset0:10 offset1:42
	ds_read_u16 v6, v2
	s_waitcnt lgkmcnt(0)
	v_lshlrev_b32_e32 v6, 16, v6
	v_mul_f32_e32 v6, v4, v6
	v_fmac_f32_e32 v6, v42, v5
	v_cvt_pk_bf16_f32 v6, v6, v3
	ds_write_b16 v2, v6
	ds_read_u16 v6, v2 offset:64
	s_waitcnt lgkmcnt(0)
	v_lshlrev_b32_e32 v6, 16, v6
	v_mul_f32_e32 v4, v4, v6
	v_fmac_f32_e32 v4, v26, v5
	v_cvt_pk_bf16_f32 v4, v4, v3
	ds_write_b16 v2, v4 offset:64
	v_add_u32_e32 v2, v1, v138
	ds_read2_b32 v[4:5], v19 offset0:11 offset1:43
	ds_read_u16 v6, v2
	s_waitcnt lgkmcnt(0)
	v_lshlrev_b32_e32 v6, 16, v6
	v_mul_f32_e32 v6, v4, v6
	v_fmac_f32_e32 v6, v43, v5
	v_cvt_pk_bf16_f32 v6, v6, v3
	ds_write_b16 v2, v6
	ds_read_u16 v6, v2 offset:64
	s_waitcnt lgkmcnt(0)
	v_lshlrev_b32_e32 v6, 16, v6
	v_mul_f32_e32 v4, v4, v6
	v_fmac_f32_e32 v4, v27, v5
	v_cvt_pk_bf16_f32 v4, v4, v3
	ds_write_b16 v2, v4 offset:64
	v_add_u32_e32 v2, v1, v136
	ds_read2_b32 v[4:5], v19 offset0:16 offset1:48
	ds_read_u16 v6, v2
	s_waitcnt lgkmcnt(0)
	v_lshlrev_b32_e32 v6, 16, v6
	v_mul_f32_e32 v6, v4, v6
	v_fmac_f32_e32 v6, v44, v5
	v_cvt_pk_bf16_f32 v6, v6, v3
	ds_write_b16 v2, v6
	ds_read_u16 v6, v2 offset:64
	s_waitcnt lgkmcnt(0)
	v_lshlrev_b32_e32 v6, 16, v6
	v_mul_f32_e32 v4, v4, v6
	v_fmac_f32_e32 v4, v28, v5
	v_cvt_pk_bf16_f32 v4, v4, v3
	ds_write_b16 v2, v4 offset:64
	v_add_u32_e32 v2, v1, v135
	ds_read2_b32 v[4:5], v19 offset0:17 offset1:49
	ds_read_u16 v6, v2
	s_waitcnt lgkmcnt(0)
	v_lshlrev_b32_e32 v6, 16, v6
	v_mul_f32_e32 v6, v4, v6
	v_fmac_f32_e32 v6, v45, v5
	v_cvt_pk_bf16_f32 v6, v6, v3
	ds_write_b16 v2, v6
	ds_read_u16 v6, v2 offset:64
	s_waitcnt lgkmcnt(0)
	v_lshlrev_b32_e32 v6, 16, v6
	v_mul_f32_e32 v4, v4, v6
	v_fmac_f32_e32 v4, v29, v5
	v_cvt_pk_bf16_f32 v4, v4, v3
	ds_write_b16 v2, v4 offset:64
	v_add_u32_e32 v2, v1, v134
	ds_read2_b32 v[4:5], v19 offset0:18 offset1:50
	ds_read_u16 v6, v2
	s_waitcnt lgkmcnt(0)
	v_lshlrev_b32_e32 v6, 16, v6
	v_mul_f32_e32 v6, v4, v6
	v_fmac_f32_e32 v6, v46, v5
	v_cvt_pk_bf16_f32 v6, v6, v3
	ds_write_b16 v2, v6
	ds_read_u16 v6, v2 offset:64
	s_waitcnt lgkmcnt(0)
	v_lshlrev_b32_e32 v6, 16, v6
	v_mul_f32_e32 v4, v4, v6
	v_fmac_f32_e32 v4, v30, v5
	v_cvt_pk_bf16_f32 v4, v4, v3
	ds_write_b16 v2, v4 offset:64
	v_add_u32_e32 v2, v1, v133
	ds_read2_b32 v[4:5], v19 offset0:19 offset1:51
	ds_read_u16 v6, v2
	s_waitcnt lgkmcnt(0)
	v_lshlrev_b32_e32 v6, 16, v6
	v_mul_f32_e32 v6, v4, v6
	v_fmac_f32_e32 v6, v47, v5
	v_cvt_pk_bf16_f32 v6, v6, v3
	ds_write_b16 v2, v6
	ds_read_u16 v6, v2 offset:64
	s_waitcnt lgkmcnt(0)
	v_lshlrev_b32_e32 v6, 16, v6
	v_mul_f32_e32 v4, v4, v6
	v_fmac_f32_e32 v4, v31, v5
	v_cvt_pk_bf16_f32 v4, v4, v3
	ds_write_b16 v2, v4 offset:64
	v_add_u32_e32 v2, v1, v132
	ds_read2_b32 v[4:5], v19 offset0:24 offset1:56
	ds_read_u16 v6, v2
	s_waitcnt lgkmcnt(0)
	v_lshlrev_b32_e32 v6, 16, v6
	v_mul_f32_e32 v6, v4, v6
	v_fmac_f32_e32 v6, v48, v5
	v_cvt_pk_bf16_f32 v6, v6, v3
	ds_write_b16 v2, v6
	ds_read_u16 v6, v2 offset:64
	s_waitcnt lgkmcnt(0)
	v_lshlrev_b32_e32 v6, 16, v6
	v_mul_f32_e32 v4, v4, v6
	v_fmac_f32_e32 v4, v32, v5
	v_cvt_pk_bf16_f32 v4, v4, v3
	ds_write_b16 v2, v4 offset:64
	v_add_u32_e32 v2, v1, v131
	ds_read2_b32 v[4:5], v19 offset0:25 offset1:57
	ds_read_u16 v6, v2
	s_waitcnt lgkmcnt(0)
	v_lshlrev_b32_e32 v6, 16, v6
	v_mul_f32_e32 v6, v4, v6
	v_fmac_f32_e32 v6, v49, v5
	v_cvt_pk_bf16_f32 v6, v6, v3
	ds_write_b16 v2, v6
	ds_read_u16 v6, v2 offset:64
	s_waitcnt lgkmcnt(0)
	v_lshlrev_b32_e32 v6, 16, v6
	v_mul_f32_e32 v4, v4, v6
	v_fmac_f32_e32 v4, v33, v5
	v_cvt_pk_bf16_f32 v4, v4, v3
	ds_write_b16 v2, v4 offset:64
	v_add_u32_e32 v2, v1, v130
	ds_read2_b32 v[4:5], v19 offset0:26 offset1:58
	ds_read_u16 v6, v2
	v_add_u32_e32 v1, v1, v125
	s_waitcnt lgkmcnt(0)
	v_lshlrev_b32_e32 v6, 16, v6
	v_mul_f32_e32 v6, v4, v6
	v_fmac_f32_e32 v6, v50, v5
	v_cvt_pk_bf16_f32 v6, v6, v3
	ds_write_b16 v2, v6
	ds_read_u16 v6, v2 offset:64
	s_waitcnt lgkmcnt(0)
	v_lshlrev_b32_e32 v6, 16, v6
	v_mul_f32_e32 v4, v4, v6
	v_fmac_f32_e32 v4, v34, v5
	v_cvt_pk_bf16_f32 v4, v4, v3
	ds_write_b16 v2, v4 offset:64
	ds_read2_b32 v[4:5], v19 offset0:27 offset1:59
	ds_read_u16 v2, v1
	s_waitcnt lgkmcnt(0)
	v_lshlrev_b32_e32 v2, 16, v2
	v_mul_f32_e32 v2, v4, v2
	v_fmac_f32_e32 v2, v51, v5
	v_cvt_pk_bf16_f32 v2, v2, v3
	ds_write_b16 v1, v2
	ds_read_u16 v2, v1 offset:64
	s_waitcnt lgkmcnt(0)
	v_lshlrev_b32_e32 v2, 16, v2
	v_mul_f32_e32 v2, v4, v2
	v_fmac_f32_e32 v2, v35, v5
	v_cvt_pk_bf16_f32 v2, v2, v3
	ds_write_b16 v1, v2 offset:64
	v_add_u32_e32 v1, s10, v146
	v_mad_i64_i32 v[12:13], s[0:1], v1, s96, v[116:117]
	v_add_u32_e32 v1, s11, v118
	v_med3_i32 v1, v1, 0, v227
	v_mul_u32_u24_e32 v2, 0xa00, v1
	s_waitcnt lgkmcnt(0)
	v_lshl_add_u64 v[24:25], v[2:3], 1, v[116:117]
	global_load_dwordx4 v[68:71], v[12:13], off offset:2048
	global_load_dwordx4 v[4:7], v[12:13], off offset:2080
	global_load_dwordx4 v[8:11], v[12:13], off offset:2112
	s_nop 0
	global_load_dwordx4 v[12:15], v[12:13], off offset:2144
	s_nop 0
	global_load_dwordx4 v[20:23], v[24:25], off offset:3072
	global_load_dwordx4 v[36:39], v[24:25], off offset:3104
	global_load_dwordx4 v[40:43], v[24:25], off offset:3136
	global_load_dwordx4 v[44:47], v[24:25], off offset:3168
	v_add_u32_e32 v1, s11, v119
	v_med3_i32 v1, v1, 0, v227
	v_mul_u32_u24_e32 v2, 0xa00, v1
	v_add_u32_e32 v1, s11, v121
	v_med3_i32 v1, v1, 0, v227
	v_lshl_add_u64 v[24:25], v[2:3], 1, s[20:21]
	v_mul_u32_u24_e32 v2, 0xa00, v1
	v_add_u32_e32 v1, s11, v123
	v_lshl_add_u64 v[24:25], v[24:25], 0, v[16:17]
	v_med3_i32 v1, v1, 0, v227
	global_load_lds_dwordx4 v[24:25], off
	v_lshl_add_u64 v[24:25], v[2:3], 1, s[20:21]
	v_mul_u32_u24_e32 v2, 0xa00, v1
	v_add_u32_e32 v1, s11, v124
	v_lshl_add_u64 v[24:25], v[24:25], 0, v[16:17]
	s_mov_b32 m0, s30
	v_med3_i32 v1, v1, 0, v227
	global_load_lds_dwordx4 v[24:25], off
	v_lshl_add_u64 v[24:25], v[2:3], 1, s[20:21]
	v_mul_u32_u24_e32 v2, 0xa00, v1
	v_add_u32_e32 v1, s11, v137
	v_lshl_add_u64 v[24:25], v[24:25], 0, v[16:17]
	s_mov_b32 m0, s28
	v_med3_i32 v1, v1, 0, v227
	s_add_i32 s0, s12, 0xfffffa00
	global_load_lds_dwordx4 v[24:25], off
	v_lshl_add_u64 v[24:25], v[2:3], 1, s[20:21]
	v_mul_u32_u24_e32 v2, 0xa00, v1
	v_add_u32_e32 v1, s0, v119
	v_lshl_add_u64 v[24:25], v[24:25], 0, v[16:17]
	s_mov_b32 m0, s29
	v_med3_i32 v1, v1, 0, v227
	global_load_lds_dwordx4 v[24:25], off
	v_lshl_add_u64 v[24:25], v[2:3], 1, v[116:117]
	v_mul_u32_u24_e32 v2, 0xa00, v1
	v_add_u32_e32 v1, s0, v121
	global_load_dwordx4 v[52:55], v[24:25], off offset:3072
	global_load_dwordx4 v[80:83], v[24:25], off offset:3104
	global_load_dwordx4 v[76:79], v[24:25], off offset:3136
	global_load_dwordx4 v[72:75], v[24:25], off offset:3168
	v_lshl_add_u64 v[24:25], v[2:3], 1, s[20:21]
	v_med3_i32 v1, v1, 0, v227
	v_lshl_add_u64 v[24:25], v[24:25], 0, v[16:17]
	s_mov_b32 m0, s36
	v_mul_u32_u24_e32 v2, 0xa00, v1
	v_add_u32_e32 v1, s0, v123
	global_load_lds_dwordx4 v[24:25], off
	v_lshl_add_u64 v[24:25], v[2:3], 1, s[20:21]
	v_med3_i32 v1, v1, 0, v227
	v_lshl_add_u64 v[24:25], v[24:25], 0, v[16:17]
	s_mov_b32 m0, s34
	v_mul_u32_u24_e32 v2, 0xa00, v1
	v_add_u32_e32 v1, s0, v124
	global_load_lds_dwordx4 v[24:25], off
	v_lshl_add_u64 v[24:25], v[2:3], 1, s[20:21]
	v_med3_i32 v1, v1, 0, v227
	v_lshl_add_u64 v[24:25], v[24:25], 0, v[16:17]
	s_mov_b32 m0, s31
	v_mul_u32_u24_e32 v2, 0xa00, v1
	global_load_lds_dwordx4 v[24:25], off
	v_lshl_add_u64 v[24:25], v[2:3], 1, s[20:21]
	v_lshl_add_u64 v[24:25], v[24:25], 0, v[16:17]
	s_mov_b32 m0, s35
	v_add_u32_e32 v1, s11, v120
	global_load_lds_dwordx4 v[24:25], off
	s_waitcnt vmcnt(0)
	v_mfma_f32_32x32x16_bf16 v[20:35], v[20:23], v[68:71], 0
	v_readlane_b32 s0, v255, 22
	v_cmp_lt_i32_e32 vcc, -1, v1
	v_readlane_b32 s1, v255, 23
	s_and_b64 vcc, s[0:1], vcc
	v_readlane_b32 s0, v255, 24
	v_readlane_b32 s1, v255, 25
	s_waitcnt vmcnt(8)
	v_mfma_f32_32x32x16_bf16 v[20:35], v[36:39], v[4:7], v[20:35]
	ds_read_b64_tr_b16 v[84:85], v181 offset:0
	ds_read_b64_tr_b16 v[86:87], v181 offset:0x400
	ds_read_b64_tr_b16 v[64:65], v181 offset:0x800
	ds_read_b64_tr_b16 v[66:67], v181 offset:0xc00
	ds_read_b64_tr_b16 v[60:61], v181 offset:0x200
	ds_read_b64_tr_b16 v[62:63], v181 offset:0x600
	ds_read_b64_tr_b16 v[56:57], v181 offset:0xa00
	v_mfma_f32_32x32x16_bf16 v[20:35], v[40:43], v[8:11], v[20:35]
	ds_read_b64_tr_b16 v[58:59], v181 offset:0xe00
	v_mfma_f32_32x32x16_bf16 v[20:35], v[44:47], v[12:15], v[20:35]
	s_nop 11
	v_cndmask_b32_e32 v2, v18, v20, vcc
	v_cmp_lt_i32_e32 vcc, s90, v1
	s_and_b64 vcc, s[0:1], vcc
	v_readlane_b32 s0, v255, 26
	v_cndmask_b32_e32 v17, v18, v21, vcc
	v_cmp_lt_i32_e32 vcc, s13, v1
	v_readlane_b32 s1, v255, 27
	s_and_b64 vcc, s[0:1], vcc
	v_readlane_b32 s0, v255, 28
	v_cndmask_b32_e32 v20, v18, v22, vcc
	v_cmp_lt_i32_e32 vcc, s43, v1
	v_readlane_b32 s1, v255, 29
	s_and_b64 vcc, s[0:1], vcc
	v_readlane_b32 s0, v255, 30
	v_cndmask_b32_e32 v21, v18, v23, vcc
	v_cmp_lt_i32_e32 vcc, s76, v1
	v_readlane_b32 s1, v255, 31
	s_and_b64 vcc, s[0:1], vcc
	v_readlane_b32 s0, v255, 32
	v_cndmask_b32_e32 v22, v18, v24, vcc
	v_cmp_lt_i32_e32 vcc, s77, v1
	v_readlane_b32 s1, v255, 33
	s_and_b64 vcc, s[0:1], vcc
	v_readlane_b32 s0, v255, 34
	v_cndmask_b32_e32 v23, v18, v25, vcc
	v_cmp_lt_i32_e32 vcc, s78, v1
	v_readlane_b32 s1, v255, 35
	s_and_b64 vcc, s[0:1], vcc
	v_readlane_b32 s0, v255, 36
	v_cndmask_b32_e32 v24, v18, v26, vcc
	v_cmp_lt_i32_e32 vcc, s79, v1
	v_readlane_b32 s1, v255, 37
	s_and_b64 vcc, s[0:1], vcc
	v_readlane_b32 s0, v255, 38
	v_cndmask_b32_e32 v25, v18, v27, vcc
	v_cmp_lt_i32_e32 vcc, s80, v1
	v_readlane_b32 s1, v255, 39
	s_and_b64 vcc, s[0:1], vcc
	v_readlane_b32 s0, v255, 40
	v_cndmask_b32_e32 v26, v18, v28, vcc
	v_cmp_lt_i32_e32 vcc, s81, v1
	v_readlane_b32 s1, v255, 41
	s_and_b64 vcc, s[0:1], vcc
	v_readlane_b32 s0, v255, 42
	v_cndmask_b32_e32 v27, v18, v29, vcc
	v_cmp_lt_i32_e32 vcc, s82, v1
	v_readlane_b32 s1, v255, 43
	s_and_b64 vcc, s[0:1], vcc
	v_readlane_b32 s0, v255, 44
	v_cndmask_b32_e32 v28, v18, v30, vcc
	v_cmp_lt_i32_e32 vcc, s83, v1
	v_readlane_b32 s1, v255, 45
	s_and_b64 vcc, s[0:1], vcc
	v_readlane_b32 s0, v255, 46
	v_cndmask_b32_e32 v29, v18, v31, vcc
	v_cmp_lt_i32_e32 vcc, s84, v1
	v_readlane_b32 s1, v255, 47
	s_and_b64 vcc, s[0:1], vcc
	v_readlane_b32 s0, v255, 48
	v_cndmask_b32_e32 v30, v18, v32, vcc
	v_cmp_lt_i32_e32 vcc, s85, v1
	v_readlane_b32 s1, v255, 49
	s_and_b64 vcc, s[0:1], vcc
	v_readlane_b32 s0, v255, 50
	v_cndmask_b32_e32 v31, v18, v33, vcc
	v_cmp_lt_i32_e32 vcc, s86, v1
	v_readlane_b32 s1, v255, 51
	s_and_b64 vcc, s[0:1], vcc
	v_cndmask_b32_e32 v32, v18, v34, vcc
	v_max_f32_e32 v33, v17, v17
	v_max_f32_e32 v34, v2, v2
	v_max_f32_e32 v33, v34, v33
	v_max3_f32 v33, v33, v20, v21
	v_max3_f32 v33, v33, v22, v23
	v_readlane_b32 s0, v255, 52
	v_max3_f32 v33, v33, v24, v25
	v_cmp_lt_i32_e32 vcc, s87, v1
	v_readlane_b32 s1, v255, 53
	v_max3_f32 v33, v33, v26, v27
	s_and_b64 vcc, s[0:1], vcc
	v_max3_f32 v33, v33, v28, v29
	v_cndmask_b32_e32 v1, v18, v35, vcc
	v_max3_f32 v33, v33, v30, v31
	v_max3_f32 v33, v33, v32, v1
	v_mov_b32_e32 v34, v33
	s_nop 1
	v_permlane32_swap_b32_e32 v33, v34
	s_mov_b32 s0, 0xf149f2ca
	v_max3_f32 v150, v33, v34, s0
	v_sub_f32_e32 v2, v2, v150
	v_exp_f32_e32 v2, v2
	v_sub_f32_e32 v17, v17, v150
	v_exp_f32_e32 v17, v17
	v_sub_f32_e32 v20, v20, v150
	v_exp_f32_e32 v20, v20
	v_sub_f32_e32 v21, v21, v150
	v_exp_f32_e32 v21, v21
	v_sub_f32_e32 v22, v22, v150
	v_add_f32_e32 v34, 0, v2
	v_exp_f32_e32 v22, v22
	v_sub_f32_e32 v23, v23, v150
	v_add_f32_e32 v34, v17, v34
	v_exp_f32_e32 v23, v23
	v_sub_f32_e32 v24, v24, v150
	v_add_f32_e32 v34, v20, v34
	v_exp_f32_e32 v24, v24
	v_sub_f32_e32 v25, v25, v150
	v_add_f32_e32 v34, v21, v34
	v_exp_f32_e32 v25, v25
	v_sub_f32_e32 v26, v26, v150
	v_add_f32_e32 v34, v22, v34
	v_exp_f32_e32 v26, v26
	v_sub_f32_e32 v27, v27, v150
	v_add_f32_e32 v34, v23, v34
	v_exp_f32_e32 v27, v27
	v_sub_f32_e32 v28, v28, v150
	v_add_f32_e32 v34, v24, v34
	v_exp_f32_e32 v28, v28
	v_sub_f32_e32 v29, v29, v150
	v_add_f32_e32 v34, v25, v34
	v_exp_f32_e32 v29, v29
	v_sub_f32_e32 v30, v30, v150
	v_add_f32_e32 v34, v26, v34
	v_exp_f32_e32 v30, v30
	v_sub_f32_e32 v31, v31, v150
	v_add_f32_e32 v34, v27, v34
	v_exp_f32_e32 v31, v31
	v_sub_f32_e32 v32, v32, v150
	v_add_f32_e32 v34, v28, v34
	v_exp_f32_e32 v32, v32
	v_sub_f32_e32 v1, v1, v150
	v_add_f32_e32 v34, v29, v34
	v_exp_f32_e32 v1, v1
	v_sub_f32_e32 v33, 0xf149f2ca, v150
	v_add_f32_e32 v34, v30, v34
	v_add_f32_e32 v34, v31, v34
	v_exp_f32_e32 v120, v33
	v_add_f32_e32 v34, v32, v34
	v_add_f32_e32 v137, v1, v34
	v_mov_b32_e32 v146, v137
	v_cvt_pk_bf16_f32 v104, v2, v17
	v_cvt_pk_bf16_f32 v105, v20, v21
	v_cvt_pk_bf16_f32 v106, v22, v23
	v_cvt_pk_bf16_f32 v107, v24, v25
	v_cvt_pk_bf16_f32 v100, v26, v27
	v_cvt_pk_bf16_f32 v101, v28, v29
	v_cvt_pk_bf16_f32 v102, v30, v31
	v_cvt_pk_bf16_f32 v103, v32, v1
	s_nop 1
	v_permlane32_swap_b32_e32 v137, v146
	v_permlane32_swap_b32_e32 v104, v106
	v_permlane32_swap_b32_e32 v105, v107
	v_permlane32_swap_b32_e32 v100, v102
	v_permlane32_swap_b32_e32 v101, v103
	v_cmp_gt_f32_e32 vcc, 1.0, v120
	s_cbranch_vccz .LBB0_1376
	s_and_saveexec_b64 s[0:1], s[6:7]
	ds_write_b32 v185, v120
	s_or_b64 exec, exec, s[0:1]
	ds_read_b128 v[20:23], v19 offset:96
	ds_read_b128 v[24:27], v19 offset:64
	ds_read_b128 v[36:39], v19 offset:32
	ds_read_b128 v[40:43], v19
	s_waitcnt lgkmcnt(0)
	v_pk_mul_f32 v[34:35], v[22:23], 0 op_sel_hi:[1,0]
	v_pk_mul_f32 v[30:31], v[26:27], 0 op_sel_hi:[1,0]
	v_pk_mul_f32 v[26:27], v[38:39], 0 op_sel_hi:[1,0]
	v_pk_mul_f32 v[22:23], v[42:43], 0 op_sel_hi:[1,0]
	v_pk_mul_f32 v[32:33], v[20:21], 0 op_sel_hi:[1,0]
	v_pk_mul_f32 v[28:29], v[24:25], 0 op_sel_hi:[1,0]
	v_pk_mul_f32 v[24:25], v[36:37], 0 op_sel_hi:[1,0]
	v_pk_mul_f32 v[20:21], v[40:41], 0 op_sel_hi:[1,0]
	s_branch .LBB0_1377

.LBB0_1379:
	s_nop 10
	v_max_f32_e32 v1, v53, v53
	v_max_f32_e32 v2, v52, v52
	v_max_f32_e32 v1, v2, v1
	v_max3_f32 v1, v1, v54, v55
	v_max3_f32 v1, v1, v56, v57
	v_max3_f32 v1, v1, v58, v59
	v_max3_f32 v1, v1, v60, v61
	v_max3_f32 v1, v1, v62, v63
	v_max3_f32 v1, v1, v64, v65
	v_max3_f32 v1, v1, v66, v67
	v_mov_b32_e32 v2, v1
	s_nop 1
	v_permlane32_swap_b32_e32 v1, v2
	v_max3_f32 v151, v150, v1, v2
	v_sub_f32_e32 v2, v52, v151
	v_exp_f32_e32 v2, v2
	v_sub_f32_e32 v17, v53, v151
	v_exp_f32_e32 v17, v17
	v_sub_f32_e32 v52, v54, v151
	v_exp_f32_e32 v52, v52
	v_sub_f32_e32 v53, v55, v151
	v_exp_f32_e32 v53, v53
	v_sub_f32_e32 v55, v56, v151
	v_add_f32_e32 v54, 0, v2
	v_exp_f32_e32 v55, v55
	v_sub_f32_e32 v56, v57, v151
	v_add_f32_e32 v54, v17, v54
	v_exp_f32_e32 v72, v56
	v_sub_f32_e32 v56, v58, v151
	v_add_f32_e32 v54, v52, v54
	v_exp_f32_e32 v73, v56
	v_sub_f32_e32 v56, v59, v151
	v_add_f32_e32 v54, v53, v54
	v_exp_f32_e32 v59, v56
	v_sub_f32_e32 v56, v60, v151
	v_add_f32_e32 v54, v55, v54
	v_exp_f32_e32 v60, v56
	v_sub_f32_e32 v56, v61, v151
	v_add_f32_e32 v54, v72, v54
	v_exp_f32_e32 v61, v56
	v_sub_f32_e32 v56, v62, v151
	v_add_f32_e32 v54, v73, v54
	v_exp_f32_e32 v62, v56
	v_sub_f32_e32 v56, v63, v151
	v_add_f32_e32 v54, v59, v54
	v_exp_f32_e32 v63, v56
	v_sub_f32_e32 v56, v64, v151
	v_add_f32_e32 v54, v60, v54
	v_exp_f32_e32 v64, v56
	v_sub_f32_e32 v56, v65, v151
	v_add_f32_e32 v54, v61, v54
	v_exp_f32_e32 v65, v56
	v_sub_f32_e32 v56, v66, v151
	v_add_f32_e32 v54, v62, v54
	v_exp_f32_e32 v66, v56
	v_sub_f32_e32 v56, v67, v151
	v_add_f32_e32 v54, v63, v54
	v_exp_f32_e32 v67, v56
	v_sub_f32_e32 v1, v150, v151
	v_add_f32_e32 v54, v64, v54
	v_add_f32_e32 v54, v65, v54
	v_exp_f32_e32 v126, v1
	v_add_f32_e32 v54, v66, v54
	v_add_f32_e32 v139, v67, v54
	v_mov_b32_e32 v150, v139
	v_cvt_pk_bf16_f32 v56, v2, v17
	v_cvt_pk_bf16_f32 v57, v52, v53
	v_cvt_pk_bf16_f32 v58, v55, v72
	v_cvt_pk_bf16_f32 v59, v73, v59
	v_cvt_pk_bf16_f32 v52, v60, v61
	v_cvt_pk_bf16_f32 v53, v62, v63
	v_cvt_pk_bf16_f32 v54, v64, v65
	v_cvt_pk_bf16_f32 v55, v66, v67
	s_nop 1
	v_permlane32_swap_b32_e32 v139, v150
	v_permlane32_swap_b32_e32 v56, v58
	v_permlane32_swap_b32_e32 v57, v59
	v_permlane32_swap_b32_e32 v52, v54
	v_permlane32_swap_b32_e32 v53, v55
	v_cmp_gt_f32_e32 vcc, 1.0, v126
	s_cbranch_vccz .LBB0_1383
	s_and_saveexec_b64 s[4:5], s[6:7]
	ds_write_b32 v185, v126
	s_or_b64 exec, exec, s[4:5]
	ds_read_b128 v[60:63], v19 offset:96
	ds_read_b128 v[64:67], v19 offset:64
	ds_read_b128 v[72:75], v19 offset:32
	ds_read_b128 v[76:79], v19
	s_waitcnt lgkmcnt(0)
	v_pk_mul_f32 v[50:51], v[50:51], v[62:63]
	v_pk_mul_f32 v[46:47], v[46:47], v[66:67]
	v_pk_mul_f32 v[42:43], v[42:43], v[74:75]
	v_pk_mul_f32 v[38:39], v[38:39], v[78:79]
	v_pk_mul_f32 v[48:49], v[48:49], v[60:61]
	v_pk_mul_f32 v[44:45], v[44:45], v[64:65]
	v_pk_mul_f32 v[40:41], v[40:41], v[72:73]
	v_pk_mul_f32 v[36:37], v[36:37], v[76:77]
	v_pk_mul_f32 v[34:35], v[34:35], v[62:63]
	v_pk_mul_f32 v[30:31], v[30:31], v[66:67]
	v_pk_mul_f32 v[26:27], v[26:27], v[74:75]
	v_pk_mul_f32 v[22:23], v[22:23], v[78:79]
	v_pk_mul_f32 v[32:33], v[32:33], v[60:61]
	v_pk_mul_f32 v[28:29], v[28:29], v[64:65]
	v_pk_mul_f32 v[24:25], v[24:25], v[72:73]
	v_pk_mul_f32 v[20:21], v[20:21], v[76:77]

.LBB0_1385:
	s_nop 10
	v_max_f32_e32 v1, v53, v53
	v_max_f32_e32 v2, v52, v52
	v_max_f32_e32 v1, v2, v1
	v_max3_f32 v1, v1, v54, v55
	v_max3_f32 v1, v1, v56, v57
	v_max3_f32 v1, v1, v58, v59
	v_max3_f32 v1, v1, v60, v61
	v_max3_f32 v1, v1, v62, v63
	v_max3_f32 v1, v1, v64, v65
	v_max3_f32 v1, v1, v66, v67
	v_mov_b32_e32 v2, v1
	s_nop 1
	v_permlane32_swap_b32_e32 v1, v2
	v_max3_f32 v152, v151, v1, v2
	v_sub_f32_e32 v2, v52, v152
	v_exp_f32_e32 v2, v2
	v_sub_f32_e32 v17, v53, v152
	v_exp_f32_e32 v17, v17
	v_sub_f32_e32 v52, v54, v152
	v_exp_f32_e32 v52, v52
	v_sub_f32_e32 v53, v55, v152
	v_exp_f32_e32 v53, v53
	v_sub_f32_e32 v55, v56, v152
	v_add_f32_e32 v54, 0, v2
	v_exp_f32_e32 v55, v55
	v_sub_f32_e32 v56, v57, v152
	v_add_f32_e32 v54, v17, v54
	v_exp_f32_e32 v84, v56
	v_sub_f32_e32 v56, v58, v152
	v_add_f32_e32 v54, v52, v54
	v_exp_f32_e32 v85, v56
	v_sub_f32_e32 v56, v59, v152
	v_add_f32_e32 v54, v53, v54
	v_exp_f32_e32 v59, v56
	v_sub_f32_e32 v56, v60, v152
	v_add_f32_e32 v54, v55, v54
	v_exp_f32_e32 v60, v56
	v_sub_f32_e32 v56, v61, v152
	v_add_f32_e32 v54, v84, v54
	v_exp_f32_e32 v61, v56
	v_sub_f32_e32 v56, v62, v152
	v_add_f32_e32 v54, v85, v54
	v_exp_f32_e32 v62, v56
	v_sub_f32_e32 v56, v63, v152
	v_add_f32_e32 v54, v59, v54
	v_exp_f32_e32 v63, v56
	v_sub_f32_e32 v56, v64, v152
	v_add_f32_e32 v54, v60, v54
	v_exp_f32_e32 v64, v56
	v_sub_f32_e32 v56, v65, v152
	v_add_f32_e32 v54, v61, v54
	v_exp_f32_e32 v65, v56
	v_sub_f32_e32 v56, v66, v152
	v_add_f32_e32 v54, v62, v54
	v_exp_f32_e32 v66, v56
	v_sub_f32_e32 v56, v67, v152
	v_add_f32_e32 v54, v63, v54
	v_exp_f32_e32 v67, v56
	v_sub_f32_e32 v1, v151, v152
	v_add_f32_e32 v54, v64, v54
	v_add_f32_e32 v54, v65, v54
	v_exp_f32_e32 v128, v1
	v_add_f32_e32 v54, v66, v54
	v_add_f32_e32 v143, v67, v54
	v_mov_b32_e32 v151, v143
	v_cvt_pk_bf16_f32 v56, v2, v17
	v_cvt_pk_bf16_f32 v57, v52, v53
	v_cvt_pk_bf16_f32 v58, v55, v84
	v_cvt_pk_bf16_f32 v59, v85, v59
	v_cvt_pk_bf16_f32 v52, v60, v61
	v_cvt_pk_bf16_f32 v53, v62, v63
	v_cvt_pk_bf16_f32 v54, v64, v65
	v_cvt_pk_bf16_f32 v55, v66, v67
	s_nop 1
	v_permlane32_swap_b32_e32 v143, v151
	v_permlane32_swap_b32_e32 v56, v58
	v_permlane32_swap_b32_e32 v57, v59
	v_permlane32_swap_b32_e32 v52, v54
	v_permlane32_swap_b32_e32 v53, v55
	v_cmp_gt_f32_e32 vcc, 1.0, v128
	s_cbranch_vccz .LBB0_1389
	s_and_saveexec_b64 s[0:1], s[6:7]
	ds_write_b32 v185, v128
	s_or_b64 exec, exec, s[0:1]
	ds_read_b128 v[60:63], v19 offset:96
	ds_read_b128 v[64:67], v19 offset:64
	ds_read_b128 v[84:87], v19 offset:32
	ds_read_b128 v[88:91], v19
	s_waitcnt lgkmcnt(0)
	v_pk_mul_f32 v[50:51], v[50:51], v[62:63]
	v_pk_mul_f32 v[46:47], v[46:47], v[66:67]
	v_pk_mul_f32 v[42:43], v[42:43], v[86:87]
	v_pk_mul_f32 v[38:39], v[38:39], v[90:91]
	v_pk_mul_f32 v[48:49], v[48:49], v[60:61]
	v_pk_mul_f32 v[44:45], v[44:45], v[64:65]
	v_pk_mul_f32 v[40:41], v[40:41], v[84:85]
	v_pk_mul_f32 v[36:37], v[36:37], v[88:89]
	v_pk_mul_f32 v[34:35], v[34:35], v[62:63]
	v_pk_mul_f32 v[30:31], v[30:31], v[66:67]
	v_pk_mul_f32 v[26:27], v[26:27], v[86:87]
	v_pk_mul_f32 v[22:23], v[22:23], v[90:91]
	v_pk_mul_f32 v[32:33], v[32:33], v[60:61]
	v_pk_mul_f32 v[28:29], v[28:29], v[64:65]
	v_pk_mul_f32 v[24:25], v[24:25], v[84:85]
	v_pk_mul_f32 v[20:21], v[20:21], v[88:89]

.LBB0_1391:
	s_nop 10
	v_max_f32_e32 v1, v53, v53
	v_max_f32_e32 v2, v52, v52
	v_max_f32_e32 v1, v2, v1
	v_max3_f32 v1, v1, v54, v55
	v_max3_f32 v1, v1, v56, v57
	v_max3_f32 v1, v1, v58, v59
	v_max3_f32 v1, v1, v60, v61
	v_max3_f32 v1, v1, v62, v63
	v_max3_f32 v1, v1, v64, v65
	v_max3_f32 v1, v1, v66, v67
	v_mov_b32_e32 v2, v1
	s_nop 1
	v_permlane32_swap_b32_e32 v1, v2
	v_max3_f32 v108, v152, v1, v2
	v_sub_f32_e32 v2, v52, v108
	v_exp_f32_e32 v52, v2
	v_sub_f32_e32 v2, v53, v108
	v_exp_f32_e32 v53, v2
	v_sub_f32_e32 v2, v54, v108
	v_exp_f32_e32 v54, v2
	v_sub_f32_e32 v2, v55, v108
	v_exp_f32_e32 v55, v2
	v_sub_f32_e32 v16, v56, v108
	v_add_f32_e32 v2, 0, v52
	v_exp_f32_e32 v56, v16
	v_sub_f32_e32 v16, v57, v108
	v_add_f32_e32 v2, v53, v2
	v_exp_f32_e32 v57, v16
	v_sub_f32_e32 v16, v58, v108
	v_add_f32_e32 v2, v54, v2
	v_exp_f32_e32 v58, v16
	v_sub_f32_e32 v16, v59, v108
	v_add_f32_e32 v2, v55, v2
	v_exp_f32_e32 v59, v16
	v_sub_f32_e32 v16, v60, v108
	v_add_f32_e32 v2, v56, v2
	v_exp_f32_e32 v60, v16
	v_sub_f32_e32 v16, v61, v108
	v_add_f32_e32 v2, v57, v2
	v_exp_f32_e32 v61, v16
	v_sub_f32_e32 v16, v62, v108
	v_add_f32_e32 v2, v58, v2
	v_exp_f32_e32 v62, v16
	v_sub_f32_e32 v16, v63, v108
	v_add_f32_e32 v2, v59, v2
	v_exp_f32_e32 v63, v16
	v_sub_f32_e32 v16, v64, v108
	v_add_f32_e32 v2, v60, v2
	v_exp_f32_e32 v64, v16
	v_sub_f32_e32 v16, v65, v108
	v_add_f32_e32 v2, v61, v2
	v_exp_f32_e32 v65, v16
	v_sub_f32_e32 v16, v66, v108
	v_add_f32_e32 v2, v62, v2
	v_exp_f32_e32 v66, v16
	v_sub_f32_e32 v16, v67, v108
	v_add_f32_e32 v2, v63, v2
	v_exp_f32_e32 v67, v16
	v_add_f32_e32 v2, v64, v2
	v_add_f32_e32 v2, v65, v2
	v_sub_f32_e32 v1, v152, v108
	v_add_f32_e32 v2, v66, v2
	v_add_f32_e32 v16, v67, v2
	v_exp_f32_e32 v2, v1
	v_readlane_b32 s28, v255, 17
	v_mov_b32_e32 v17, v16
	v_cvt_pk_bf16_f32 v52, v52, v53
	v_cvt_pk_bf16_f32 v53, v54, v55
	v_cvt_pk_bf16_f32 v54, v56, v57
	v_cvt_pk_bf16_f32 v55, v58, v59
	v_cvt_pk_bf16_f32 v56, v60, v61
	v_cvt_pk_bf16_f32 v57, v62, v63
	v_cvt_pk_bf16_f32 v58, v64, v65
	v_cvt_pk_bf16_f32 v59, v66, v67
	v_readlane_b32 s29, v255, 18
	s_nop 0
	v_permlane32_swap_b32_e32 v16, v17
	v_permlane32_swap_b32_e32 v52, v54
	v_permlane32_swap_b32_e32 v53, v55
	v_permlane32_swap_b32_e32 v56, v58
	v_permlane32_swap_b32_e32 v57, v59
	v_cmp_gt_f32_e32 vcc, 1.0, v2
	s_cbranch_vccz .LBB0_1395
	s_and_saveexec_b64 s[0:1], s[6:7]
	ds_write_b32 v185, v2
	s_or_b64 exec, exec, s[0:1]
	ds_read_b128 v[60:63], v19 offset:96
	ds_read_b128 v[64:67], v19 offset:64
	ds_read_b128 v[72:75], v19 offset:32
	ds_read_b128 v[110:113], v19
	s_waitcnt lgkmcnt(0)
	v_pk_mul_f32 v[50:51], v[50:51], v[62:63]
	v_pk_mul_f32 v[46:47], v[46:47], v[66:67]
	v_pk_mul_f32 v[42:43], v[42:43], v[74:75]
	v_pk_mul_f32 v[38:39], v[38:39], v[112:113]
	v_pk_mul_f32 v[48:49], v[48:49], v[60:61]
	v_pk_mul_f32 v[44:45], v[44:45], v[64:65]
	v_pk_mul_f32 v[40:41], v[40:41], v[72:73]
	v_pk_mul_f32 v[36:37], v[36:37], v[110:111]
	v_pk_mul_f32 v[34:35], v[34:35], v[62:63]
	v_pk_mul_f32 v[30:31], v[30:31], v[66:67]
	v_pk_mul_f32 v[26:27], v[26:27], v[74:75]
	v_pk_mul_f32 v[22:23], v[22:23], v[112:113]
	v_pk_mul_f32 v[32:33], v[32:33], v[60:61]
	v_pk_mul_f32 v[28:29], v[28:29], v[64:65]
	v_pk_mul_f32 v[24:25], v[24:25], v[72:73]
	v_pk_mul_f32 v[20:21], v[20:21], v[110:111]
.LBB0_1395:
	s_waitcnt lgkmcnt(0)
	v_mfma_f32_32x32x16_bf16 v[36:51], v[52:55], v[80:83], v[36:51]
	v_add_u32_e32 v1, s11, v127
	v_cmp_lt_i32_e32 vcc, -1, v1
	s_and_b64 vcc, s[14:15], vcc
	v_readlane_b32 s0, v255, 54
	v_readlane_b32 s1, v255, 55
	s_waitcnt vmcnt(0)
	v_mfma_f32_32x32x16_bf16 v[20:35], v[52:55], v[84:87], v[20:35]
	ds_read_b64_tr_b16 v[84:85], v181 offset:0
	ds_read_b64_tr_b16 v[86:87], v181 offset:0x400
	ds_read_b64_tr_b16 v[80:81], v181 offset:0x800
	ds_read_b64_tr_b16 v[82:83], v181 offset:0xc00
	v_mfma_f32_32x32x16_bf16 v[36:51], v[56:59], v[76:79], v[36:51]
	ds_read_b64_tr_b16 v[76:77], v181 offset:0x200
	ds_read_b64_tr_b16 v[78:79], v181 offset:0x600
	ds_read_b64_tr_b16 v[72:73], v181 offset:0xa00
	ds_read_b64_tr_b16 v[74:75], v181 offset:0xe00
	v_mfma_f32_32x32x16_bf16 v[20:35], v[56:59], v[100:103], v[20:35]
	s_waitcnt vmcnt(0)
	v_mfma_f32_32x32x16_bf16 v[52:67], v[104:107], v[68:71], 0
	v_mfma_f32_32x32x16_bf16 v[52:67], v[88:91], v[4:7], v[52:67]
	v_mfma_f32_32x32x16_bf16 v[52:67], v[92:95], v[8:11], v[52:67]
	v_mfma_f32_32x32x16_bf16 v[52:67], v[96:99], v[12:15], v[52:67]
	s_nop 11
	v_cndmask_b32_e32 v4, v18, v52, vcc
	v_cmp_lt_i32_e32 vcc, s90, v1
	s_and_b64 vcc, s[70:71], vcc
	s_nop 0
	v_cndmask_b32_e32 v5, v18, v53, vcc
	v_cmp_lt_i32_e32 vcc, s13, v1
	s_and_b64 vcc, s[16:17], vcc
	v_max_f32_e32 v12, v5, v5
	v_cndmask_b32_e32 v6, v18, v54, vcc
	v_cmp_lt_i32_e32 vcc, s43, v1
	s_and_b64 vcc, s[66:67], vcc
	s_nop 0
	v_cndmask_b32_e32 v7, v18, v55, vcc
	v_cmp_lt_i32_e32 vcc, s76, v1
	s_and_b64 vcc, s[64:65], vcc
	s_nop 0
	v_cndmask_b32_e32 v8, v18, v56, vcc
	v_cmp_lt_i32_e32 vcc, s77, v1
	s_and_b64 vcc, s[62:63], vcc
	v_max_f32_e32 v56, v4, v4
	v_cndmask_b32_e32 v9, v18, v57, vcc
	v_cmp_lt_i32_e32 vcc, s78, v1
	s_and_b64 vcc, s[44:45], vcc
	v_max_f32_e32 v12, v56, v12
	v_cndmask_b32_e32 v10, v18, v58, vcc
	v_cmp_lt_i32_e32 vcc, s79, v1
	s_and_b64 vcc, s[0:1], vcc
	v_max3_f32 v12, v12, v6, v7
	v_cndmask_b32_e32 v11, v18, v59, vcc
	v_cmp_lt_i32_e32 vcc, s80, v1
	s_and_b64 vcc, s[46:47], vcc
	v_max3_f32 v12, v12, v8, v9
	v_cndmask_b32_e32 v13, v18, v60, vcc
	v_cmp_lt_i32_e32 vcc, s81, v1
	s_and_b64 vcc, s[52:53], vcc
	v_max3_f32 v12, v12, v10, v11
	v_cndmask_b32_e32 v14, v18, v61, vcc
	v_cmp_lt_i32_e32 vcc, s82, v1
	s_and_b64 vcc, s[48:49], vcc
	v_max3_f32 v12, v12, v13, v14
	v_cndmask_b32_e32 v15, v18, v62, vcc
	v_cmp_lt_i32_e32 vcc, s83, v1
	s_and_b64 vcc, s[54:55], vcc
	s_nop 0
	v_cndmask_b32_e32 v52, v18, v63, vcc
	v_cmp_lt_i32_e32 vcc, s84, v1
	s_and_b64 vcc, s[50:51], vcc
	v_max3_f32 v12, v12, v15, v52
	v_cndmask_b32_e32 v53, v18, v64, vcc
	v_cmp_lt_i32_e32 vcc, s85, v1
	s_and_b64 vcc, s[56:57], vcc
	s_nop 0
	v_cndmask_b32_e32 v54, v18, v65, vcc
	v_cmp_lt_i32_e32 vcc, s86, v1
	s_and_b64 vcc, s[60:61], vcc
	v_max3_f32 v12, v12, v53, v54
	v_cndmask_b32_e32 v55, v18, v66, vcc
	v_cmp_lt_i32_e32 vcc, s87, v1
	s_and_b64 vcc, s[58:59], vcc
	s_nop 0
	v_cndmask_b32_e32 v1, v18, v67, vcc
	v_max3_f32 v12, v12, v55, v1
	v_mov_b32_e32 v56, v12
	s_nop 1
	v_permlane32_swap_b32_e32 v12, v56
	v_max3_f32 v12, v108, v12, v56
	v_sub_f32_e32 v4, v4, v12
	v_exp_f32_e32 v4, v4
	v_sub_f32_e32 v5, v5, v12
	v_exp_f32_e32 v5, v5
	v_sub_f32_e32 v6, v6, v12
	v_exp_f32_e32 v6, v6
	v_sub_f32_e32 v7, v7, v12
	v_exp_f32_e32 v7, v7
	v_sub_f32_e32 v8, v8, v12
	v_add_f32_e32 v57, 0, v4
	v_exp_f32_e32 v8, v8
	v_sub_f32_e32 v9, v9, v12
	v_add_f32_e32 v57, v5, v57
	v_exp_f32_e32 v9, v9
	v_sub_f32_e32 v10, v10, v12
	v_add_f32_e32 v57, v6, v57
	v_exp_f32_e32 v10, v10
	v_sub_f32_e32 v11, v11, v12
	v_add_f32_e32 v57, v7, v57
	v_exp_f32_e32 v11, v11
	v_sub_f32_e32 v13, v13, v12
	v_add_f32_e32 v57, v8, v57
	v_exp_f32_e32 v58, v13
	v_add_f32_e32 v57, v9, v57
	v_add_f32_e32 v57, v10, v57
	v_add_f32_e32 v57, v11, v57
	v_sub_f32_e32 v14, v14, v12
	v_add_f32_e32 v13, v58, v57
	v_exp_f32_e32 v57, v14
	v_sub_f32_e32 v14, v15, v12
	v_exp_f32_e32 v59, v14
	v_sub_f32_e32 v14, v52, v12
	v_exp_f32_e32 v52, v14
	v_sub_f32_e32 v14, v53, v12
	v_exp_f32_e32 v53, v14
	v_sub_f32_e32 v14, v54, v12
	v_add_f32_e32 v13, v57, v13
	v_exp_f32_e32 v54, v14
	v_sub_f32_e32 v14, v55, v12
	v_add_f32_e32 v13, v59, v13
	v_exp_f32_e32 v55, v14
	v_sub_f32_e32 v1, v1, v12
	v_add_f32_e32 v13, v52, v13
	v_exp_f32_e32 v1, v1
	v_add_f32_e32 v13, v53, v13
	v_add_f32_e32 v13, v54, v13
	v_sub_f32_e32 v56, v108, v12
	v_add_f32_e32 v13, v55, v13
	v_add_f32_e32 v14, v1, v13
	v_exp_f32_e32 v13, v56
	v_mov_b32_e32 v15, v14
	v_cvt_pk_bf16_f32 v4, v4, v5
	v_cvt_pk_bf16_f32 v5, v6, v7
	v_cvt_pk_bf16_f32 v6, v8, v9
	v_cvt_pk_bf16_f32 v7, v10, v11
	v_cvt_pk_bf16_f32 v8, v58, v57
	v_cvt_pk_bf16_f32 v9, v59, v52
	v_cvt_pk_bf16_f32 v10, v53, v54
	v_cvt_pk_bf16_f32 v11, v55, v1
	s_nop 1
	v_permlane32_swap_b32_e32 v14, v15
	v_permlane32_swap_b32_e32 v4, v6
	v_permlane32_swap_b32_e32 v5, v7
	v_permlane32_swap_b32_e32 v8, v10
	v_permlane32_swap_b32_e32 v9, v11
	v_cmp_gt_f32_e32 vcc, 1.0, v13
	s_cbranch_vccz .LBB0_1399
	s_and_saveexec_b64 s[0:1], s[6:7]
	s_mov_b64 s[86:87], 0x80
	ds_write_b32 v185, v13
	s_or_b64 exec, exec, s[0:1]
	ds_read_b128 v[52:55], v19 offset:96
	ds_read_b128 v[56:59], v19 offset:64
	ds_read_b128 v[60:63], v19 offset:32
	ds_read_b128 v[64:67], v19
	s_waitcnt lgkmcnt(0)
	v_pk_mul_f32 v[50:51], v[50:51], v[54:55]
	v_pk_mul_f32 v[46:47], v[46:47], v[58:59]
	v_pk_mul_f32 v[42:43], v[42:43], v[62:63]
	v_pk_mul_f32 v[38:39], v[38:39], v[66:67]
	v_pk_mul_f32 v[48:49], v[48:49], v[52:53]
	v_pk_mul_f32 v[44:45], v[44:45], v[56:57]
	v_pk_mul_f32 v[40:41], v[40:41], v[60:61]
	v_pk_mul_f32 v[36:37], v[36:37], v[64:65]
	v_pk_mul_f32 v[34:35], v[34:35], v[54:55]
	v_pk_mul_f32 v[30:31], v[30:31], v[58:59]
	v_pk_mul_f32 v[26:27], v[26:27], v[62:63]
	v_pk_mul_f32 v[22:23], v[22:23], v[66:67]
	v_pk_mul_f32 v[32:33], v[32:33], v[52:53]
	v_pk_mul_f32 v[28:29], v[28:29], v[56:57]
	v_pk_mul_f32 v[24:25], v[24:25], v[60:61]
	v_pk_mul_f32 v[20:21], v[20:21], v[64:65]
	s_branch .LBB0_1400
